# extends nt hint to remaining read-once loads (norm1 L1 rows+Y gathers, scan operands, attention Q, wout residual reads, norm2 rows, final)
# baseline (speedup 1.0000x reference)
.LBB0_256:
	s_add_u32 s4, s46, s29
	s_addc_u32 s5, s47, s52
	global_load_dwordx4 v[126:129], v1, s[4:5] nt
	v_lshl_add_u64 v[124:125], s[46:47], 0, v[88:89]
	v_add_co_u32_e32 v150, vcc, 0x11100000, v124
	v_lshl_add_u64 v[122:123], s[46:47], 0, v[86:87]
	s_nop 0
	v_addc_co_u32_e32 v151, vcc, 0, v125, vcc
	global_load_dwordx2 v[124:125], v[150:151], off nt
	s_mov_b32 s4, 0x3e000000
	v_add_co_u32_e64 v122, s[38:39], s80, v122
	s_add_i32 s25, s25, s66
	s_nop 0
	v_addc_co_u32_e64 v123, s[38:39], 0, v123, s[38:39]
	v_lshl_add_u64 v[86:87], v[86:87], 0, s[22:23]
	v_lshl_add_u64 v[88:89], v[88:89], 0, s[94:95]
	s_waitcnt vmcnt(1)
	v_readfirstlane_b32 s5, v126
	v_readfirstlane_b32 s6, v127
	s_nop 0
	v_pk_mul_f32 v[126:127], v[128:129], s[4:5] op_sel_hi:[1,0]
	s_lshr_b32 s4, s5, 18
	s_lshl_b32 s5, s5, 11
	s_lshr_b32 s7, s6, 18
	s_and_b32 s4, s4, 0x3ffc
	s_and_b32 s20, s5, 0x7ffff800
	s_and_b32 s5, s7, 0x3ffc
	s_add_i32 s4, s81, s4
	s_add_i32 s5, s81, s5
	v_mov_b32_e32 v128, s4
	v_mov_b32_e32 v129, s5
	ds_read_b32 v128, v128
	ds_read_b32 v130, v129
	s_lshl_b32 s6, s6, 11
	s_waitcnt lgkmcnt(1)
	v_ashrrev_i32_e32 v129, 31, v128
	v_lshlrev_b64 v[128:129], 19, v[128:129]
	v_lshl_add_u64 v[128:129], s[48:49], 0, v[128:129]
	v_lshl_add_u64 v[128:129], v[128:129], 0, s[20:21]
	s_waitcnt lgkmcnt(0)
	v_ashrrev_i32_e32 v131, 31, v130
	v_readfirstlane_b32 s4, v128
	v_readfirstlane_b32 s5, v129
	v_lshlrev_b64 v[130:131], 19, v[130:131]
	v_lshl_add_u64 v[130:131], s[48:49], 0, v[130:131]
	s_and_b32 s20, s6, 0x7ffff800
	v_lshl_add_u64 v[130:131], v[130:131], 0, s[20:21]
	s_add_u32 s29, s29, s68
	global_load_dword v129, v170, s[4:5] nt
	v_readfirstlane_b32 s6, v130
	v_readfirstlane_b32 s7, v131
	global_load_dword v131, v170, s[4:5] offset:256 nt
	global_load_dword v145, v170, s[4:5] offset:512 nt
	global_load_dword v154, v170, s[4:5] offset:768 nt
	global_load_dword v156, v170, s[4:5] offset:1024 nt
	global_load_dword v158, v170, s[4:5] offset:1280 nt
	global_load_dword v159, v170, s[4:5] offset:1536 nt
	global_load_dword v160, v170, s[4:5] offset:1792 nt
	global_load_dword v133, v170, s[6:7] nt
	global_load_dword v141, v170, s[6:7] offset:256 nt
	global_load_dword v149, v170, s[6:7] offset:512 nt
	global_load_dword v157, v170, s[6:7] offset:768 nt
	global_load_dword v161, v170, s[6:7] offset:1024 nt
	global_load_dword v162, v170, s[6:7] offset:1280 nt
	global_load_dword v163, v170, s[6:7] offset:1536 nt
	global_load_dword v171, v170, s[6:7] offset:1792 nt
	s_addc_u32 s52, s52, s69
	s_cmp_ge_i32 s25, s28
	s_waitcnt vmcnt(14)
	v_cvt_f32_fp8_e32 v136, v131
	v_cvt_f32_fp8_sdwa v138, v131 src0_sel:BYTE_1
	v_cvt_f32_fp8_sdwa v140, v131 src0_sel:BYTE_2
	v_cvt_f32_fp8_sdwa v142, v131 src0_sel:BYTE_3
	s_waitcnt vmcnt(13)
	v_cvt_f32_fp8_sdwa v146, v145 src0_sel:BYTE_1
	v_cvt_f32_fp8_e32 v144, v145
	v_cvt_f32_fp8_sdwa v148, v145 src0_sel:BYTE_2
	s_waitcnt vmcnt(7)
	v_cvt_f32_fp8_e32 v131, v133
	v_cvt_f32_fp8_sdwa v135, v133 src0_sel:BYTE_2
	s_waitcnt vmcnt(6)
	v_cvt_f32_fp8_e32 v139, v141
	v_cvt_f32_fp8_sdwa v137, v141 src0_sel:BYTE_1
	v_cvt_f32_fp8_sdwa v130, v129 src0_sel:BYTE_1
	v_cvt_f32_fp8_sdwa v134, v129 src0_sel:BYTE_3
	v_cvt_f32_fp8_e32 v128, v129
	v_cvt_f32_fp8_sdwa v132, v129 src0_sel:BYTE_2
	v_cvt_f32_fp8_sdwa v129, v133 src0_sel:BYTE_1
	v_cvt_f32_fp8_sdwa v133, v133 src0_sel:BYTE_3
	s_waitcnt vmcnt(5)
	v_cvt_f32_fp8_e32 v147, v149
	v_cvt_f32_fp8_sdwa v143, v141 src0_sel:BYTE_2
	v_cvt_f32_fp8_sdwa v152, v145 src0_sel:BYTE_3
	v_cvt_f32_fp8_sdwa v145, v149 src0_sel:BYTE_1
	v_cvt_f32_fp8_sdwa v141, v141 src0_sel:BYTE_3
	v_pk_mul_f32 v[130:131], v[126:127], v[130:131]
	v_pk_mul_f32 v[134:135], v[126:127], v[134:135]
	v_pk_mul_f32 v[138:139], v[126:127], v[138:139]
	v_pk_fma_f32 v[128:129], v[126:127], v[128:129], v[130:131] op_sel:[0,0,1] op_sel_hi:[1,1,0]
	v_cvt_f32_fp8_e32 v130, v154
	v_pk_fma_f32 v[132:133], v[126:127], v[132:133], v[134:135] op_sel:[0,0,1] op_sel_hi:[1,1,0]
	v_cvt_f32_fp8_sdwa v134, v154 src0_sel:BYTE_1
	v_pk_fma_f32 v[136:137], v[126:127], v[136:137], v[138:139] op_sel:[0,0,1] op_sel_hi:[1,1,0]
	v_cvt_f32_fp8_sdwa v138, v154 src0_sel:BYTE_2
	v_cvt_f32_fp8_sdwa v154, v154 src0_sel:BYTE_3
	s_waitcnt vmcnt(4)
	v_cvt_f32_fp8_sdwa v155, v157 src0_sel:BYTE_2
	v_pk_mul_f32 v[146:147], v[126:127], v[146:147]
	v_cvt_f32_fp8_e32 v135, v157
	v_cvt_f32_fp8_sdwa v139, v157 src0_sel:BYTE_3
	v_pk_mul_f32 v[142:143], v[126:127], v[142:143]
	v_pk_fma_f32 v[144:145], v[126:127], v[144:145], v[146:147] op_sel:[0,0,1] op_sel_hi:[1,1,0]
	v_cvt_f32_fp8_sdwa v146, v156 src0_sel:BYTE_1
	v_cvt_f32_fp8_sdwa v131, v157 src0_sel:BYTE_1
	s_waitcnt vmcnt(3)
	v_cvt_f32_fp8_e32 v147, v161
	v_cvt_f32_fp8_sdwa v153, v149 src0_sel:BYTE_2
	v_pk_fma_f32 v[140:141], v[126:127], v[140:141], v[142:143] op_sel:[0,0,1] op_sel_hi:[1,1,0]
	v_cvt_f32_fp8_e32 v142, v156
	v_cvt_f32_fp8_sdwa v143, v161 src0_sel:BYTE_1
	v_cvt_f32_fp8_sdwa v149, v149 src0_sel:BYTE_3
	v_pk_mul_f32 v[154:155], v[126:127], v[154:155]
	v_pk_mul_f32 v[134:135], v[126:127], v[134:135]
	v_pk_fma_f32 v[172:173], v[126:127], v[138:139], v[154:155] op_sel:[0,0,1] op_sel_hi:[1,1,0]
	v_cvt_f32_fp8_sdwa v138, v158 src0_sel:BYTE_1
	s_waitcnt vmcnt(2)
	v_cvt_f32_fp8_e32 v139, v162
	v_pk_fma_f32 v[134:135], v[126:127], v[130:131], v[134:135] op_sel:[0,0,1] op_sel_hi:[1,1,0]
	v_cvt_f32_fp8_e32 v130, v158
	v_pk_mul_f32 v[146:147], v[126:127], v[146:147]
	v_cvt_f32_fp8_sdwa v154, v158 src0_sel:BYTE_3
	v_cvt_f32_fp8_sdwa v131, v162 src0_sel:BYTE_1
	v_cvt_f32_fp8_sdwa v155, v162 src0_sel:BYTE_2
	v_pk_mul_f32 v[152:153], v[126:127], v[152:153]
	v_pk_fma_f32 v[146:147], v[126:127], v[142:143], v[146:147] op_sel:[0,0,1] op_sel_hi:[1,1,0]
	v_cvt_f32_fp8_sdwa v142, v158 src0_sel:BYTE_2
	v_cvt_f32_fp8_sdwa v143, v162 src0_sel:BYTE_3
	v_pk_fma_f32 v[148:149], v[126:127], v[148:149], v[152:153] op_sel:[0,0,1] op_sel_hi:[1,1,0]
	v_cvt_f32_fp8_sdwa v152, v156 src0_sel:BYTE_2
	v_cvt_f32_fp8_sdwa v156, v156 src0_sel:BYTE_3
	v_cvt_f32_fp8_sdwa v157, v161 src0_sel:BYTE_2
	v_cvt_f32_fp8_sdwa v153, v161 src0_sel:BYTE_3
	v_pk_mul_f32 v[138:139], v[126:127], v[138:139]
	v_pk_mul_f32 v[156:157], v[126:127], v[156:157]
	v_pk_fma_f32 v[176:177], v[126:127], v[130:131], v[138:139] op_sel:[0,0,1] op_sel_hi:[1,1,0]
	v_pk_mul_f32 v[138:139], v[126:127], v[154:155]
	v_cvt_f32_fp8_sdwa v130, v159 src0_sel:BYTE_1
	v_pk_fma_f32 v[178:179], v[126:127], v[142:143], v[138:139] op_sel:[0,0,1] op_sel_hi:[1,1,0]
	v_cvt_f32_fp8_sdwa v142, v159 src0_sel:BYTE_3
	s_waitcnt vmcnt(1)
	v_cvt_f32_fp8_sdwa v143, v163 src0_sel:BYTE_2
	v_cvt_f32_fp8_sdwa v138, v159 src0_sel:BYTE_2
	v_cvt_f32_fp8_e32 v131, v163
	v_cvt_f32_fp8_sdwa v139, v163 src0_sel:BYTE_3
	v_pk_fma_f32 v[174:175], v[126:127], v[152:153], v[156:157] op_sel:[0,0,1] op_sel_hi:[1,1,0]
	v_cvt_f32_fp8_e32 v152, v159
	v_cvt_f32_fp8_sdwa v153, v163 src0_sel:BYTE_1
	v_pk_mul_f32 v[142:143], v[126:127], v[142:143]
	v_pk_mul_f32 v[130:131], v[126:127], v[130:131]
	v_pk_fma_f32 v[180:181], v[126:127], v[138:139], v[142:143] op_sel:[0,0,1] op_sel_hi:[1,1,0]
	v_cvt_f32_fp8_sdwa v138, v160 src0_sel:BYTE_1
	s_waitcnt vmcnt(0)
	v_cvt_f32_fp8_e32 v139, v171
	v_pk_fma_f32 v[154:155], v[126:127], v[152:153], v[130:131] op_sel:[0,0,1] op_sel_hi:[1,1,0]
	v_cvt_f32_fp8_e32 v130, v160
	v_cvt_f32_fp8_sdwa v131, v171 src0_sel:BYTE_1
	v_pk_mul_f32 v[138:139], v[126:127], v[138:139]
	v_lshlrev_b32_e32 v142, 16, v124
	v_and_b32_e32 v143, 0xffff0000, v124
	v_pk_fma_f32 v[152:153], v[126:127], v[130:131], v[138:139] op_sel:[0,0,1] op_sel_hi:[1,1,0]
	v_cvt_f32_fp8_sdwa v138, v160 src0_sel:BYTE_3
	v_cvt_f32_fp8_sdwa v139, v171 src0_sel:BYTE_2
	v_cvt_f32_fp8_sdwa v130, v160 src0_sel:BYTE_2
	v_cvt_f32_fp8_sdwa v131, v171 src0_sel:BYTE_3
	v_lshlrev_b32_e32 v124, 16, v125
	v_pk_mul_f32 v[138:139], v[126:127], v[138:139]
	v_and_b32_e32 v125, 0xffff0000, v125
	v_pk_fma_f32 v[156:157], v[126:127], v[130:131], v[138:139] op_sel:[0,0,1] op_sel_hi:[1,1,0]
	global_load_dwordx2 v[126:127], v[150:151], off offset:512 nt
	global_load_dwordx2 v[130:131], v[150:151], off offset:1024 nt
	global_load_dwordx2 v[138:139], v[150:151], off offset:1536 nt
	v_pk_fma_f32 v[124:125], v[8:9], v[132:133], v[124:125]
	v_and_b32_e32 v171, 64, v226
	s_waitcnt vmcnt(2)
	v_lshlrev_b32_e32 v182, 16, v126
	v_and_b32_e32 v183, 0xffff0000, v126
	s_waitcnt vmcnt(0)
	v_lshlrev_b32_e32 v186, 16, v138
	v_and_b32_e32 v187, 0xffff0000, v138
	v_lshlrev_b32_e32 v188, 16, v139
	v_and_b32_e32 v189, 0xffff0000, v139
	global_load_dwordx2 v[138:139], v[150:151], off offset:2048 nt
	global_load_dwordx2 v[158:159], v[150:151], off offset:2560 nt
	global_load_dwordx2 v[160:161], v[150:151], off offset:3072 nt
	global_load_dwordx2 v[190:191], v[150:151], off offset:3584 nt
	v_lshlrev_b32_e32 v126, 16, v127
	v_and_b32_e32 v127, 0xffff0000, v127
	v_lshlrev_b32_e32 v184, 16, v130
	v_and_b32_e32 v185, 0xffff0000, v130
	v_lshlrev_b32_e32 v130, 16, v131
	v_and_b32_e32 v131, 0xffff0000, v131
	v_pk_fma_f32 v[126:127], v[16:17], v[140:141], v[126:127]
	v_pk_fma_f32 v[140:141], v[14:15], v[136:137], v[182:183]
	s_waitcnt vmcnt(3)
	v_lshlrev_b32_e32 v192, 16, v138
	s_waitcnt vmcnt(2)
	v_lshlrev_b32_e32 v196, 16, v158
	v_and_b32_e32 v197, 0xffff0000, v158
	v_lshlrev_b32_e32 v198, 16, v159
	v_and_b32_e32 v199, 0xffff0000, v159
	s_waitcnt vmcnt(0)
	v_lshlrev_b32_e32 v158, 16, v190
	v_and_b32_e32 v159, 0xffff0000, v190
	v_and_b32_e32 v193, 0xffff0000, v138
	v_lshlrev_b32_e32 v194, 16, v139
	v_and_b32_e32 v195, 0xffff0000, v139
	v_pk_fma_f32 v[138:139], v[6:7], v[128:129], v[142:143]
	v_pk_fma_f32 v[158:159], v[62:63], v[152:153], v[158:159]
	v_cvt_pk_bf16_f32 v152, v138, v139
	v_cvt_pk_bf16_f32 v153, v124, v125
	global_store_dwordx2 v[150:151], v[152:153], off
	v_cvt_pk_bf16_f32 v152, v140, v141
	v_cvt_pk_bf16_f32 v153, v126, v127
	v_pk_fma_f32 v[128:129], v[24:25], v[148:149], v[130:131]
	v_pk_fma_f32 v[142:143], v[22:23], v[144:145], v[184:185]
	global_store_dwordx2 v[150:151], v[152:153], off offset:512
	v_cvt_pk_bf16_f32 v152, v142, v143
	v_cvt_pk_bf16_f32 v153, v128, v129
	v_pk_fma_f32 v[130:131], v[32:33], v[172:173], v[188:189]
	v_pk_fma_f32 v[144:145], v[30:31], v[134:135], v[186:187]
	global_store_dwordx2 v[150:151], v[152:153], off offset:1024
	v_cvt_pk_bf16_f32 v152, v144, v145
	v_cvt_pk_bf16_f32 v153, v130, v131
	v_pk_fma_f32 v[132:133], v[40:41], v[174:175], v[194:195]
	v_pk_fma_f32 v[146:147], v[38:39], v[146:147], v[192:193]
	global_store_dwordx2 v[150:151], v[152:153], off offset:1536
	v_cvt_pk_bf16_f32 v152, v146, v147
	v_cvt_pk_bf16_f32 v153, v132, v133
	v_lshlrev_b32_e32 v162, 16, v160
	v_and_b32_e32 v163, 0xffff0000, v160
	v_lshlrev_b32_e32 v200, 16, v161
	v_and_b32_e32 v201, 0xffff0000, v161
	v_lshlrev_b32_e32 v160, 16, v191
	v_and_b32_e32 v161, 0xffff0000, v191
	v_pk_fma_f32 v[134:135], v[48:49], v[178:179], v[198:199]
	v_pk_fma_f32 v[148:149], v[46:47], v[176:177], v[196:197]
	global_store_dwordx2 v[150:151], v[152:153], off offset:2048
	v_cvt_pk_bf16_f32 v152, v148, v149
	v_cvt_pk_bf16_f32 v153, v134, v135
	v_pk_fma_f32 v[136:137], v[56:57], v[180:181], v[200:201]
	v_pk_fma_f32 v[154:155], v[54:55], v[154:155], v[162:163]
	v_xor_b32_e32 v163, 1, v226
	v_xor_b32_e32 v172, 2, v226
	v_pk_fma_f32 v[156:157], v[64:65], v[156:157], v[160:161]
	v_xor_b32_e32 v173, 4, v226
	v_xor_b32_e32 v174, 8, v226
	v_add_u32_e32 v160, 64, v171
	global_store_dwordx2 v[150:151], v[152:153], off offset:2560
	v_cvt_pk_bf16_f32 v152, v154, v155
	v_cvt_pk_bf16_f32 v153, v136, v137
	v_cmp_lt_i32_e32 vcc, v163, v160
	v_cmp_lt_i32_e64 s[38:39], v172, v160
	v_cmp_lt_i32_e64 s[40:41], v173, v160
	v_cmp_lt_i32_e64 s[42:43], v174, v160
	v_mul_f32_e32 v160, v139, v139
	global_store_dwordx2 v[150:151], v[152:153], off offset:3072
	v_cvt_pk_bf16_f32 v152, v158, v159
	v_cvt_pk_bf16_f32 v153, v156, v157
	global_store_dwordx2 v[150:151], v[152:153], off offset:3584
	v_mul_f32_e32 v150, v125, v125
	v_fmac_f32_e32 v160, v138, v138
	v_fmac_f32_e32 v150, v124, v124
	v_mul_f32_e32 v151, v141, v141
	v_mul_f32_e32 v152, v127, v127
	v_mul_f32_e32 v153, v143, v143
	v_add_f32_e32 v150, v160, v150
	v_mul_f32_e32 v160, v129, v129
	v_fmac_f32_e32 v151, v140, v140
	v_fmac_f32_e32 v152, v126, v126
	v_fmac_f32_e32 v153, v142, v142
	v_fmac_f32_e32 v160, v128, v128
	v_add_f32_e32 v151, v151, v152
	v_mul_f32_e32 v152, v145, v145
	v_add_f32_e32 v153, v153, v160
	v_mul_f32_e32 v160, v131, v131
	v_fmac_f32_e32 v152, v144, v144
	v_fmac_f32_e32 v160, v130, v130
	v_add_f32_e32 v152, v152, v160
	v_mul_f32_e32 v160, v147, v147
	v_mul_f32_e32 v161, v133, v133
	v_fmac_f32_e32 v160, v146, v146
	v_fmac_f32_e32 v161, v132, v132
	v_add_f32_e32 v160, v160, v161
	v_mul_f32_e32 v161, v149, v149
	v_mul_f32_e32 v162, v135, v135
	v_fmac_f32_e32 v161, v148, v148
	v_fmac_f32_e32 v162, v134, v134
	v_add_f32_e32 v150, v150, v151
	v_add_f32_e32 v161, v161, v162
	v_mul_f32_e32 v162, v155, v155
	v_mul_f32_e32 v171, v137, v137
	v_add_f32_e32 v150, v150, v153
	v_fmac_f32_e32 v162, v154, v154
	v_fmac_f32_e32 v171, v136, v136
	v_add_f32_e32 v150, v150, v152
	v_add_f32_e32 v162, v162, v171
	v_mul_f32_e32 v171, v159, v159
	v_mul_f32_e32 v175, v157, v157
	v_add_f32_e32 v150, v150, v160
	v_fmac_f32_e32 v171, v158, v158
	v_fmac_f32_e32 v175, v156, v156
	v_add_f32_e32 v150, v150, v161
	v_add_f32_e32 v171, v171, v175
	v_add_f32_e32 v150, v150, v162
	v_cndmask_b32_e32 v151, v226, v163, vcc
	v_lshlrev_b32_e32 v151, 2, v151
	v_add_f32_e32 v150, v150, v171
	ds_bpermute_b32 v151, v151, v150
	v_cndmask_b32_e64 v152, v226, v172, s[38:39]
	v_lshlrev_b32_e32 v152, 2, v152
	v_cndmask_b32_e64 v153, v226, v173, s[40:41]
	v_lshlrev_b32_e32 v153, 2, v153
	s_waitcnt lgkmcnt(0)
	v_add_f32_e32 v150, v150, v151
	ds_bpermute_b32 v151, v152, v150
	v_cndmask_b32_e64 v163, v226, v174, s[42:43]
	v_lshlrev_b32_e32 v163, 2, v163
	v_mov_b32_e32 v160, 0
	v_mov_b32_e32 v161, 0
	s_waitcnt lgkmcnt(0)
	v_add_f32_e32 v150, v150, v151
	ds_bpermute_b32 v151, v153, v150
	v_mov_b32_e32 v162, 0
	v_mov_b32_e32 v173, 0
	s_waitcnt lgkmcnt(0)
	v_add_f32_e32 v150, v150, v151
	ds_bpermute_b32 v151, v163, v150
	s_waitcnt lgkmcnt(0)
	v_add_f32_e32 v150, v150, v151
	v_mov_b32_e32 v151, v150
	s_nop 1
	v_permlane16_swap_b32_e32 v150, v151
	v_add_f32_e32 v150, v150, v151
	v_mov_b32_e32 v151, v150
	s_nop 1
	v_permlane32_swap_b32_e32 v150, v151
	v_add_f32_e32 v150, v150, v151
	v_fmamk_f32 v150, v150, 0x3a000000, v228
	v_mul_f32_e32 v151, 0x4f800000, v150
	v_cmp_gt_f32_e32 vcc, s82, v150
	s_nop 1
	v_cndmask_b32_e32 v150, v150, v151, vcc
	v_sqrt_f32_e32 v151, v150
	s_nop 0
	v_add_u32_e32 v152, -1, v151
	v_add_u32_e32 v153, 1, v151
	v_fma_f32 v163, -v152, v151, v150
	v_fma_f32 v171, -v153, v151, v150
	v_cmp_ge_f32_e64 s[38:39], 0, v163
	s_nop 1
	v_cndmask_b32_e64 v151, v151, v152, s[38:39]
	v_cmp_lt_f32_e64 s[38:39], 0, v171
	v_mov_b32_e32 v171, 0
	s_nop 0
	v_cndmask_b32_e64 v151, v151, v153, s[38:39]
	v_mul_f32_e32 v152, 0x37800000, v151
	v_cndmask_b32_e32 v151, v151, v152, vcc
	v_cmp_class_f32_e32 vcc, v150, v229
	s_nop 1
	v_cndmask_b32_e32 v150, v151, v150, vcc
	v_div_scale_f32 v151, s[4:5], v150, v150, 1.0
	v_rcp_f32_e32 v153, v151
	v_div_scale_f32 v152, vcc, 1.0, v150, 1.0
	v_fma_f32 v163, -v151, v153, 1.0
	v_fmac_f32_e32 v153, v163, v153
	v_mul_f32_e32 v172, v152, v153
	v_fma_f32 v163, -v151, v172, v152
	v_fmac_f32_e32 v172, v163, v153
	v_fma_f32 v151, -v151, v172, v152
	v_div_fmas_f32 v151, v151, v153, v172
	v_div_fixup_f32 v174, v151, v150, 1.0
	v_pk_mul_f32 v[138:139], v[138:139], v[174:175] op_sel_hi:[1,0]
	v_pk_mul_f32 v[150:151], v[124:125], v[174:175] op_sel_hi:[1,0]
	v_pk_mul_f32 v[124:125], v[140:141], v[174:175] op_sel_hi:[1,0]
	v_pk_fma_f32 v[138:139], v[92:93], v[138:139], v[2:3]
	v_pk_mul_f32 v[140:141], v[126:127], v[174:175] op_sel_hi:[1,0]
	v_pk_mul_f32 v[126:127], v[142:143], v[174:175] op_sel_hi:[1,0]
	v_pk_fma_f32 v[124:125], v[96:97], v[124:125], v[10:11]
	v_med3_f32 v138, v138, s33, v233
	v_med3_f32 v139, v139, s33, v233
	v_pk_mul_f32 v[142:143], v[128:129], v[174:175] op_sel_hi:[1,0]
	v_pk_mul_f32 v[128:129], v[144:145], v[174:175] op_sel_hi:[1,0]
	v_pk_fma_f32 v[126:127], v[100:101], v[126:127], v[18:19]
	v_med3_f32 v124, v124, s33, v233
	v_med3_f32 v125, v125, s33, v233
	v_cvt_pk_fp8_f32 v160, v138, v139
	v_pk_mul_f32 v[144:145], v[130:131], v[174:175] op_sel_hi:[1,0]
	v_pk_mul_f32 v[130:131], v[146:147], v[174:175] op_sel_hi:[1,0]
	v_pk_mul_f32 v[146:147], v[132:133], v[174:175] op_sel_hi:[1,0]
	v_pk_mul_f32 v[132:133], v[148:149], v[174:175] op_sel_hi:[1,0]
	v_pk_mul_f32 v[148:149], v[134:135], v[174:175] op_sel_hi:[1,0]
	v_pk_mul_f32 v[134:135], v[154:155], v[174:175] op_sel_hi:[1,0]
	v_pk_mul_f32 v[152:153], v[136:137], v[174:175] op_sel_hi:[1,0]
	v_pk_mul_f32 v[136:137], v[158:159], v[174:175] op_sel_hi:[1,0]
	v_pk_fma_f32 v[128:129], v[104:105], v[128:129], v[26:27]
	v_med3_f32 v126, v126, s33, v233
	v_med3_f32 v127, v127, s33, v233
	v_cvt_pk_fp8_f32 v161, v124, v125
	v_mov_b32_e32 v163, 0
	v_pk_fma_f32 v[150:151], v[90:91], v[150:151], v[4:5]
	v_pk_fma_f32 v[130:131], v[108:109], v[130:131], v[34:35]
	v_pk_fma_f32 v[132:133], v[112:113], v[132:133], v[42:43]
	v_pk_fma_f32 v[134:135], v[116:117], v[134:135], v[50:51]
	v_pk_fma_f32 v[136:137], v[120:121], v[136:137], v[58:59]
	v_med3_f32 v128, v128, s33, v233
	v_med3_f32 v129, v129, s33, v233
	v_cvt_pk_fp8_f32 v162, v126, v127
	v_mov_b32_e32 v172, 0
	v_pk_mul_f32 v[154:155], v[156:157], v[174:175] op_sel_hi:[1,0]
	v_mov_b32_e32 v156, 0
	v_pk_fma_f32 v[140:141], v[94:95], v[140:141], v[12:13]
	v_med3_f32 v150, v150, s33, v233
	v_med3_f32 v151, v151, s33, v233
	v_med3_f32 v130, v130, s33, v233
	v_med3_f32 v131, v131, s33, v233
	v_med3_f32 v132, v132, s33, v233
	v_med3_f32 v133, v133, s33, v233
	v_med3_f32 v134, v134, s33, v233
	v_med3_f32 v135, v135, s33, v233
	v_med3_f32 v136, v136, s33, v233
	v_med3_f32 v137, v137, s33, v233
	v_cvt_pk_fp8_f32 v163, v128, v129
	v_pk_fma_f32 v[142:143], v[98:99], v[142:143], v[20:21]
	v_med3_f32 v140, v140, s33, v233
	v_med3_f32 v141, v141, s33, v233
	v_cvt_pk_fp8_f32 v171, v130, v131
	v_cvt_pk_fp8_f32 v172, v132, v133
	v_cvt_pk_fp8_f32 v173, v134, v135
	v_cvt_pk_fp8_f32 v156, v136, v137
	v_cvt_pk_fp8_f32 v160, v150, v151 op_sel:[0,0,1]
	v_pk_fma_f32 v[144:145], v[102:103], v[144:145], v[28:29]
	v_med3_f32 v142, v142, s33, v233
	v_med3_f32 v143, v143, s33, v233
	v_cvt_pk_fp8_f32 v161, v140, v141 op_sel:[0,0,1]
	v_pk_fma_f32 v[146:147], v[106:107], v[146:147], v[36:37]
	v_pk_fma_f32 v[148:149], v[110:111], v[148:149], v[44:45]
	v_pk_fma_f32 v[152:153], v[114:115], v[152:153], v[52:53]
	v_pk_fma_f32 v[154:155], v[118:119], v[154:155], v[60:61]
	v_med3_f32 v144, v144, s33, v233
	v_med3_f32 v145, v145, s33, v233
	v_cvt_pk_fp8_f32 v162, v142, v143 op_sel:[0,0,1]
	v_med3_f32 v146, v146, s33, v233
	v_med3_f32 v147, v147, s33, v233
	v_med3_f32 v148, v148, s33, v233
	v_med3_f32 v149, v149, s33, v233
	v_med3_f32 v152, v152, s33, v233
	v_med3_f32 v153, v153, s33, v233
	v_med3_f32 v154, v154, s33, v233
	v_med3_f32 v155, v155, s33, v233
	v_cvt_pk_fp8_f32 v163, v144, v145 op_sel:[0,0,1]
	v_cvt_pk_fp8_f32 v171, v146, v147 op_sel:[0,0,1]
	v_cvt_pk_fp8_f32 v172, v148, v149 op_sel:[0,0,1]
	v_cvt_pk_fp8_f32 v173, v152, v153 op_sel:[0,0,1]
	v_cvt_pk_fp8_f32 v156, v154, v155 op_sel:[0,0,1]
	global_store_dword v[122:123], v160, off
	global_store_dword v[122:123], v161, off offset:256
	global_store_dword v[122:123], v162, off offset:512
	global_store_dword v[122:123], v163, off offset:768
	global_store_dword v[122:123], v171, off offset:1024
	global_store_dword v[122:123], v172, off offset:1280
	global_store_dword v[122:123], v173, off offset:1536
	global_store_dword v[122:123], v156, off offset:1792
	s_cbranch_scc0 .LBB0_256
	s_branch .LBB0_253

.LBB0_948:
	s_cmp_lt_u32 s67, 64
	s_cselect_b64 vcc, -1, 0
	v_cndmask_b32_e32 v0, v130, v126, vcc
	v_or_b32_e32 v4, s20, v0
	v_cndmask_b32_e32 v0, v131, v132, vcc
	v_or_b32_e32 v6, s20, v0
	v_lshlrev_b32_e32 v0, 13, v4
	v_lshl_add_u64 v[2:3], s[86:87], 0, v[0:1]
	s_lshl_b32 s8, s12, 7
	s_mov_b32 s9, s21
	v_lshl_add_u64 v[2:3], v[2:3], 0, s[8:9]
	v_mov_b32_e32 v115, v1
	v_lshlrev_b32_e32 v0, 13, v6
	v_lshl_add_u64 v[18:19], v[2:3], 0, v[114:115]
	v_lshl_add_u64 v[2:3], s[86:87], 0, v[0:1]
	v_lshl_add_u64 v[2:3], v[2:3], 0, s[8:9]
	v_lshl_add_u64 v[22:23], v[2:3], 0, v[114:115]
	v_mov_b64_e32 v[2:3], s[88:89]
	s_movk_i32 s5, 0x2800
	v_mad_u64_u32 v[4:5], s[6:7], v4, s5, v[2:3]
	s_lshl_b32 s6, s4, 10
	s_ashr_i32 s7, s6, 31
	s_lshl_b64 s[10:11], s[6:7], 1
	v_mad_u64_u32 v[2:3], s[60:61], v6, s5, v[2:3]
	v_lshl_add_u64 v[4:5], v[4:5], 0, s[10:11]
	v_lshl_add_u64 v[2:3], v[2:3], 0, s[10:11]
	s_movk_i32 s5, 0x1000
	v_lshl_add_u64 v[4:5], v[4:5], 0, s[8:9]
	v_lshl_add_u64 v[2:3], v[2:3], 0, s[8:9]
	v_add_co_u32_e32 v10, vcc, s5, v18
	v_lshl_add_u64 v[20:21], v[4:5], 0, v[114:115]
	v_lshl_add_u64 v[24:25], v[2:3], 0, v[114:115]
	v_addc_co_u32_e32 v11, vcc, 0, v19, vcc
	global_load_dwordx4 v[2:5], v[20:21], off nt
	global_load_dwordx4 v[6:9], v[24:25], off nt
	v_add_co_u32_e32 v14, vcc, s5, v22
	v_lshl_add_u64 v[20:21], v[20:21], 0, s[14:15]
	v_lshl_add_u64 v[24:25], v[24:25], 0, s[14:15]
	v_addc_co_u32_e32 v15, vcc, 0, v23, vcc
	v_cndmask_b32_e64 v27, v25, v23, s[38:39]
	v_cndmask_b32_e64 v26, v24, v22, s[38:39]
	v_cndmask_b32_e64 v25, v21, v19, s[38:39]
	v_cndmask_b32_e64 v24, v20, v18, s[38:39]
	v_lshl_add_u64 v[18:19], v[18:19], 0, s[92:93]
	v_lshl_add_u64 v[30:31], v[22:23], 0, s[92:93]
	global_load_dwordx4 v[10:13], v[10:11], off offset:2048 nt
	s_nop 0
	global_load_dwordx4 v[14:17], v[14:15], off offset:2048 nt
	s_lshl_b32 s8, s12, 6
	global_load_dwordx4 v[18:21], v[18:19], off nt
	s_nop 0
	global_load_dwordx4 v[22:25], v[24:25], off nt
	s_nop 0
	global_load_dwordx4 v[26:29], v[26:27], off nt
	s_nop 0
	global_load_dwordx4 v[30:33], v[30:31], off nt
	s_waitcnt vmcnt(0)
	s_waitcnt vmcnt(7)
	ds_write_b128 v151, v[2:5]
	s_waitcnt vmcnt(6)
	ds_write_b128 v151, v[6:9] offset:1024
	s_waitcnt vmcnt(5)
	ds_write_b128 v151, v[10:13] offset:2048
	s_waitcnt vmcnt(3)
	ds_write_b128 v151, v[18:21] offset:6144
	ds_write_b128 v151, v[14:17] offset:3072
	s_waitcnt vmcnt(2)
	ds_write_b128 v151, v[22:25] offset:4096
	s_waitcnt vmcnt(1)
	ds_write_b128 v151, v[26:29] offset:5120
	s_waitcnt vmcnt(0)
	ds_write_b128 v151, v[30:33] offset:7168
	s_waitcnt lgkmcnt(0)

.LBB0_964:
	s_andn2_b64 vcc, exec, s[10:11]
	s_cbranch_vccnz .LBB0_967
	s_cmpk_gt_u32 s84, 0xfe
	s_cbranch_scc1 .LBB0_967
	v_add_u32_e32 v2, s70, v126
	v_add_u32_e32 v0, 16, v2
	v_add_u32_e32 v2, 24, v2
	v_cndmask_b32_e64 v0, v115, v0, s[60:61]
	v_cndmask_b32_e64 v2, v117, v2, s[60:61]
	v_add_u32_e32 v0, s20, v0
	v_add_u32_e32 v2, s20, v2
	s_movk_i32 s12, 0x2800
	v_lshlrev_b64 v[4:5], 13, v[0:1]
	v_mad_u64_u32 v[56:57], s[10:11], v0, s12, v[120:121]
	v_mad_u64_u32 v[58:59], s[10:11], v2, s12, v[120:121]
	v_mov_b32_e32 v3, v1
	v_lshl_add_u64 v[14:15], v[118:119], 0, v[4:5]
	s_movk_i32 s10, 0x1000
	v_lshlrev_b64 v[4:5], 13, v[2:3]
	v_add_co_u32_e32 v10, vcc, s10, v14
	v_lshl_add_u64 v[64:65], v[118:119], 0, v[4:5]
	s_nop 0
	v_addc_co_u32_e32 v11, vcc, 0, v15, vcc
	v_add_co_u32_e32 v48, vcc, s10, v64
	global_load_dwordx4 v[2:5], v[56:57], off nt
	global_load_dwordx4 v[6:9], v[58:59], off nt
	v_addc_co_u32_e32 v49, vcc, 0, v65, vcc
	global_load_dwordx4 v[10:13], v[10:11], off offset:2048 nt
	s_nop 0
	global_load_dwordx4 v[48:51], v[48:49], off offset:2048 nt
	s_nop 0
	global_load_dwordx4 v[52:55], v[14:15], off offset:2048 nt
	v_add_co_u32_e32 v14, vcc, s10, v58
	s_nop 1
	v_addc_co_u32_e32 v15, vcc, 0, v59, vcc
	v_add_co_u32_e32 v60, vcc, 0x1000, v56
	s_nop 1
	v_addc_co_u32_e32 v61, vcc, 0, v57, vcc
	global_load_dwordx4 v[56:59], v[14:15], off nt
	s_nop 0
	global_load_dwordx4 v[60:63], v[60:61], off nt
	s_nop 0
	global_load_dwordx4 v[64:67], v[64:65], off offset:2048 nt
	s_waitcnt vmcnt(0)
	s_waitcnt vmcnt(7)
	ds_write_b128 v151, v[2:5]
	s_waitcnt vmcnt(6)
	ds_write_b128 v151, v[6:9] offset:1024
	s_waitcnt vmcnt(3)
	ds_write_b128 v151, v[52:55] offset:6144
	ds_write_b128 v151, v[10:13] offset:2048
	ds_write_b128 v151, v[48:51] offset:3072
	s_waitcnt vmcnt(2)
	ds_write_b128 v151, v[56:59] offset:5120
	s_waitcnt vmcnt(1)
	ds_write_b128 v151, v[60:63] offset:4096
	s_waitcnt vmcnt(0)
	ds_write_b128 v151, v[64:67] offset:7168
	s_waitcnt lgkmcnt(0)

.LBB0_978:
	s_andn2_b64 vcc, exec, s[8:9]
	s_cbranch_vccnz .LBB0_981
	s_cmpk_gt_u32 s84, 0xfe
	s_cbranch_scc1 .LBB0_981
	v_add_u32_e32 v2, s70, v126
	v_add_u32_e32 v0, 16, v2
	v_cndmask_b32_e64 v0, v115, v0, s[60:61]
	v_add_u32_e32 v2, 24, v2
	v_add_u32_e32 v0, s20, v0
	v_cndmask_b32_e64 v2, v117, v2, s[60:61]
	v_add_u32_e32 v2, s20, v2
	v_mov_b32_e32 v3, v1
	v_lshlrev_b64 v[4:5], 13, v[0:1]
	v_lshl_add_u64 v[14:15], v[118:119], 0, v[4:5]
	v_lshlrev_b64 v[4:5], 13, v[2:3]
	s_movk_i32 s12, 0x2800
	v_lshl_add_u64 v[56:57], v[118:119], 0, v[4:5]
	v_mad_u64_u32 v[4:5], s[8:9], v0, s12, v[120:121]
	v_mad_u64_u32 v[6:7], s[8:9], v2, s12, v[120:121]
	s_movk_i32 s8, 0x1000
	s_nop 0
	v_add_co_u32_e32 v60, vcc, s8, v14
	global_load_dwordx4 v[2:5], v[4:5], off nt
	s_nop 0
	global_load_dwordx4 v[6:9], v[6:7], off nt
	v_addc_co_u32_e32 v61, vcc, 0, v15, vcc
	global_load_dwordx4 v[10:13], v[60:61], off offset:2048 nt
	global_load_dwordx4 v[48:51], v[56:57], off nt
	global_load_dwordx4 v[52:55], v[14:15], off nt
	v_add_co_u32_e32 v14, vcc, s8, v56
	s_nop 1
	v_addc_co_u32_e32 v15, vcc, 0, v57, vcc
	global_load_dwordx4 v[56:59], v[14:15], off offset:2048 nt
	s_nop 0
	global_load_dwordx4 v[60:63], v[60:61], off nt
	s_nop 0
	global_load_dwordx4 v[64:67], v[14:15], off nt
	s_waitcnt vmcnt(0)
	s_waitcnt vmcnt(7)
	ds_write_b128 v151, v[2:5]
	s_waitcnt vmcnt(6)
	ds_write_b128 v151, v[6:9] offset:1024
	s_waitcnt vmcnt(3)
	ds_write_b128 v151, v[52:55] offset:4096
	ds_write_b128 v151, v[48:51] offset:5120
	ds_write_b128 v151, v[10:13] offset:2048
	s_waitcnt vmcnt(2)
	ds_write_b128 v151, v[56:59] offset:3072
	s_waitcnt vmcnt(1)
	ds_write_b128 v151, v[60:63] offset:6144
	s_waitcnt vmcnt(0)
	ds_write_b128 v151, v[64:67] offset:7168
	s_waitcnt lgkmcnt(0)

.LBB0_1026:
	s_or_b64 exec, exec, s[4:5]
	v_mov_b32_e32 v2, s2
	s_waitcnt lgkmcnt(0)
	s_barrier
	ds_read_b32 v2, v2
	s_mov_b64 s[4:5], -1
	s_waitcnt lgkmcnt(0)
	s_barrier
	v_readfirstlane_b32 s7, v2
	s_cmpk_gt_i32 s7, 0x7f
	s_cbranch_scc1 .LBB0_1021
	s_ashr_i32 s6, s7, 5
	s_add_i32 s8, s6, s28
	s_ashr_i32 s4, s8, 3
	s_ashr_i32 s5, s4, 31
	s_lshl_b64 s[90:91], s[4:5], 12
	s_lshl_b32 s5, s7, 7
	s_and_b32 s5, s5, 0xf80
	s_or_b32 s90, s90, s5
	s_mul_i32 s5, s91, 0x3400
	s_mul_hi_u32 s7, s90, 0x3400
	s_add_i32 s7, s7, s5
	s_mul_i32 s5, s90, 0x3400
	s_add_u32 s5, s13, s5
	s_addc_u32 s7, s94, s7
	s_lshl_b32 s8, s8, 7
	s_and_b32 s29, s8, 0x380
	s_lshl_b32 s10, s29, 1
	s_add_u32 s8, s5, s10
	s_addc_u32 s9, s7, 0
	s_mul_i32 s11, s4, 0x3400000
	s_mul_hi_i32 s7, s4, 0x3400000
	s_add_u32 s4, s13, s11
	s_addc_u32 s5, s94, s7
	s_add_u32 s4, s4, s10
	v_readfirstlane_b32 s10, v238
	s_addc_u32 s5, s5, 0
	s_ashr_i32 s20, s10, 6
	v_lshl_or_b32 v6, s20, 3, v241
	v_mov_b64_e32 v[2:3], s[4:5]
	v_mad_i64_i32 v[4:5], s[44:45], v6, s83, v[2:3]
	v_lshl_add_u64 v[50:51], v[4:5], 0, v[0:1]
	v_or_b32_e32 v4, 4, v6
	s_and_b32 s24, s20, 1
	v_mad_i64_i32 v[2:3], s[44:45], v4, s83, v[2:3]
	v_mov_b32_e32 v205, v1
	s_ashr_i32 s25, s10, 7
	v_lshl_add_u64 v[54:55], v[2:3], 0, v[204:205]
	v_lshl_or_b32 v2, s24, 5, v242
	s_mov_b32 s72, s88
	v_mul_u32_u24_e32 v2, 0x1a00, v2
	s_lshl_b32 s88, s25, 5
	v_lshlrev_b32_e32 v52, 1, v2
	v_mov_b32_e32 v53, v1
	s_ashr_i32 s89, s88, 31
	s_and_b32 s71, s10, 0x3fffffc0
	v_lshl_add_u64 v[2:3], s[4:5], 0, v[52:53]
	s_lshl_b64 s[4:5], s[88:89], 1
	s_lshl_b32 s89, s20, 11
	s_cmp_lg_u32 0, -1
	s_cselect_b32 s10, 0, 0
	s_lshl_b32 s25, s25, 12
	v_lshl_add_u64 v[2:3], v[2:3], 0, s[4:5]
	v_mov_b32_e32 v207, v1
	s_add_i32 s89, s89, s10
	s_add_i32 s10, s10, s25
	s_lshl_b32 s20, s24, 11
	s_load_dwordx2 s[92:93], s[60:61], 0xc0
	v_lshl_add_u64 v[214:215], v[50:51], 0, s[30:31]
	v_lshl_add_u64 v[56:57], v[2:3], 0, v[206:207]
	s_add_i32 s70, s10, s20
	s_mov_b32 s10, m0
	s_mov_b32 m0, s89
	s_nop 0
	global_load_lds_dwordx4 v[214:215], off
	s_mov_b32 m0, s10
	s_add_i32 vcc_lo, s89, 0x400
	v_lshl_add_u64 v[216:217], v[54:55], 0, s[30:31]
	v_lshl_add_u64 v[2:3], v[56:57], 0, s[14:15]
	s_mov_b32 s10, m0
	s_mov_b32 m0, vcc_lo
	s_nop 0
	global_load_lds_dwordx4 v[216:217], off
	s_mov_b32 m0, s10
	s_mov_b64 s[44:45], 0x35000
	s_add_i32 s70, s70, 0xc000
	s_mov_b32 s10, m0
	s_mov_b32 m0, s70
	s_nop 0
	global_load_lds_dwordx4 v[2:3], off
	s_mov_b32 m0, s10
	v_lshl_add_u64 v[2:3], v[56:57], 0, s[44:45]
	s_add_i32 s10, s70, 0x400
	s_mov_b32 s44, m0
	s_mov_b32 m0, s10
	s_nop 0
	global_load_lds_dwordx4 v[2:3], off
	s_mov_b32 m0, s44
	v_lshl_add_u64 v[2:3], v[50:51], 0, s[34:35]
	s_add_i32 s10, s89, 0x4000
	s_mov_b32 s44, m0
	s_mov_b32 m0, s10
	s_nop 0
	global_load_lds_dwordx4 v[2:3], off
	s_mov_b32 m0, s44
	v_lshl_add_u64 v[2:3], v[54:55], 0, s[34:35]
	s_add_i32 s10, s89, 0x4400
	s_mov_b32 s44, m0
	s_mov_b32 m0, s10
	s_nop 0
	global_load_lds_dwordx4 v[2:3], off
	s_mov_b32 m0, s44
	v_or_b32_e32 v4, s88, v240
	v_mov_b64_e32 v[2:3], s[8:9]
	s_lshl_b32 s20, s24, 7
	v_mad_i64_i32 v[2:3], s[8:9], v4, s83, v[2:3]
	v_lshl_add_u64 v[2:3], v[2:3], 0, s[20:21]
	v_mov_b32_e32 v209, v1
	v_lshl_add_u64 v[2:3], v[2:3], 0, v[208:209]
	global_load_dwordx4 v[158:161], v[2:3], off nt
	global_load_dwordx4 v[154:157], v[2:3], off offset:32 nt
	global_load_dwordx4 v[146:149], v[2:3], off offset:64 nt
	global_load_dwordx4 v[142:145], v[2:3], off offset:96 nt
	v_lshl_add_u64 v[2:3], v[50:51], 0, s[36:37]
	v_or_b32_e32 v6, s20, v245
	s_add_i32 s8, s89, 0x8000
	s_mov_b32 s10, m0
	s_mov_b32 m0, s8
	s_nop 0
	global_load_lds_dwordx4 v[2:3], off
	s_mov_b32 m0, s10
	v_lshl_add_u64 v[4:5], v[54:55], 0, s[36:37]
	v_bitop3_b32 v209, v6, v247, v246 bitop3:0xde
	s_add_i32 s9, s89, 0x8400
	s_mov_b32 s8, m0
	s_mov_b32 m0, s9
	s_nop 0
	global_load_lds_dwordx4 v[4:5], off
	s_mov_b32 m0, s8
	v_add_u32_e32 v211, 0, v209
	s_waitcnt vmcnt(6) lgkmcnt(0)
	s_barrier
	ds_read_b128 v[2:5], v211
	ds_read_b128 v[6:9], v211 offset:8192
	v_bitop3_b32 v10, s20, v246, v245 bitop3:0x36
	v_bitop3_b32 v213, v10, 32, v247 bitop3:0x36
	v_add_u32_e32 v250, 0, v213
	v_bitop3_b32 v251, v10, 64, v247 bitop3:0x36
	v_add_u32_e32 v252, 0, v251
	s_movk_i32 s20, 0x60
	v_bitop3_b32 v235, v10, s20, v247 bitop3:0x36
	v_add_u32_e32 v227, 0, v235
	s_mov_b32 s44, 0
	s_mov_b32 s45, s44
	s_mov_b32 s46, s44
	s_mov_b32 s47, s44
	s_mov_b32 s48, s44
	s_mov_b32 s49, s44
	s_mov_b32 s50, s44
	s_mov_b32 s51, s44
	s_mov_b32 s52, s44
	s_waitcnt vmcnt(3) lgkmcnt(0)
	v_mfma_f32_32x32x16_bf16 v[18:33], v[2:5], v[158:161], 0
	s_mov_b32 s53, s44
	s_mov_b32 s54, s44
	s_mov_b32 s55, s44
	s_mov_b32 s56, s44
	s_mov_b32 s57, s44
	s_mov_b32 s58, s44
	s_mov_b32 s59, s44
	v_mfma_f32_32x32x16_bf16 v[34:49], v[6:9], v[158:161], 0
	ds_read_b128 v[2:5], v250
	ds_read_b128 v[6:9], v250 offset:8192
	ds_read_b128 v[58:61], v227 offset:8192
	s_lshl_b32 s6, s6, 7
	s_add_i32 s6, s12, s6
	s_lshl_b32 s6, s6, 1
	s_and_b32 s6, s6, 0x700
	s_or_b32 s6, s11, s6
	s_waitcnt vmcnt(2) lgkmcnt(2)
	v_mfma_f32_32x32x16_bf16 v[18:33], v[2:5], v[154:157], v[18:33]
	ds_read_b128 v[2:5], v252
	v_lshl_add_u64 v[218:219], v[54:55], 0, s[16:17]
	v_lshl_add_u64 v[220:221], v[50:51], 0, s[16:17]
	s_mov_b32 s8, -1
	s_movk_i32 s10, 0x4000
	s_mov_b32 s9, 0x8000
	v_mov_b32_e32 v234, 0
	s_waitcnt lgkmcnt(2)
	v_mfma_f32_32x32x16_bf16 v[34:49], v[6:9], v[154:157], v[34:49]
	ds_read_b128 v[6:9], v252 offset:8192
	s_waitcnt vmcnt(1) lgkmcnt(1)
	v_mfma_f32_32x32x16_bf16 v[18:33], v[2:5], v[146:149], v[18:33]
	ds_read_b128 v[2:5], v227
	s_waitcnt vmcnt(0) lgkmcnt(0)
	s_barrier
	s_waitcnt lgkmcnt(1)
	v_mfma_f32_32x32x16_bf16 v[34:49], v[6:9], v[146:149], v[34:49]
	s_waitcnt vmcnt(0) lgkmcnt(0)
	v_mfma_f32_32x32x16_bf16 v[18:33], v[2:5], v[142:145], v[18:33]
	v_mov_b64_e32 v[2:3], s[44:45]
	v_mov_b64_e32 v[4:5], s[46:47]
	v_mov_b64_e32 v[6:7], s[48:49]
	v_mov_b64_e32 v[8:9], s[50:51]
	v_mov_b64_e32 v[10:11], s[52:53]
	v_mov_b64_e32 v[12:13], s[54:55]
	v_mov_b64_e32 v[14:15], s[56:57]
	v_mfma_f32_32x32x16_bf16 v[34:49], v[58:61], v[142:145], v[34:49]
	s_nop 3
	v_max_f32_e32 v58, v19, v19
	v_max_f32_e32 v59, v18, v18
	v_max_f32_e32 v58, v59, v58
	v_mov_b64_e32 v[16:17], s[58:59]
	s_mov_b64 s[46:47], 0xd1000
	s_nop 2
	v_max3_f32 v59, v20, v21, v35
	v_max3_f32 v58, v58, v34, v36
	v_max3_f32 v58, v58, v37, v22
	v_max3_f32 v59, v59, v24, v25
	v_max3_f32 v58, v58, v23, v38
	v_max3_f32 v59, v59, v40, v41
	v_max3_f32 v58, v58, v39, v26
	v_max3_f32 v59, v59, v28, v29
	v_max3_f32 v58, v58, v27, v42
	v_max3_f32 v59, v59, v44, v45
	v_max3_f32 v58, v58, v43, v30
	v_max3_f32 v59, v59, v32, v33
	v_max3_f32 v58, v58, v31, v46
	v_max3_f32 v59, v59, v48, v49
	v_max3_f32 v58, v58, v47, v59
	v_mov_b32_e32 v59, v58
	s_nop 1
	v_permlane32_swap_b32_e32 v58, v59
	v_max_f32_e32 v59, v59, v59
	v_max_f32_e32 v58, v58, v58
	v_max_f32_e32 v207, v58, v59
	v_sub_f32_e32 v18, v18, v207
	v_exp_f32_e32 v82, v18
	v_sub_f32_e32 v18, v34, v207
	v_exp_f32_e32 v66, v18
	v_sub_f32_e32 v18, v19, v207
	v_exp_f32_e32 v83, v18
	v_sub_f32_e32 v18, v35, v207
	v_exp_f32_e32 v67, v18
	v_sub_f32_e32 v18, v20, v207
	v_exp_f32_e32 v84, v18
	v_sub_f32_e32 v18, v36, v207
	v_exp_f32_e32 v68, v18
	v_sub_f32_e32 v18, v21, v207
	v_exp_f32_e32 v85, v18
	v_sub_f32_e32 v18, v37, v207
	v_exp_f32_e32 v69, v18
	v_sub_f32_e32 v18, v22, v207
	v_exp_f32_e32 v86, v18
	v_sub_f32_e32 v18, v38, v207
	v_exp_f32_e32 v70, v18
	v_sub_f32_e32 v18, v23, v207
	v_exp_f32_e32 v87, v18
	v_sub_f32_e32 v18, v39, v207
	v_exp_f32_e32 v71, v18
	v_sub_f32_e32 v18, v24, v207
	v_exp_f32_e32 v88, v18
	v_sub_f32_e32 v18, v40, v207
	v_exp_f32_e32 v72, v18
	v_sub_f32_e32 v18, v25, v207
	v_exp_f32_e32 v89, v18
	v_sub_f32_e32 v18, v41, v207
	v_exp_f32_e32 v73, v18
	v_sub_f32_e32 v18, v26, v207
	v_exp_f32_e32 v90, v18
	v_sub_f32_e32 v18, v42, v207
	v_exp_f32_e32 v74, v18
	v_sub_f32_e32 v18, v27, v207
	v_exp_f32_e32 v91, v18
	v_sub_f32_e32 v18, v43, v207
	v_exp_f32_e32 v75, v18
	v_sub_f32_e32 v18, v28, v207
	v_exp_f32_e32 v92, v18
	v_sub_f32_e32 v18, v44, v207
	v_exp_f32_e32 v76, v18
	v_sub_f32_e32 v18, v29, v207
	v_exp_f32_e32 v93, v18
	v_sub_f32_e32 v18, v45, v207
	v_exp_f32_e32 v77, v18
	v_sub_f32_e32 v18, v30, v207
	v_exp_f32_e32 v94, v18
	v_sub_f32_e32 v18, v46, v207
	v_exp_f32_e32 v78, v18
	v_sub_f32_e32 v18, v31, v207
	v_exp_f32_e32 v95, v18
	v_sub_f32_e32 v18, v47, v207
	v_exp_f32_e32 v79, v18
	v_sub_f32_e32 v18, v32, v207
	v_exp_f32_e32 v96, v18
	v_sub_f32_e32 v18, v48, v207
	v_exp_f32_e32 v80, v18
	v_sub_f32_e32 v18, v33, v207
	v_exp_f32_e32 v97, v18
	v_sub_f32_e32 v18, v49, v207
	v_exp_f32_e32 v81, v18
	v_lshl_add_u64 v[18:19], v[50:51], 0, s[18:19]
	s_mov_b32 s20, m0
	s_mov_b32 m0, s89
	s_nop 0
	global_load_lds_dwordx4 v[18:19], off
	s_mov_b32 m0, s20
	v_lshl_add_u64 v[18:19], v[54:55], 0, s[18:19]
	s_mov_b32 s20, m0
	s_mov_b32 m0, vcc_lo
	s_nop 0
	global_load_lds_dwordx4 v[18:19], off
	s_mov_b32 m0, s20
	v_lshl_add_u64 v[18:19], v[56:57], 0, s[46:47]
	s_add_i32 s20, s70, 0x4000
	s_mov_b32 s45, m0
	s_mov_b32 m0, s20
	s_nop 0
	global_load_lds_dwordx4 v[18:19], off
	s_mov_b32 m0, s45
	s_mov_b64 s[46:47], 0x105000
	v_lshl_add_u64 v[18:19], v[56:57], 0, s[46:47]
	s_add_i32 s20, s70, 0x4400
	s_mov_b32 s45, m0
	s_mov_b32 m0, s20
	s_nop 0
	global_load_lds_dwordx4 v[18:19], off
	s_mov_b32 m0, s45
	ds_read_b128 v[102:105], v211 offset:16384
	ds_read_b128 v[98:101], v211 offset:24576
	ds_read_b128 v[182:185], v250 offset:16384
	ds_read_b128 v[178:181], v250 offset:24576
	ds_read_b128 v[174:177], v252 offset:16384
	ds_read_b128 v[170:173], v252 offset:24576
	ds_read_b128 v[166:169], v227 offset:16384
	ds_read_b128 v[162:165], v227 offset:24576
	s_lshl_b32 s20, s71, 2
	s_add_i32 s20, s20, 0
	s_add_i32 s20, s20, 0x18000
	s_add_u32 s4, s6, s4
	s_waitcnt vmcnt(4) lgkmcnt(0)
	s_barrier
	s_addc_u32 s5, s7, s5
	v_lshl_add_u64 v[222:223], s[4:5], 0, v[52:53]
	v_mov_b64_e32 v[64:65], v[16:17]
	v_mov_b64_e32 v[48:49], v[16:17]
	v_mov_b64_e32 v[32:33], v[16:17]
	v_lshl_add_u32 v205, v240, 2, s20
	v_lshl_add_u64 v[224:225], v[200:201], 0, v[222:223]
	v_mov_b64_e32 v[62:63], v[14:15]
	v_mov_b64_e32 v[60:61], v[12:13]
	v_mov_b64_e32 v[58:59], v[10:11]
	v_mov_b64_e32 v[56:57], v[8:9]
	v_mov_b64_e32 v[54:55], v[6:7]
	v_mov_b64_e32 v[52:53], v[4:5]
	v_mov_b64_e32 v[50:51], v[2:3]
	v_mov_b64_e32 v[46:47], v[14:15]
	v_mov_b64_e32 v[44:45], v[12:13]
	v_mov_b64_e32 v[42:43], v[10:11]
	v_mov_b64_e32 v[40:41], v[8:9]
	v_mov_b64_e32 v[38:39], v[6:7]
	v_mov_b64_e32 v[36:37], v[4:5]
	v_mov_b64_e32 v[34:35], v[2:3]
	v_mov_b64_e32 v[30:31], v[14:15]
	v_mov_b64_e32 v[28:29], v[12:13]
	v_mov_b64_e32 v[26:27], v[10:11]
	v_mov_b64_e32 v[24:25], v[8:9]
	v_mov_b64_e32 v[22:23], v[6:7]
	v_mov_b64_e32 v[20:21], v[4:5]
	v_mov_b64_e32 v[18:19], v[2:3]

.LBB0_1224:
	v_mov_b32_e32 v12, v192
	s_lshl_b32 s4, s70, 8
	s_add_i32 s6, s4, s84
	s_lshl_b32 s4, s71, 8
	v_ashrrev_i32_e32 v2, 1, v12
	s_or_b32 s4, s4, s85
	v_and_b32_e32 v2, -8, v2
	v_add_u32_e32 v22, s4, v2
	s_ashr_i32 s4, s70, 31
	s_lshr_b32 s4, s4, 28
	s_add_i32 s4, s70, s4
	s_ashr_i32 s4, s4, 4
	s_mul_hi_i32 s5, s4, 0xc000
	s_mul_i32 s4, s4, 0xc000
	s_add_u32 s4, s10, s4
	s_addc_u32 s5, s11, s5
	v_ashrrev_i32_e32 v23, 31, v22
	v_lshl_add_u64 v[10:11], v[22:23], 2, s[4:5]
	global_load_dwordx4 v[2:5], v[10:11], off offset:16
	global_load_dwordx4 v[6:9], v[10:11], off
	s_mov_b32 s4, 0x3b800000
	s_andn2_b64 vcc, exec, s[56:57]
	v_lshlrev_b64 v[178:179], 1, v[22:23]
	s_waitcnt vmcnt(0)
	v_pk_mul_f32 v[32:33], v[4:5], s[4:5] op_sel_hi:[1,0]
	v_pk_mul_f32 v[176:177], v[8:9], s[4:5] op_sel_hi:[1,0]
	v_pk_mul_f32 v[174:175], v[6:7], s[4:5] op_sel_hi:[1,0]
	v_pk_mul_f32 v[28:29], v[2:3], s[4:5] op_sel_hi:[1,0]
	global_load_dwordx4 v[2:5], v[10:11], off offset:528
	global_load_dwordx4 v[6:9], v[10:11], off offset:512
	s_waitcnt vmcnt(0)
	v_pk_mul_f32 v[24:25], v[2:3], s[4:5] op_sel_hi:[1,0]
	v_and_or_b32 v2, v12, 15, s6
	v_ashrrev_i32_e32 v3, 31, v2
	v_lshlrev_b64 v[180:181], 12, v[2:3]
	v_pk_mul_f32 v[172:173], v[8:9], s[4:5] op_sel_hi:[1,0]
	v_pk_mul_f32 v[30:31], v[6:7], s[4:5] op_sel_hi:[1,0]
	v_pk_mul_f32 v[26:27], v[4:5], s[4:5] op_sel_hi:[1,0]
	v_or_b32_e32 v12, 16, v2
	v_lshl_add_u64 v[182:183], s[50:51], 0, v[180:181]
	v_or_b32_e32 v10, 32, v2
	v_or_b32_e32 v184, 48, v2
	s_cbranch_vccnz .LBB0_1230
	v_lshl_add_u64 v[4:5], v[22:23], 2, s[42:43]
	v_lshlrev_b64 v[6:7], 13, v[2:3]
	v_lshl_add_u64 v[186:187], v[4:5], 0, v[6:7]
	global_load_dwordx4 v[6:9], v[186:187], off offset:16 nt
	global_load_dwordx4 v[14:17], v[186:187], off nt
	global_load_dwordx4 v[18:21], v[186:187], off offset:528 nt
	s_nop 0
	global_load_dwordx4 v[186:189], v[186:187], off offset:512 nt
	v_ashrrev_i32_e32 v13, 31, v12
	v_lshlrev_b64 v[190:191], 13, v[12:13]
	v_lshl_add_u64 v[190:191], v[4:5], 0, v[190:191]
	global_load_dwordx4 v[196:199], v[190:191], off offset:16 nt
	global_load_dwordx4 v[200:203], v[190:191], off nt
	global_load_dwordx4 v[204:207], v[190:191], off offset:528 nt
	global_load_dwordx4 v[208:211], v[190:191], off offset:512 nt
	v_ashrrev_i32_e32 v11, 31, v10
	v_ashrrev_i32_e32 v185, 31, v184
	s_waitcnt vmcnt(0)
	v_pk_fma_f32 v[190:191], v[160:161], v[32:33], v[8:9]
	v_pk_fma_f32 v[14:15], v[154:155], v[174:175], v[14:15]
	v_pk_fma_f32 v[8:9], v[158:159], v[28:29], v[6:7]
	v_pk_fma_f32 v[16:17], v[156:157], v[176:177], v[16:17]
	v_cvt_pk_bf16_f32 v6, v14, v15
	v_lshl_add_u64 v[14:15], v[182:183], 0, v[178:179]
	v_cvt_pk_bf16_f32 v7, v16, v17
	v_cvt_pk_bf16_f32 v8, v8, v9
	v_cvt_pk_bf16_f32 v9, v190, v191
	global_store_dwordx4 v[14:15], v[6:9], off sc1
	v_pk_fma_f32 v[16:17], v[148:149], v[26:27], v[20:21]
	v_pk_fma_f32 v[18:19], v[146:147], v[24:25], v[18:19]
	v_pk_fma_f32 v[8:9], v[152:153], v[172:173], v[188:189]
	v_pk_fma_f32 v[6:7], v[150:151], v[30:31], v[186:187]
	v_lshlrev_b64 v[190:191], 13, v[184:185]
	v_cvt_pk_bf16_f32 v6, v6, v7
	v_cvt_pk_bf16_f32 v7, v8, v9
	v_cvt_pk_bf16_f32 v8, v18, v19
	v_cvt_pk_bf16_f32 v9, v16, v17
	global_store_dwordx4 v[14:15], v[6:9], off offset:256 sc1
	v_lshlrev_b64 v[14:15], 12, v[12:13]
	v_lshl_add_u64 v[14:15], s[50:51], 0, v[14:15]
	v_pk_fma_f32 v[6:7], v[142:143], v[174:175], v[200:201]
	v_pk_fma_f32 v[8:9], v[144:145], v[176:177], v[202:203]
	v_cvt_pk_bf16_f32 v6, v6, v7
	v_lshl_add_u64 v[14:15], v[14:15], 0, v[178:179]
	v_cvt_pk_bf16_f32 v7, v8, v9
	v_pk_fma_f32 v[16:17], v[140:141], v[32:33], v[198:199]
	v_pk_fma_f32 v[18:19], v[138:139], v[28:29], v[196:197]
	v_lshl_add_u64 v[190:191], v[4:5], 0, v[190:191]
	v_cvt_pk_bf16_f32 v8, v18, v19
	v_cvt_pk_bf16_f32 v9, v16, v17
	global_store_dwordx4 v[14:15], v[6:9], off sc1
	v_pk_fma_f32 v[16:17], v[132:133], v[26:27], v[206:207]
	v_pk_fma_f32 v[18:19], v[130:131], v[24:25], v[204:205]
	v_pk_fma_f32 v[6:7], v[134:135], v[30:31], v[208:209]
	v_pk_fma_f32 v[8:9], v[136:137], v[172:173], v[210:211]
	v_cvt_pk_bf16_f32 v6, v6, v7
	s_nop 0
	v_cvt_pk_bf16_f32 v7, v8, v9
	v_cvt_pk_bf16_f32 v8, v18, v19
	v_cvt_pk_bf16_f32 v9, v16, v17
	global_store_dwordx4 v[14:15], v[6:9], off offset:256 sc1
	s_nop 1
	v_lshlrev_b64 v[6:7], 13, v[10:11]
	v_lshl_add_u64 v[186:187], v[4:5], 0, v[6:7]
	global_load_dwordx4 v[6:9], v[186:187], off offset:16 nt
	global_load_dwordx4 v[14:17], v[186:187], off nt
	global_load_dwordx4 v[18:21], v[186:187], off offset:528 nt
	s_nop 0
	global_load_dwordx4 v[186:189], v[186:187], off offset:512 nt
	s_nop 0
	global_load_dwordx4 v[196:199], v[190:191], off offset:16 nt
	global_load_dwordx4 v[200:203], v[190:191], off nt
	global_load_dwordx4 v[204:207], v[190:191], off offset:528 nt
	global_load_dwordx4 v[208:211], v[190:191], off offset:512 nt
	v_lshlrev_b64 v[190:191], 12, v[10:11]
	s_waitcnt vmcnt(0)
	v_pk_fma_f32 v[212:213], v[124:125], v[32:33], v[8:9]
	v_pk_fma_f32 v[14:15], v[126:127], v[174:175], v[14:15]
	v_pk_fma_f32 v[8:9], v[122:123], v[28:29], v[6:7]
	v_cvt_pk_bf16_f32 v6, v14, v15
	v_lshl_add_u64 v[14:15], s[50:51], 0, v[190:191]
	v_pk_fma_f32 v[16:17], v[128:129], v[176:177], v[16:17]
	v_lshl_add_u64 v[14:15], v[14:15], 0, v[178:179]
	v_cvt_pk_bf16_f32 v7, v16, v17
	v_cvt_pk_bf16_f32 v8, v8, v9
	v_cvt_pk_bf16_f32 v9, v212, v213
	global_store_dwordx4 v[14:15], v[6:9], off sc1
	v_pk_fma_f32 v[16:17], v[116:117], v[26:27], v[20:21]
	v_pk_fma_f32 v[18:19], v[114:115], v[24:25], v[18:19]
	v_pk_fma_f32 v[8:9], v[120:121], v[172:173], v[188:189]
	v_pk_fma_f32 v[6:7], v[118:119], v[30:31], v[186:187]
	v_add_u32_e32 v190, 0x80, v2
	v_cvt_pk_bf16_f32 v6, v6, v7
	v_cvt_pk_bf16_f32 v7, v8, v9
	v_cvt_pk_bf16_f32 v8, v18, v19
	v_cvt_pk_bf16_f32 v9, v16, v17
	global_store_dwordx4 v[14:15], v[6:9], off offset:256 sc1
	v_lshlrev_b64 v[14:15], 12, v[184:185]
	v_lshl_add_u64 v[14:15], s[50:51], 0, v[14:15]
	v_pk_fma_f32 v[6:7], v[110:111], v[174:175], v[200:201]
	v_pk_fma_f32 v[8:9], v[112:113], v[176:177], v[202:203]
	v_cvt_pk_bf16_f32 v6, v6, v7
	v_lshl_add_u64 v[14:15], v[14:15], 0, v[178:179]
	v_cvt_pk_bf16_f32 v7, v8, v9
	v_pk_fma_f32 v[16:17], v[108:109], v[32:33], v[198:199]
	v_pk_fma_f32 v[18:19], v[106:107], v[28:29], v[196:197]
	v_ashrrev_i32_e32 v191, 31, v190
	v_cvt_pk_bf16_f32 v8, v18, v19
	v_cvt_pk_bf16_f32 v9, v16, v17
	global_store_dwordx4 v[14:15], v[6:9], off sc1
	v_pk_fma_f32 v[16:17], v[100:101], v[26:27], v[206:207]
	v_pk_fma_f32 v[18:19], v[98:99], v[24:25], v[204:205]
	v_pk_fma_f32 v[6:7], v[102:103], v[30:31], v[208:209]
	v_pk_fma_f32 v[8:9], v[104:105], v[172:173], v[210:211]
	v_cvt_pk_bf16_f32 v6, v6, v7
	v_add_u32_e32 v212, 0x90, v2
	v_cvt_pk_bf16_f32 v7, v8, v9
	v_cvt_pk_bf16_f32 v8, v18, v19
	v_cvt_pk_bf16_f32 v9, v16, v17
	global_store_dwordx4 v[14:15], v[6:9], off offset:256 sc1
	v_ashrrev_i32_e32 v213, 31, v212
	v_lshlrev_b64 v[196:197], 13, v[212:213]
	v_lshlrev_b64 v[6:7], 13, v[190:191]
	v_lshl_add_u64 v[186:187], v[4:5], 0, v[6:7]
	global_load_dwordx4 v[6:9], v[186:187], off offset:16 nt
	global_load_dwordx4 v[14:17], v[186:187], off nt
	global_load_dwordx4 v[18:21], v[186:187], off offset:528 nt
	s_nop 0
	global_load_dwordx4 v[186:189], v[186:187], off offset:512 nt
	v_lshl_add_u64 v[208:209], v[4:5], 0, v[196:197]
	global_load_dwordx4 v[196:199], v[208:209], off offset:16 nt
	global_load_dwordx4 v[200:203], v[208:209], off nt
	global_load_dwordx4 v[204:207], v[208:209], off offset:528 nt
	s_nop 0
	global_load_dwordx4 v[208:211], v[208:209], off offset:512 nt
	v_lshlrev_b64 v[190:191], 12, v[190:191]
	s_waitcnt vmcnt(0)
	v_pk_fma_f32 v[214:215], v[92:93], v[32:33], v[8:9]
	v_pk_fma_f32 v[14:15], v[94:95], v[174:175], v[14:15]
	v_pk_fma_f32 v[8:9], v[90:91], v[28:29], v[6:7]
	v_cvt_pk_bf16_f32 v6, v14, v15
	v_lshl_add_u64 v[14:15], s[50:51], 0, v[190:191]
	v_pk_fma_f32 v[16:17], v[96:97], v[176:177], v[16:17]
	v_lshl_add_u64 v[14:15], v[14:15], 0, v[178:179]
	v_cvt_pk_bf16_f32 v7, v16, v17
	v_cvt_pk_bf16_f32 v8, v8, v9
	v_cvt_pk_bf16_f32 v9, v214, v215
	global_store_dwordx4 v[14:15], v[6:9], off sc1
	v_pk_fma_f32 v[16:17], v[84:85], v[26:27], v[20:21]
	v_pk_fma_f32 v[18:19], v[82:83], v[24:25], v[18:19]
	v_pk_fma_f32 v[8:9], v[88:89], v[172:173], v[188:189]
	v_pk_fma_f32 v[6:7], v[86:87], v[30:31], v[186:187]
	v_add_u32_e32 v190, 0xa0, v2
	v_cvt_pk_bf16_f32 v6, v6, v7
	v_cvt_pk_bf16_f32 v7, v8, v9
	v_cvt_pk_bf16_f32 v8, v18, v19
	v_cvt_pk_bf16_f32 v9, v16, v17
	global_store_dwordx4 v[14:15], v[6:9], off offset:256 sc1
	v_lshlrev_b64 v[14:15], 12, v[212:213]
	v_lshl_add_u64 v[14:15], s[50:51], 0, v[14:15]
	v_pk_fma_f32 v[6:7], v[78:79], v[174:175], v[200:201]
	v_pk_fma_f32 v[8:9], v[80:81], v[176:177], v[202:203]
	v_cvt_pk_bf16_f32 v6, v6, v7
	v_lshl_add_u64 v[14:15], v[14:15], 0, v[178:179]
	v_cvt_pk_bf16_f32 v7, v8, v9
	v_pk_fma_f32 v[16:17], v[76:77], v[32:33], v[198:199]
	v_pk_fma_f32 v[18:19], v[74:75], v[28:29], v[196:197]
	v_ashrrev_i32_e32 v191, 31, v190
	v_cvt_pk_bf16_f32 v8, v18, v19
	v_cvt_pk_bf16_f32 v9, v16, v17
	global_store_dwordx4 v[14:15], v[6:9], off sc1
	v_pk_fma_f32 v[16:17], v[68:69], v[26:27], v[206:207]
	v_pk_fma_f32 v[18:19], v[66:67], v[24:25], v[204:205]
	v_pk_fma_f32 v[6:7], v[70:71], v[30:31], v[208:209]
	v_pk_fma_f32 v[8:9], v[72:73], v[172:173], v[210:211]
	v_cvt_pk_bf16_f32 v6, v6, v7
	v_add_u32_e32 v208, 0xb0, v2
	v_cvt_pk_bf16_f32 v7, v8, v9
	v_cvt_pk_bf16_f32 v8, v18, v19
	v_cvt_pk_bf16_f32 v9, v16, v17
	global_store_dwordx4 v[14:15], v[6:9], off offset:256 sc1
	v_ashrrev_i32_e32 v209, 31, v208
	v_lshlrev_b64 v[2:3], 13, v[208:209]
	v_lshlrev_b64 v[6:7], 13, v[190:191]
	v_lshl_add_u64 v[6:7], v[4:5], 0, v[6:7]
	global_load_dwordx4 v[14:17], v[6:7], off offset:16 nt
	global_load_dwordx4 v[18:21], v[6:7], off nt
	global_load_dwordx4 v[186:189], v[6:7], off offset:528 nt
	global_load_dwordx4 v[196:199], v[6:7], off offset:512 nt
	v_lshl_add_u64 v[6:7], v[4:5], 0, v[2:3]
	global_load_dwordx4 v[200:203], v[6:7], off offset:16 nt
	global_load_dwordx4 v[204:207], v[6:7], off nt
	global_load_dwordx4 v[2:5], v[6:7], off offset:528 nt
	s_nop 0
	global_load_dwordx4 v[6:9], v[6:7], off offset:512 nt
	v_lshlrev_b64 v[190:191], 12, v[190:191]
	s_waitcnt vmcnt(0)
	v_pk_fma_f32 v[210:211], v[60:61], v[32:33], v[16:17]
	v_pk_fma_f32 v[18:19], v[62:63], v[174:175], v[18:19]
	v_pk_fma_f32 v[16:17], v[58:59], v[28:29], v[14:15]
	v_cvt_pk_bf16_f32 v14, v18, v19
	v_lshl_add_u64 v[18:19], s[50:51], 0, v[190:191]
	v_pk_fma_f32 v[20:21], v[64:65], v[176:177], v[20:21]
	v_lshl_add_u64 v[18:19], v[18:19], 0, v[178:179]
	v_cvt_pk_bf16_f32 v15, v20, v21
	v_cvt_pk_bf16_f32 v16, v16, v17
	v_cvt_pk_bf16_f32 v17, v210, v211
	global_store_dwordx4 v[18:19], v[14:17], off sc1
	v_pk_fma_f32 v[20:21], v[52:53], v[26:27], v[188:189]
	v_pk_fma_f32 v[186:187], v[50:51], v[24:25], v[186:187]
	v_pk_fma_f32 v[16:17], v[56:57], v[172:173], v[198:199]
	v_pk_fma_f32 v[14:15], v[54:55], v[30:31], v[196:197]
	v_pk_fma_f32 v[8:9], v[40:41], v[172:173], v[8:9]
	v_cvt_pk_bf16_f32 v14, v14, v15
	v_cvt_pk_bf16_f32 v15, v16, v17
	v_cvt_pk_bf16_f32 v16, v186, v187
	v_cvt_pk_bf16_f32 v17, v20, v21
	global_store_dwordx4 v[18:19], v[14:17], off offset:256 sc1
	v_pk_fma_f32 v[18:19], v[48:49], v[176:177], v[206:207]
	v_pk_fma_f32 v[20:21], v[44:45], v[32:33], v[202:203]
	v_lshlrev_b64 v[14:15], 12, v[208:209]
	v_pk_fma_f32 v[16:17], v[46:47], v[174:175], v[204:205]
	v_pk_fma_f32 v[186:187], v[42:43], v[28:29], v[200:201]
	v_cvt_pk_bf16_f32 v16, v16, v17
	v_cvt_pk_bf16_f32 v17, v18, v19
	v_pk_fma_f32 v[6:7], v[38:39], v[30:31], v[6:7]
	v_cvt_pk_bf16_f32 v18, v186, v187
	v_cvt_pk_bf16_f32 v19, v20, v21
	v_lshl_add_u64 v[20:21], s[50:51], 0, v[14:15]
	v_lshl_add_u64 v[20:21], v[20:21], 0, v[178:179]
	global_store_dwordx4 v[20:21], v[16:19], off sc1
	s_nop 1
	v_pk_fma_f32 v[16:17], v[36:37], v[26:27], v[4:5]
	v_pk_fma_f32 v[4:5], v[34:35], v[24:25], v[2:3]
	v_cvt_pk_bf16_f32 v2, v6, v7
	v_cvt_pk_bf16_f32 v3, v8, v9
	s_nop 0
	v_cvt_pk_bf16_f32 v4, v4, v5
	v_cvt_pk_bf16_f32 v5, v16, v17
	s_cbranch_execnz .LBB0_1227
.LBB0_1226:
	v_lshl_add_u64 v[186:187], s[50:51], 0, v[178:179]
	v_lshl_add_u64 v[2:3], v[186:187], 0, v[180:181]
	global_load_dwordx4 v[196:199], v[2:3], off nt
	global_load_dwordx4 v[200:203], v[2:3], off offset:256 nt
	v_ashrrev_i32_e32 v13, 31, v12
	v_lshlrev_b64 v[190:191], 12, v[12:13]
	v_lshl_add_u64 v[2:3], v[186:187], 0, v[190:191]
	global_load_dwordx4 v[204:207], v[2:3], off nt
	global_load_dwordx4 v[18:21], v[2:3], off offset:256 nt
	v_ashrrev_i32_e32 v11, 31, v10
	v_lshlrev_b64 v[188:189], 12, v[10:11]
	v_lshl_add_u64 v[2:3], v[186:187], 0, v[188:189]
	global_load_dwordx4 v[14:17], v[2:3], off nt
	global_load_dwordx4 v[10:13], v[2:3], off offset:256 nt
	v_ashrrev_i32_e32 v185, 31, v184
	v_lshlrev_b64 v[184:185], 12, v[184:185]
	v_lshl_add_u64 v[2:3], v[186:187], 0, v[184:185]
	global_load_dwordx4 v[6:9], v[2:3], off nt
	s_nop 0
	global_load_dwordx4 v[2:5], v[2:3], off offset:256 nt
	s_mov_b64 s[4:5], 0x80000
	s_waitcnt vmcnt(0)
	v_lshlrev_b32_e32 v208, 16, v196
	v_and_b32_e32 v209, 0xffff0000, v196
	v_lshlrev_b32_e32 v196, 16, v197
	v_and_b32_e32 v197, 0xffff0000, v197
	v_lshlrev_b32_e32 v210, 16, v198
	v_and_b32_e32 v211, 0xffff0000, v198
	v_lshlrev_b32_e32 v198, 16, v199
	v_and_b32_e32 v199, 0xffff0000, v199
	v_pk_fma_f32 v[156:157], v[156:157], v[176:177], v[196:197]
	v_pk_fma_f32 v[154:155], v[154:155], v[174:175], v[208:209]
	v_pk_fma_f32 v[158:159], v[158:159], v[28:29], v[210:211]
	v_pk_fma_f32 v[160:161], v[160:161], v[32:33], v[198:199]
	v_cvt_pk_bf16_f32 v154, v154, v155
	v_cvt_pk_bf16_f32 v155, v156, v157
	v_cvt_pk_bf16_f32 v156, v158, v159
	v_lshl_add_u64 v[158:159], v[182:183], 0, v[178:179]
	v_cvt_pk_bf16_f32 v157, v160, v161
	global_store_dwordx4 v[158:159], v[154:157], off sc1
	v_lshlrev_b32_e32 v160, 16, v202
	v_and_b32_e32 v161, 0xffff0000, v202
	v_lshlrev_b32_e32 v154, 16, v200
	v_and_b32_e32 v155, 0xffff0000, v200
	v_lshlrev_b32_e32 v156, 16, v201
	v_and_b32_e32 v157, 0xffff0000, v201
	v_lshlrev_b32_e32 v182, 16, v203
	v_and_b32_e32 v183, 0xffff0000, v203
	v_pk_fma_f32 v[152:153], v[152:153], v[172:173], v[156:157]
	v_pk_fma_f32 v[150:151], v[150:151], v[30:31], v[154:155]
	v_pk_fma_f32 v[154:155], v[148:149], v[26:27], v[182:183]
	v_pk_fma_f32 v[148:149], v[146:147], v[24:25], v[160:161]
	v_cvt_pk_bf16_f32 v146, v150, v151
	v_cvt_pk_bf16_f32 v147, v152, v153
	v_lshlrev_b32_e32 v150, 16, v206
	v_cvt_pk_bf16_f32 v148, v148, v149
	v_cvt_pk_bf16_f32 v149, v154, v155
	global_store_dwordx4 v[158:159], v[146:149], off offset:256 sc1
	v_and_b32_e32 v151, 0xffff0000, v206
	v_lshlrev_b32_e32 v152, 16, v207
	v_lshlrev_b32_e32 v146, 16, v204
	v_and_b32_e32 v147, 0xffff0000, v204
	v_and_b32_e32 v153, 0xffff0000, v207
	v_pk_fma_f32 v[142:143], v[142:143], v[174:175], v[146:147]
	v_lshlrev_b32_e32 v148, 16, v205
	v_and_b32_e32 v149, 0xffff0000, v205
	v_pk_fma_f32 v[146:147], v[140:141], v[32:33], v[152:153]
	v_pk_fma_f32 v[140:141], v[138:139], v[28:29], v[150:151]
	v_cvt_pk_bf16_f32 v138, v142, v143
	v_lshl_add_u64 v[142:143], s[50:51], 0, v[190:191]
	v_pk_fma_f32 v[144:145], v[144:145], v[176:177], v[148:149]
	v_lshl_add_u64 v[142:143], v[142:143], 0, v[178:179]
	v_cvt_pk_bf16_f32 v139, v144, v145
	v_cvt_pk_bf16_f32 v140, v140, v141
	v_cvt_pk_bf16_f32 v141, v146, v147
	global_store_dwordx4 v[142:143], v[138:141], off sc1
	s_nop 1
	v_lshlrev_b32_e32 v138, 16, v18
	v_and_b32_e32 v139, 0xffff0000, v18
	v_lshlrev_b32_e32 v18, 16, v19
	v_and_b32_e32 v19, 0xffff0000, v19
	v_lshlrev_b32_e32 v140, 16, v20
	v_and_b32_e32 v141, 0xffff0000, v20
	v_lshlrev_b32_e32 v20, 16, v21
	v_and_b32_e32 v21, 0xffff0000, v21
	v_pk_fma_f32 v[136:137], v[136:137], v[172:173], v[18:19]
	v_pk_fma_f32 v[18:19], v[134:135], v[30:31], v[138:139]
	v_pk_fma_f32 v[132:133], v[132:133], v[26:27], v[20:21]
	v_pk_fma_f32 v[20:21], v[130:131], v[24:25], v[140:141]
	v_cvt_pk_bf16_f32 v18, v18, v19
	v_cvt_pk_bf16_f32 v19, v136, v137
	s_nop 0
	v_cvt_pk_bf16_f32 v20, v20, v21
	v_cvt_pk_bf16_f32 v21, v132, v133
	global_store_dwordx4 v[142:143], v[18:21], off offset:256 sc1
	s_nop 1
	v_lshlrev_b32_e32 v18, 16, v14
	v_and_b32_e32 v19, 0xffff0000, v14
	v_lshlrev_b32_e32 v14, 16, v15
	v_and_b32_e32 v15, 0xffff0000, v15
	v_lshlrev_b32_e32 v20, 16, v16
	v_and_b32_e32 v21, 0xffff0000, v16
	v_lshlrev_b32_e32 v16, 16, v17
	v_and_b32_e32 v17, 0xffff0000, v17
	v_pk_fma_f32 v[128:129], v[128:129], v[176:177], v[14:15]
	v_pk_fma_f32 v[14:15], v[126:127], v[174:175], v[18:19]
	v_pk_fma_f32 v[18:19], v[124:125], v[32:33], v[16:17]
	v_pk_fma_f32 v[16:17], v[122:123], v[28:29], v[20:21]
	v_cvt_pk_bf16_f32 v14, v14, v15
	v_cvt_pk_bf16_f32 v15, v128, v129
	s_nop 0
	v_cvt_pk_bf16_f32 v16, v16, v17
	v_cvt_pk_bf16_f32 v17, v18, v19
	v_lshl_add_u64 v[18:19], s[50:51], 0, v[188:189]
	v_lshl_add_u64 v[18:19], v[18:19], 0, v[178:179]
	global_store_dwordx4 v[18:19], v[14:17], off sc1
	s_nop 1
	v_lshlrev_b32_e32 v14, 16, v10
	v_and_b32_e32 v15, 0xffff0000, v10
	v_lshlrev_b32_e32 v10, 16, v11
	v_and_b32_e32 v11, 0xffff0000, v11
	v_lshlrev_b32_e32 v16, 16, v12
	v_and_b32_e32 v17, 0xffff0000, v12
	v_lshlrev_b32_e32 v12, 16, v13
	v_and_b32_e32 v13, 0xffff0000, v13
	v_pk_fma_f32 v[20:21], v[120:121], v[172:173], v[10:11]
	v_pk_fma_f32 v[10:11], v[118:119], v[30:31], v[14:15]
	v_pk_fma_f32 v[14:15], v[116:117], v[26:27], v[12:13]
	v_pk_fma_f32 v[12:13], v[114:115], v[24:25], v[16:17]
	v_cvt_pk_bf16_f32 v10, v10, v11
	v_cvt_pk_bf16_f32 v11, v20, v21
	v_lshl_add_u64 v[20:21], v[180:181], 0, s[4:5]
	v_cvt_pk_bf16_f32 v12, v12, v13
	v_cvt_pk_bf16_f32 v13, v14, v15
	global_store_dwordx4 v[18:19], v[10:13], off offset:256 sc1
	s_mov_b64 s[4:5], 0x90000
	v_lshl_add_u64 v[114:115], v[180:181], 0, s[4:5]
	v_lshlrev_b32_e32 v10, 16, v6
	v_and_b32_e32 v11, 0xffff0000, v6
	v_lshlrev_b32_e32 v6, 16, v7
	v_and_b32_e32 v7, 0xffff0000, v7
	v_lshlrev_b32_e32 v12, 16, v8
	v_and_b32_e32 v13, 0xffff0000, v8
	v_lshlrev_b32_e32 v8, 16, v9
	v_and_b32_e32 v9, 0xffff0000, v9
	v_pk_fma_f32 v[14:15], v[112:113], v[176:177], v[6:7]
	v_pk_fma_f32 v[6:7], v[110:111], v[174:175], v[10:11]
	v_pk_fma_f32 v[10:11], v[108:109], v[32:33], v[8:9]
	v_pk_fma_f32 v[8:9], v[106:107], v[28:29], v[12:13]
	v_cvt_pk_bf16_f32 v6, v6, v7
	v_cvt_pk_bf16_f32 v7, v14, v15
	s_mov_b64 s[4:5], 0xa0000
	v_cvt_pk_bf16_f32 v8, v8, v9
	v_cvt_pk_bf16_f32 v9, v10, v11
	v_lshl_add_u64 v[10:11], s[50:51], 0, v[184:185]
	v_lshl_add_u64 v[10:11], v[10:11], 0, v[178:179]
	global_store_dwordx4 v[10:11], v[6:9], off sc1
	v_lshl_add_u64 v[116:117], v[180:181], 0, s[4:5]
	s_mov_b64 s[4:5], 0xb0000
	v_lshlrev_b32_e32 v6, 16, v2
	v_and_b32_e32 v7, 0xffff0000, v2
	v_lshlrev_b32_e32 v2, 16, v3
	v_and_b32_e32 v3, 0xffff0000, v3
	v_lshlrev_b32_e32 v8, 16, v4
	v_and_b32_e32 v9, 0xffff0000, v4
	v_lshlrev_b32_e32 v4, 16, v5
	v_and_b32_e32 v5, 0xffff0000, v5
	v_pk_fma_f32 v[12:13], v[104:105], v[172:173], v[2:3]
	v_pk_fma_f32 v[2:3], v[102:103], v[30:31], v[6:7]
	v_pk_fma_f32 v[6:7], v[100:101], v[26:27], v[4:5]
	v_pk_fma_f32 v[4:5], v[98:99], v[24:25], v[8:9]
	v_cvt_pk_bf16_f32 v2, v2, v3
	v_cvt_pk_bf16_f32 v3, v12, v13
	v_lshl_add_u64 v[14:15], v[180:181], 0, s[4:5]
	v_cvt_pk_bf16_f32 v4, v4, v5
	v_cvt_pk_bf16_f32 v5, v6, v7
	global_store_dwordx4 v[10:11], v[2:5], off offset:256 sc1
	s_nop 1
	v_lshl_add_u64 v[2:3], v[186:187], 0, v[20:21]
	global_load_dwordx4 v[10:13], v[2:3], off nt
	global_load_dwordx4 v[16:19], v[2:3], off offset:256 nt
	v_lshl_add_u64 v[2:3], v[186:187], 0, v[114:115]
	global_load_dwordx4 v[98:101], v[2:3], off nt
	global_load_dwordx4 v[102:105], v[2:3], off offset:256 nt
	v_lshl_add_u64 v[2:3], v[186:187], 0, v[116:117]
	global_load_dwordx4 v[106:109], v[2:3], off nt
	global_load_dwordx4 v[110:113], v[2:3], off offset:256 nt
	v_lshl_add_u64 v[2:3], v[186:187], 0, v[14:15]
	global_load_dwordx4 v[6:9], v[2:3], off nt
	s_nop 0
	global_load_dwordx4 v[2:5], v[2:3], off offset:256 nt
	v_lshl_add_u64 v[20:21], s[50:51], 0, v[20:21]
	v_lshl_add_u64 v[20:21], v[20:21], 0, v[178:179]
	s_waitcnt vmcnt(0)
	v_lshlrev_b32_e32 v118, 16, v10
	v_and_b32_e32 v119, 0xffff0000, v10
	v_lshlrev_b32_e32 v10, 16, v11
	v_and_b32_e32 v11, 0xffff0000, v11
	v_lshlrev_b32_e32 v120, 16, v12
	v_and_b32_e32 v121, 0xffff0000, v12
	v_lshlrev_b32_e32 v12, 16, v13
	v_and_b32_e32 v13, 0xffff0000, v13
	v_pk_fma_f32 v[96:97], v[96:97], v[176:177], v[10:11]
	v_pk_fma_f32 v[10:11], v[94:95], v[174:175], v[118:119]
	v_pk_fma_f32 v[92:93], v[92:93], v[32:33], v[12:13]
	v_pk_fma_f32 v[12:13], v[90:91], v[28:29], v[120:121]
	v_cvt_pk_bf16_f32 v10, v10, v11
	v_cvt_pk_bf16_f32 v11, v96, v97
	s_nop 0
	v_cvt_pk_bf16_f32 v12, v12, v13
	v_cvt_pk_bf16_f32 v13, v92, v93
	global_store_dwordx4 v[20:21], v[10:13], off sc1
	s_nop 1
	v_lshlrev_b32_e32 v10, 16, v16
	v_and_b32_e32 v11, 0xffff0000, v16
	v_lshlrev_b32_e32 v12, 16, v17
	v_and_b32_e32 v13, 0xffff0000, v17
	v_lshlrev_b32_e32 v16, 16, v18
	v_and_b32_e32 v17, 0xffff0000, v18
	v_lshlrev_b32_e32 v18, 16, v19
	v_and_b32_e32 v19, 0xffff0000, v19
	v_pk_fma_f32 v[12:13], v[88:89], v[172:173], v[12:13]
	v_pk_fma_f32 v[10:11], v[86:87], v[30:31], v[10:11]
	v_pk_fma_f32 v[18:19], v[84:85], v[26:27], v[18:19]
	v_pk_fma_f32 v[16:17], v[82:83], v[24:25], v[16:17]
	v_cvt_pk_bf16_f32 v10, v10, v11
	v_cvt_pk_bf16_f32 v11, v12, v13
	s_nop 0
	v_cvt_pk_bf16_f32 v12, v16, v17
	v_cvt_pk_bf16_f32 v13, v18, v19
	global_store_dwordx4 v[20:21], v[10:13], off offset:256 sc1
	v_lshlrev_b32_e32 v16, 16, v100
	v_and_b32_e32 v17, 0xffff0000, v100
	v_lshlrev_b32_e32 v10, 16, v98
	v_and_b32_e32 v11, 0xffff0000, v98
	v_lshlrev_b32_e32 v12, 16, v99
	v_and_b32_e32 v13, 0xffff0000, v99
	v_pk_fma_f32 v[12:13], v[80:81], v[176:177], v[12:13]
	v_pk_fma_f32 v[10:11], v[78:79], v[174:175], v[10:11]
	v_pk_fma_f32 v[16:17], v[74:75], v[28:29], v[16:17]
	v_lshlrev_b32_e32 v18, 16, v101
	v_and_b32_e32 v19, 0xffff0000, v101
	v_cvt_pk_bf16_f32 v10, v10, v11
	v_cvt_pk_bf16_f32 v11, v12, v13
	v_cvt_pk_bf16_f32 v12, v16, v17
	v_lshl_add_u64 v[16:17], s[50:51], 0, v[114:115]
	v_pk_fma_f32 v[18:19], v[76:77], v[32:33], v[18:19]
	v_lshl_add_u64 v[16:17], v[16:17], 0, v[178:179]
	v_cvt_pk_bf16_f32 v13, v18, v19
	global_store_dwordx4 v[16:17], v[10:13], off sc1
	v_lshlrev_b32_e32 v18, 16, v104
	v_and_b32_e32 v19, 0xffff0000, v104
	v_lshlrev_b32_e32 v10, 16, v102
	v_and_b32_e32 v11, 0xffff0000, v102
	v_lshlrev_b32_e32 v12, 16, v103
	v_and_b32_e32 v13, 0xffff0000, v103
	v_lshlrev_b32_e32 v20, 16, v105
	v_and_b32_e32 v21, 0xffff0000, v105
	v_pk_fma_f32 v[12:13], v[72:73], v[172:173], v[12:13]
	v_pk_fma_f32 v[10:11], v[70:71], v[30:31], v[10:11]
	v_pk_fma_f32 v[20:21], v[68:69], v[26:27], v[20:21]
	v_pk_fma_f32 v[18:19], v[66:67], v[24:25], v[18:19]
	v_cvt_pk_bf16_f32 v10, v10, v11
	v_cvt_pk_bf16_f32 v11, v12, v13
	s_nop 0
	v_cvt_pk_bf16_f32 v12, v18, v19
	v_cvt_pk_bf16_f32 v13, v20, v21
	global_store_dwordx4 v[16:17], v[10:13], off offset:256 sc1
	v_lshlrev_b32_e32 v16, 16, v108
	v_and_b32_e32 v17, 0xffff0000, v108
	v_lshlrev_b32_e32 v10, 16, v106
	v_and_b32_e32 v11, 0xffff0000, v106
	v_lshlrev_b32_e32 v12, 16, v107
	v_and_b32_e32 v13, 0xffff0000, v107
	v_pk_fma_f32 v[12:13], v[64:65], v[176:177], v[12:13]
	v_pk_fma_f32 v[10:11], v[62:63], v[174:175], v[10:11]
	v_pk_fma_f32 v[16:17], v[58:59], v[28:29], v[16:17]
	v_lshlrev_b32_e32 v18, 16, v109
	v_and_b32_e32 v19, 0xffff0000, v109
	v_cvt_pk_bf16_f32 v10, v10, v11
	v_cvt_pk_bf16_f32 v11, v12, v13
	v_cvt_pk_bf16_f32 v12, v16, v17
	v_lshl_add_u64 v[16:17], s[50:51], 0, v[116:117]
	v_pk_fma_f32 v[18:19], v[60:61], v[32:33], v[18:19]
	v_lshl_add_u64 v[16:17], v[16:17], 0, v[178:179]
	v_cvt_pk_bf16_f32 v13, v18, v19
	global_store_dwordx4 v[16:17], v[10:13], off sc1
	v_lshlrev_b32_e32 v18, 16, v112
	v_and_b32_e32 v19, 0xffff0000, v112
	v_lshlrev_b32_e32 v10, 16, v110
	v_and_b32_e32 v11, 0xffff0000, v110
	v_lshlrev_b32_e32 v12, 16, v111
	v_and_b32_e32 v13, 0xffff0000, v111
	v_lshlrev_b32_e32 v20, 16, v113
	v_and_b32_e32 v21, 0xffff0000, v113
	v_pk_fma_f32 v[12:13], v[56:57], v[172:173], v[12:13]
	v_pk_fma_f32 v[10:11], v[54:55], v[30:31], v[10:11]
	v_pk_fma_f32 v[20:21], v[52:53], v[26:27], v[20:21]
	v_pk_fma_f32 v[18:19], v[50:51], v[24:25], v[18:19]
	v_cvt_pk_bf16_f32 v10, v10, v11
	v_cvt_pk_bf16_f32 v11, v12, v13
	s_nop 0
	v_cvt_pk_bf16_f32 v12, v18, v19
	v_cvt_pk_bf16_f32 v13, v20, v21
	global_store_dwordx4 v[16:17], v[10:13], off offset:256 sc1
	s_nop 1
	v_lshlrev_b32_e32 v10, 16, v6
	v_and_b32_e32 v11, 0xffff0000, v6
	v_lshlrev_b32_e32 v6, 16, v7
	v_and_b32_e32 v7, 0xffff0000, v7
	v_lshlrev_b32_e32 v12, 16, v8
	v_and_b32_e32 v13, 0xffff0000, v8
	v_lshlrev_b32_e32 v8, 16, v9
	v_and_b32_e32 v9, 0xffff0000, v9
	v_pk_fma_f32 v[16:17], v[48:49], v[176:177], v[6:7]
	v_pk_fma_f32 v[6:7], v[46:47], v[174:175], v[10:11]
	v_pk_fma_f32 v[10:11], v[44:45], v[32:33], v[8:9]
	v_pk_fma_f32 v[8:9], v[42:43], v[28:29], v[12:13]
	v_cvt_pk_bf16_f32 v6, v6, v7
	v_cvt_pk_bf16_f32 v7, v16, v17
	s_nop 0
	v_cvt_pk_bf16_f32 v8, v8, v9
	v_cvt_pk_bf16_f32 v9, v10, v11
	v_lshl_add_u64 v[10:11], s[50:51], 0, v[14:15]
	v_lshl_add_u64 v[10:11], v[10:11], 0, v[178:179]
	global_store_dwordx4 v[10:11], v[6:9], off sc1
	s_nop 1
	v_lshlrev_b32_e32 v6, 16, v2
	v_and_b32_e32 v7, 0xffff0000, v2
	v_lshlrev_b32_e32 v2, 16, v3
	v_and_b32_e32 v3, 0xffff0000, v3
	v_lshlrev_b32_e32 v8, 16, v4
	v_and_b32_e32 v9, 0xffff0000, v4
	v_lshlrev_b32_e32 v4, 16, v5
	v_and_b32_e32 v5, 0xffff0000, v5
	v_pk_fma_f32 v[10:11], v[40:41], v[172:173], v[2:3]
	v_pk_fma_f32 v[2:3], v[38:39], v[30:31], v[6:7]
	v_pk_fma_f32 v[6:7], v[36:37], v[26:27], v[4:5]
	v_pk_fma_f32 v[4:5], v[34:35], v[24:25], v[8:9]
	v_cvt_pk_bf16_f32 v2, v2, v3
	v_cvt_pk_bf16_f32 v3, v10, v11
	s_nop 0
	v_cvt_pk_bf16_f32 v4, v4, v5
	v_cvt_pk_bf16_f32 v5, v6, v7

.LBB0_1300:
	v_lshl_add_u64 v[2:3], s[58:59], 0, v[60:61]
	v_add_co_u32_e32 v4, vcc, 0x11100000, v2
	v_lshl_add_u64 v[158:159], s[58:59], 0, v[58:59]
	s_nop 0
	v_addc_co_u32_e32 v5, vcc, 0, v3, vcc
	global_load_dwordx2 v[94:95], v[4:5], off nt
	v_add_co_u32_e32 v96, vcc, 0x11101000, v2
	s_waitcnt vmcnt(0)
	v_and_b32_e32 v157, 0xffff0000, v94
	v_addc_co_u32_e32 v97, vcc, 0, v3, vcc
	global_load_dwordx2 v[98:99], v[96:97], off nt
	global_load_dwordx2 v[100:101], v[4:5], off offset:512 nt
	global_load_dwordx2 v[106:107], v[96:97], off offset:512 nt
	global_load_dwordx2 v[108:109], v[4:5], off offset:1024 nt
	global_load_dwordx2 v[110:111], v[96:97], off offset:1024 nt
	global_load_dwordx2 v[20:21], v[4:5], off offset:1536 nt
	global_load_dwordx2 v[18:19], v[96:97], off offset:1536 nt
	global_load_dwordx2 v[16:17], v[4:5], off offset:2048 nt
	global_load_dwordx2 v[14:15], v[96:97], off offset:2048 nt
	global_load_dwordx2 v[12:13], v[4:5], off offset:2560 nt
	global_load_dwordx2 v[10:11], v[96:97], off offset:2560 nt
	global_load_dwordx2 v[8:9], v[4:5], off offset:3072 nt
	global_load_dwordx2 v[6:7], v[96:97], off offset:3072 nt
	global_load_dwordx2 v[2:3], v[4:5], off offset:3584 nt
	s_nop 0
	global_load_dwordx2 v[4:5], v[96:97], off offset:3584 nt
	v_and_b32_e32 v155, 0xffff0000, v95
	v_lshlrev_b32_e32 v156, 16, v94
	v_lshlrev_b32_e32 v154, 16, v95
	v_mul_f32_e32 v47, v157, v157
	v_mul_f32_e32 v49, v155, v155
	v_fmac_f32_e32 v47, v156, v156
	v_fmac_f32_e32 v49, v154, v154
	v_add_f32_e32 v47, v47, v49
	s_waitcnt vmcnt(14)
	v_and_b32_e32 v153, 0xffff0000, v98
	v_and_b32_e32 v119, 0xffff0000, v99
	v_lshlrev_b32_e32 v152, 16, v98
	v_lshlrev_b32_e32 v118, 16, v99
	v_mul_f32_e32 v49, v153, v153
	v_mul_f32_e32 v51, v119, v119
	v_fmac_f32_e32 v49, v152, v152
	v_fmac_f32_e32 v51, v118, v118
	s_waitcnt vmcnt(13)
	v_and_b32_e32 v151, 0xffff0000, v100
	v_and_b32_e32 v149, 0xffff0000, v101
	v_add_f32_e32 v49, v49, v51
	v_lshlrev_b32_e32 v150, 16, v100
	v_lshlrev_b32_e32 v148, 16, v101
	v_mul_f32_e32 v51, v151, v151
	v_mul_f32_e32 v53, v149, v149
	v_fmac_f32_e32 v51, v150, v150
	v_fmac_f32_e32 v53, v148, v148
	s_waitcnt vmcnt(12)
	v_and_b32_e32 v147, 0xffff0000, v106
	v_and_b32_e32 v145, 0xffff0000, v107
	v_add_f32_e32 v51, v51, v53
	v_lshlrev_b32_e32 v146, 16, v106
	v_lshlrev_b32_e32 v144, 16, v107
	v_add_f32_e32 v47, v47, v51
	v_mul_f32_e32 v51, v147, v147
	v_mul_f32_e32 v53, v145, v145
	v_fmac_f32_e32 v51, v146, v146
	v_fmac_f32_e32 v53, v144, v144
	v_add_f32_e32 v51, v51, v53
	s_waitcnt vmcnt(11)
	v_and_b32_e32 v143, 0xffff0000, v108
	v_and_b32_e32 v141, 0xffff0000, v109
	v_add_f32_e32 v49, v49, v51
	v_lshlrev_b32_e32 v142, 16, v108
	v_lshlrev_b32_e32 v140, 16, v109
	v_mul_f32_e32 v51, v143, v143
	v_mul_f32_e32 v53, v141, v141
	v_fmac_f32_e32 v51, v142, v142
	v_fmac_f32_e32 v53, v140, v140
	s_waitcnt vmcnt(9)
	v_and_b32_e32 v131, 0xffff0000, v20
	v_and_b32_e32 v129, 0xffff0000, v21
	v_and_b32_e32 v139, 0xffff0000, v110
	v_and_b32_e32 v137, 0xffff0000, v111
	v_add_f32_e32 v51, v51, v53
	v_lshlrev_b32_e32 v130, 16, v20
	v_lshlrev_b32_e32 v128, 16, v21
	s_waitcnt vmcnt(8)
	v_lshlrev_b32_e32 v132, 16, v18
	v_and_b32_e32 v133, 0xffff0000, v18
	v_lshlrev_b32_e32 v134, 16, v19
	v_and_b32_e32 v135, 0xffff0000, v19
	v_mul_f32_e32 v18, v131, v131
	v_mul_f32_e32 v19, v129, v129
	s_waitcnt vmcnt(7)
	v_and_b32_e32 v127, 0xffff0000, v16
	v_and_b32_e32 v125, 0xffff0000, v17
	v_lshlrev_b32_e32 v138, 16, v110
	v_lshlrev_b32_e32 v136, 16, v111
	v_add_f32_e32 v47, v47, v51
	v_mul_f32_e32 v51, v139, v139
	v_mul_f32_e32 v53, v137, v137
	v_fmac_f32_e32 v18, v130, v130
	v_fmac_f32_e32 v19, v128, v128
	v_lshlrev_b32_e32 v126, 16, v16
	v_lshlrev_b32_e32 v124, 16, v17
	s_waitcnt vmcnt(6)
	v_lshlrev_b32_e32 v122, 16, v14
	v_and_b32_e32 v123, 0xffff0000, v14
	v_lshlrev_b32_e32 v120, 16, v15
	v_and_b32_e32 v121, 0xffff0000, v15
	v_mul_f32_e32 v14, v127, v127
	v_mul_f32_e32 v15, v125, v125
	v_fmac_f32_e32 v51, v138, v138
	v_fmac_f32_e32 v53, v136, v136
	v_add_f32_e32 v18, v18, v19
	v_mul_f32_e32 v19, v133, v133
	v_mul_f32_e32 v20, v135, v135
	v_fmac_f32_e32 v14, v126, v126
	v_fmac_f32_e32 v15, v124, v124
	v_add_f32_e32 v51, v51, v53
	v_fmac_f32_e32 v19, v132, v132
	v_fmac_f32_e32 v20, v134, v134
	v_add_f32_e32 v14, v14, v15
	v_mul_f32_e32 v15, v123, v123
	v_mul_f32_e32 v16, v121, v121
	v_add_f32_e32 v49, v49, v51
	v_add_f32_e32 v19, v19, v20
	v_fmac_f32_e32 v15, v122, v122
	v_fmac_f32_e32 v16, v120, v120
	s_waitcnt vmcnt(5)
	v_and_b32_e32 v117, 0xffff0000, v12
	v_and_b32_e32 v115, 0xffff0000, v13
	v_add_f32_e32 v18, v47, v18
	v_add_f32_e32 v19, v49, v19
	v_add_f32_e32 v15, v15, v16
	v_lshlrev_b32_e32 v116, 16, v12
	v_lshlrev_b32_e32 v114, 16, v13
	s_waitcnt vmcnt(4)
	v_lshlrev_b32_e32 v112, 16, v10
	v_and_b32_e32 v113, 0xffff0000, v10
	v_lshlrev_b32_e32 v110, 16, v11
	v_and_b32_e32 v111, 0xffff0000, v11
	v_mul_f32_e32 v10, v117, v117
	v_mul_f32_e32 v11, v115, v115
	s_waitcnt vmcnt(3)
	v_and_b32_e32 v109, 0xffff0000, v8
	v_and_b32_e32 v107, 0xffff0000, v9
	v_add_f32_e32 v14, v18, v14
	v_add_f32_e32 v15, v19, v15
	v_fmac_f32_e32 v10, v116, v116
	v_fmac_f32_e32 v11, v114, v114
	v_lshlrev_b32_e32 v108, 16, v8
	v_lshlrev_b32_e32 v106, 16, v9
	s_waitcnt vmcnt(2)
	v_lshlrev_b32_e32 v20, 16, v6
	v_and_b32_e32 v21, 0xffff0000, v6
	v_lshlrev_b32_e32 v18, 16, v7
	v_and_b32_e32 v19, 0xffff0000, v7
	v_mul_f32_e32 v6, v109, v109
	v_mul_f32_e32 v7, v107, v107
	s_waitcnt vmcnt(1)
	v_and_b32_e32 v101, 0xffff0000, v2
	v_and_b32_e32 v99, 0xffff0000, v3
	v_add_f32_e32 v10, v10, v11
	v_fmac_f32_e32 v6, v108, v108
	v_fmac_f32_e32 v7, v106, v106
	v_lshlrev_b32_e32 v100, 16, v2
	v_lshlrev_b32_e32 v98, 16, v3
	v_mul_f32_e32 v2, v101, v101
	v_mul_f32_e32 v3, v99, v99
	v_add_f32_e32 v10, v14, v10
	v_add_f32_e32 v6, v6, v7
	s_waitcnt vmcnt(0)
	v_and_b32_e32 v97, 0xffff0000, v4
	v_and_b32_e32 v95, 0xffff0000, v5
	v_fmac_f32_e32 v2, v100, v100
	v_fmac_f32_e32 v3, v98, v98
	v_add_f32_e32 v6, v10, v6
	v_lshlrev_b32_e32 v96, 16, v4
	v_lshlrev_b32_e32 v94, 16, v5
	v_add_f32_e32 v2, v2, v3
	v_mul_f32_e32 v3, v97, v97
	v_mul_f32_e32 v4, v95, v95
	v_add_f32_e32 v2, v6, v2
	v_fmac_f32_e32 v3, v96, v96
	v_fmac_f32_e32 v4, v94, v94
	v_add_f32_e32 v3, v3, v4
	ds_bpermute_b32 v4, v23, v2
	v_mul_f32_e32 v11, v113, v113
	v_mul_f32_e32 v12, v111, v111
	v_fmac_f32_e32 v11, v112, v112
	v_fmac_f32_e32 v12, v110, v110
	s_waitcnt lgkmcnt(0)
	v_add_f32_e32 v2, v2, v4
	ds_bpermute_b32 v4, v25, v2
	v_mul_f32_e32 v7, v21, v21
	v_mul_f32_e32 v8, v19, v19
	v_add_f32_e32 v11, v11, v12
	v_fmac_f32_e32 v7, v20, v20
	s_waitcnt lgkmcnt(0)
	v_add_f32_e32 v2, v2, v4
	ds_bpermute_b32 v4, v43, v2
	v_fmac_f32_e32 v8, v18, v18
	v_add_f32_e32 v11, v15, v11
	v_add_f32_e32 v7, v7, v8
	v_add_f32_e32 v7, v11, v7
	s_waitcnt lgkmcnt(0)
	v_add_f32_e32 v2, v2, v4
	ds_bpermute_b32 v4, v103, v2
	v_add_f32_e32 v3, v7, v3
	v_mov_b32_e32 v51, 0
	s_waitcnt lgkmcnt(0)
	v_add_f32_e32 v2, v2, v4
	v_mov_b32_e32 v4, v2
	s_nop 1
	v_permlane16_swap_b32_e32 v2, v4
	v_add_f32_e32 v2, v2, v4
	v_mov_b32_e32 v4, v2
	s_nop 1
	v_permlane32_swap_b32_e32 v2, v4
	v_add_f32_e32 v2, v2, v4
	v_fmamk_f32 v2, v2, 0x3a000000, v228
	v_cmp_gt_f32_e32 vcc, s82, v2
	v_mul_f32_e32 v4, 0x4f800000, v2
	s_nop 0
	v_cndmask_b32_e32 v2, v2, v4, vcc
	v_sqrt_f32_e32 v4, v2
	s_nop 0
	v_add_u32_e32 v5, -1, v4
	v_fma_f32 v6, -v5, v4, v2
	v_cmp_ge_f32_e64 s[44:45], 0, v6
	v_add_u32_e32 v6, 1, v4
	s_nop 0
	v_cndmask_b32_e64 v5, v4, v5, s[44:45]
	v_fma_f32 v4, -v6, v4, v2
	v_cmp_lt_f32_e64 s[44:45], 0, v4
	s_nop 1
	v_cndmask_b32_e64 v4, v5, v6, s[44:45]
	v_mul_f32_e32 v5, 0x37800000, v4
	v_cndmask_b32_e32 v4, v4, v5, vcc
	v_cmp_class_f32_e32 vcc, v2, v229
	s_nop 1
	v_cndmask_b32_e32 v2, v4, v2, vcc
	ds_bpermute_b32 v4, v23, v3
	s_waitcnt lgkmcnt(0)
	v_add_f32_e32 v3, v3, v4
	ds_bpermute_b32 v4, v25, v3
	s_waitcnt lgkmcnt(0)
	v_add_f32_e32 v3, v3, v4
	ds_bpermute_b32 v4, v43, v3
	s_waitcnt lgkmcnt(0)
	v_add_f32_e32 v3, v3, v4
	ds_bpermute_b32 v4, v103, v3
	s_waitcnt lgkmcnt(0)
	v_add_f32_e32 v3, v3, v4
	v_mov_b32_e32 v4, v3
	s_nop 1
	v_permlane16_swap_b32_e32 v3, v4
	v_add_f32_e32 v3, v3, v4
	v_mov_b32_e32 v4, v3
	s_nop 1
	v_permlane32_swap_b32_e32 v3, v4
	v_add_f32_e32 v3, v3, v4
	v_fmamk_f32 v3, v3, 0x3a000000, v228
	v_cmp_gt_f32_e32 vcc, s82, v3
	v_mul_f32_e32 v4, 0x4f800000, v3
	s_nop 0
	v_cndmask_b32_e32 v3, v3, v4, vcc
	v_sqrt_f32_e32 v4, v3
	s_nop 0
	v_add_u32_e32 v5, -1, v4
	v_fma_f32 v6, -v5, v4, v3
	v_cmp_ge_f32_e64 s[44:45], 0, v6
	v_add_u32_e32 v6, 1, v4
	s_nop 0
	v_cndmask_b32_e64 v5, v4, v5, s[44:45]
	v_fma_f32 v4, -v6, v4, v3
	v_cmp_lt_f32_e64 s[44:45], 0, v4
	s_nop 1
	v_cndmask_b32_e64 v4, v5, v6, s[44:45]
	v_mul_f32_e32 v5, 0x37800000, v4
	v_cndmask_b32_e32 v4, v4, v5, vcc
	v_cmp_class_f32_e32 vcc, v3, v229
	s_nop 1
	v_cndmask_b32_e32 v3, v4, v3, vcc
	v_div_scale_f32 v4, s[4:5], v2, v2, 1.0
	v_rcp_f32_e32 v5, v4
	s_nop 0
	v_fma_f32 v6, -v4, v5, 1.0
	v_fmac_f32_e32 v5, v6, v5
	v_div_scale_f32 v6, vcc, 1.0, v2, 1.0
	v_mul_f32_e32 v7, v6, v5
	v_fma_f32 v8, -v4, v7, v6
	v_fmac_f32_e32 v7, v8, v5
	v_fma_f32 v4, -v4, v7, v6
	v_div_fmas_f32 v4, v4, v5, v7
	v_div_fixup_f32 v102, v4, v2, 1.0
	v_div_scale_f32 v2, s[4:5], v3, v3, 1.0
	v_rcp_f32_e32 v4, v2
	v_pk_mul_f32 v[156:157], v[102:103], v[156:157] op_sel_hi:[0,1]
	v_pk_mul_f32 v[154:155], v[102:103], v[154:155] op_sel_hi:[0,1]
	v_fma_f32 v5, -v2, v4, 1.0
	v_fmac_f32_e32 v4, v5, v4
	v_div_scale_f32 v5, vcc, 1.0, v3, 1.0
	v_mul_f32_e32 v6, v5, v4
	v_fma_f32 v7, -v2, v6, v5
	v_fmac_f32_e32 v6, v7, v4
	v_fma_f32 v2, -v2, v6, v5
	v_div_fmas_f32 v2, v2, v4, v6
	v_div_fixup_f32 v104, v2, v3, 1.0
	global_load_dwordx4 v[2:5], v[26:27], off
	global_load_dwordx4 v[6:9], v[62:63], off
	global_load_dwordx4 v[14:17], v[64:65], off
	v_pk_mul_f32 v[152:153], v[104:105], v[152:153] op_sel_hi:[0,1]
	v_pk_mul_f32 v[118:119], v[104:105], v[118:119] op_sel_hi:[0,1]
	s_waitcnt vmcnt(1)
	v_pk_add_f32 v[8:9], v[8:9], 1.0 op_sel_hi:[1,0]
	v_pk_add_f32 v[6:7], v[6:7], 1.0 op_sel_hi:[1,0]
	v_pk_mul_f32 v[160:161], v[4:5], v[8:9]
	v_pk_mul_f32 v[162:163], v[2:3], v[6:7]
	global_load_dwordx4 v[2:5], v[66:67], off
	global_load_dwordx4 v[10:13], v[68:69], off
	global_load_dwordx4 v[6:9], v[28:29], off
	s_waitcnt vmcnt(3)
	v_pk_fma_f32 v[156:157], v[162:163], v[156:157], v[14:15]
	v_pk_fma_f32 v[154:155], v[160:161], v[154:155], v[16:17]
	v_med3_f32 v47, v156, s33, v233
	v_med3_f32 v49, v157, s33, v233
	v_cvt_pk_fp8_f32 v51, v47, v49
	ds_read_b128 v[206:209], v105
	ds_read_b128 v[238:241], v105 offset:2048
	v_med3_f32 v47, v154, s33, v233
	v_med3_f32 v49, v155, s33, v233
	v_cvt_pk_fp8_f32 v51, v47, v49 op_sel:[0,0,1]
	v_pk_fma_f32 v[16:17], v[160:161], v[118:119], v[16:17]
	v_pk_fma_f32 v[14:15], v[162:163], v[152:153], v[14:15]
	v_add_co_u32_e32 v118, vcc, s80, v158
	s_waitcnt lgkmcnt(1)
	v_fma_f32 v224, v156, v206, 0
	v_addc_co_u32_e32 v119, vcc, 0, v159, vcc
	v_fma_f32 v223, v156, v207, 0
	v_fma_f32 v221, v156, v208, 0
	v_fma_f32 v217, v156, v209, 0
	v_fma_f32 v225, v14, v206, 0
	v_fma_f32 v222, v14, v207, 0
	v_fma_f32 v219, v14, v208, 0
	v_fma_f32 v215, v14, v209, 0
	ds_read_b128 v[206:209], v105 offset:1024
	global_store_dword v[118:119], v51, off
	v_med3_f32 v47, v14, s33, v233
	v_med3_f32 v49, v15, s33, v233
	v_mov_b32_e32 v51, 0
	v_cvt_pk_fp8_f32 v51, v47, v49
	v_med3_f32 v47, v16, s33, v233
	v_med3_f32 v49, v17, s33, v233
	s_waitcnt lgkmcnt(0)
	v_fma_f32 v220, v156, v206, 0
	v_fma_f32 v216, v156, v207, 0
	v_fma_f32 v213, v156, v208, 0
	v_fma_f32 v211, v156, v209, 0
	v_fma_f32 v218, v14, v206, 0
	v_fma_f32 v214, v14, v207, 0
	v_fma_f32 v212, v14, v208, 0
	v_fma_f32 v210, v14, v209, 0
	v_fma_f32 v209, v156, v238, 0
	v_fma_f32 v207, v156, v239, 0
	v_fma_f32 v205, v156, v240, 0
	v_fma_f32 v153, v156, v241, 0
	v_fma_f32 v208, v14, v238, 0
	v_fma_f32 v206, v14, v239, 0
	v_fma_f32 v158, v14, v240, 0
	v_fma_f32 v57, v14, v241, 0
	ds_read_b128 v[238:241], v105 offset:3072
	v_cvt_pk_fp8_f32 v51, v47, v49 op_sel:[0,0,1]
	global_store_dword v[118:119], v51, off offset:2048
	s_waitcnt lgkmcnt(0)
	v_fma_f32 v159, v156, v238, 0
	v_fma_f32 v152, v156, v239, 0
	v_fma_f32 v53, v156, v240, 0
	v_fma_f32 v49, v156, v241, 0
	v_fma_f32 v156, v14, v238, 0
	v_fma_f32 v55, v14, v239, 0
	v_fma_f32 v51, v14, v240, 0
	v_fma_f32 v47, v14, v241, 0
	ds_read_b128 v[238:241], v105 offset:4096
	s_waitcnt lgkmcnt(0)
	v_fmac_f32_e32 v224, v157, v238
	v_fmac_f32_e32 v223, v157, v239
	v_fmac_f32_e32 v221, v157, v240
	v_fmac_f32_e32 v217, v157, v241
	v_fmac_f32_e32 v225, v15, v238
	v_fmac_f32_e32 v222, v15, v239
	v_fmac_f32_e32 v219, v15, v240
	v_fmac_f32_e32 v215, v15, v241
	ds_read_b128 v[238:241], v105 offset:5120
	s_waitcnt lgkmcnt(0)
	v_fmac_f32_e32 v220, v157, v238
	v_fmac_f32_e32 v216, v157, v239
	v_fmac_f32_e32 v213, v157, v240
	v_fmac_f32_e32 v211, v157, v241
	v_fmac_f32_e32 v218, v15, v238
	v_fmac_f32_e32 v214, v15, v239
	v_fmac_f32_e32 v212, v15, v240
	v_fmac_f32_e32 v210, v15, v241
	ds_read_b128 v[238:241], v105 offset:6144
	s_waitcnt lgkmcnt(0)
	v_fmac_f32_e32 v209, v157, v238
	v_fmac_f32_e32 v207, v157, v239
	v_fmac_f32_e32 v205, v157, v240
	v_fmac_f32_e32 v153, v157, v241
	v_fmac_f32_e32 v208, v15, v238
	v_fmac_f32_e32 v206, v15, v239
	v_fmac_f32_e32 v158, v15, v240
	v_fmac_f32_e32 v57, v15, v241
	ds_read_b128 v[238:241], v105 offset:7168
	s_waitcnt lgkmcnt(0)
	v_fmac_f32_e32 v159, v157, v238
	v_fmac_f32_e32 v152, v157, v239
	v_fmac_f32_e32 v53, v157, v240
	v_fmac_f32_e32 v49, v157, v241
	v_fmac_f32_e32 v156, v15, v238
	v_fmac_f32_e32 v55, v15, v239
	v_fmac_f32_e32 v51, v15, v240
	v_fmac_f32_e32 v47, v15, v241
	ds_read_b128 v[238:241], v105 offset:8192
	s_waitcnt lgkmcnt(0)
	v_fmac_f32_e32 v224, v154, v238
	v_fmac_f32_e32 v223, v154, v239
	v_fmac_f32_e32 v221, v154, v240
	v_fmac_f32_e32 v217, v154, v241
	v_fmac_f32_e32 v225, v16, v238
	v_fmac_f32_e32 v222, v16, v239
	v_fmac_f32_e32 v219, v16, v240
	v_fmac_f32_e32 v215, v16, v241
	ds_read_b128 v[238:241], v105 offset:9216
	s_waitcnt lgkmcnt(0)
	v_fmac_f32_e32 v220, v154, v238
	v_fmac_f32_e32 v216, v154, v239
	v_fmac_f32_e32 v213, v154, v240
	v_fmac_f32_e32 v211, v154, v241
	v_fmac_f32_e32 v218, v16, v238
	v_fmac_f32_e32 v214, v16, v239
	v_fmac_f32_e32 v212, v16, v240
	v_fmac_f32_e32 v210, v16, v241
	ds_read_b128 v[238:241], v105 offset:10240
	s_waitcnt lgkmcnt(0)
	v_fmac_f32_e32 v209, v154, v238
	v_fmac_f32_e32 v207, v154, v239
	v_fmac_f32_e32 v205, v154, v240
	v_fmac_f32_e32 v153, v154, v241
	v_fmac_f32_e32 v208, v16, v238
	v_fmac_f32_e32 v206, v16, v239
	v_fmac_f32_e32 v158, v16, v240
	v_fmac_f32_e32 v57, v16, v241
	ds_read_b128 v[238:241], v105 offset:11264
	s_waitcnt lgkmcnt(0)
	v_fmac_f32_e32 v159, v154, v238
	v_fmac_f32_e32 v152, v154, v239
	v_fmac_f32_e32 v53, v154, v240
	v_fmac_f32_e32 v49, v154, v241
	v_fmac_f32_e32 v156, v16, v238
	v_fmac_f32_e32 v55, v16, v239
	v_fmac_f32_e32 v51, v16, v240
	v_fmac_f32_e32 v47, v16, v241
	ds_read_b128 v[238:241], v105 offset:12288
	s_waitcnt lgkmcnt(0)
	v_fmac_f32_e32 v224, v155, v238
	v_fmac_f32_e32 v223, v155, v239
	v_fmac_f32_e32 v221, v155, v240
	v_fmac_f32_e32 v217, v155, v241
	v_fmac_f32_e32 v225, v17, v238
	v_fmac_f32_e32 v222, v17, v239
	v_fmac_f32_e32 v219, v17, v240
	v_fmac_f32_e32 v215, v17, v241
	ds_read_b128 v[238:241], v105 offset:13312
	s_waitcnt lgkmcnt(0)
	v_fmac_f32_e32 v220, v155, v238
	v_fmac_f32_e32 v216, v155, v239
	v_fmac_f32_e32 v213, v155, v240
	v_fmac_f32_e32 v211, v155, v241
	v_fmac_f32_e32 v218, v17, v238
	v_fmac_f32_e32 v214, v17, v239
	v_fmac_f32_e32 v212, v17, v240
	v_fmac_f32_e32 v210, v17, v241
	ds_read_b128 v[238:241], v105 offset:14336
	s_waitcnt lgkmcnt(0)
	v_fmac_f32_e32 v209, v155, v238
	v_fmac_f32_e32 v207, v155, v239
	v_fmac_f32_e32 v205, v155, v240
	v_fmac_f32_e32 v153, v155, v241
	v_fmac_f32_e32 v208, v17, v238
	v_fmac_f32_e32 v206, v17, v239
	v_fmac_f32_e32 v158, v17, v240
	v_fmac_f32_e32 v57, v17, v241
	ds_read_b128 v[238:241], v105 offset:15360
	s_waitcnt lgkmcnt(0)
	v_fmac_f32_e32 v53, v155, v240
	v_fmac_f32_e32 v55, v17, v239
	v_fmac_f32_e32 v51, v17, v240
	v_fmac_f32_e32 v159, v155, v238
	v_fmac_f32_e32 v152, v155, v239
	v_fmac_f32_e32 v49, v155, v241
	v_fmac_f32_e32 v156, v17, v238
	v_fmac_f32_e32 v47, v17, v241
	s_waitcnt vmcnt(3)
	v_pk_add_f32 v[10:11], v[10:11], 1.0 op_sel_hi:[1,0]
	v_pk_mul_f32 v[150:151], v[102:103], v[150:151] op_sel_hi:[0,1]
	s_waitcnt vmcnt(2)
	v_pk_mul_f32 v[154:155], v[6:7], v[10:11]
	v_pk_add_f32 v[12:13], v[12:13], 1.0 op_sel_hi:[1,0]
	v_pk_fma_f32 v[160:161], v[150:151], v[154:155], v[2:3]
	v_pk_mul_f32 v[146:147], v[104:105], v[146:147] op_sel_hi:[0,1]
	v_pk_mul_f32 v[16:17], v[8:9], v[12:13]
	v_pk_mul_f32 v[14:15], v[102:103], v[148:149] op_sel_hi:[0,1]
	v_pk_mul_f32 v[144:145], v[104:105], v[144:145] op_sel_hi:[0,1]
	v_pk_fma_f32 v[154:155], v[154:155], v[146:147], v[2:3]
	v_med3_f32 v2, v160, s33, v233
	v_med3_f32 v3, v161, s33, v233
	v_mov_b32_e32 v148, 0
	v_pk_fma_f32 v[14:15], v[14:15], v[16:17], v[4:5]
	v_pk_fma_f32 v[16:17], v[16:17], v[144:145], v[4:5]
	v_cvt_pk_fp8_f32 v148, v2, v3
	v_med3_f32 v4, v154, s33, v233
	v_med3_f32 v5, v155, s33, v233
	v_mov_b32_e32 v149, 0
	v_cvt_pk_fp8_f32 v149, v4, v5
	v_med3_f32 v2, v14, s33, v233
	v_med3_f32 v3, v15, s33, v233
	v_cvt_pk_fp8_f32 v148, v2, v3 op_sel:[0,0,1]
	v_med3_f32 v2, v16, s33, v233
	v_med3_f32 v3, v17, s33, v233
	global_load_dwordx4 v[6:9], v[70:71], off
	global_load_dwordx4 v[10:13], v[72:73], off
	v_cvt_pk_fp8_f32 v149, v2, v3 op_sel:[0,0,1]
	global_load_dwordx4 v[2:5], v[30:31], off
	ds_read_b128 v[144:147], v105 offset:16384
	global_store_dword v[118:119], v148, off offset:256
	global_store_dword v[118:119], v149, off offset:2304
	ds_read_b128 v[148:151], v105 offset:17408
	s_waitcnt lgkmcnt(1)
	v_fmac_f32_e32 v224, v160, v144
	v_fmac_f32_e32 v223, v160, v145
	v_fmac_f32_e32 v221, v160, v146
	v_fmac_f32_e32 v217, v160, v147
	v_fmac_f32_e32 v225, v154, v144
	v_fmac_f32_e32 v222, v154, v145
	v_fmac_f32_e32 v219, v154, v146
	v_fmac_f32_e32 v215, v154, v147
	ds_read_b128 v[144:147], v105 offset:18432
	s_waitcnt lgkmcnt(1)
	v_fmac_f32_e32 v220, v160, v148
	v_fmac_f32_e32 v216, v160, v149
	v_fmac_f32_e32 v213, v160, v150
	v_fmac_f32_e32 v211, v160, v151
	v_fmac_f32_e32 v218, v154, v148
	v_fmac_f32_e32 v214, v154, v149
	v_fmac_f32_e32 v212, v154, v150
	v_fmac_f32_e32 v210, v154, v151
	ds_read_b128 v[148:151], v105 offset:19456
	s_waitcnt lgkmcnt(1)
	v_fmac_f32_e32 v209, v160, v144
	v_fmac_f32_e32 v207, v160, v145
	v_fmac_f32_e32 v205, v160, v146
	v_fmac_f32_e32 v153, v160, v147
	v_fmac_f32_e32 v208, v154, v144
	v_fmac_f32_e32 v206, v154, v145
	v_fmac_f32_e32 v158, v154, v146
	v_fmac_f32_e32 v57, v154, v147
	ds_read_b128 v[144:147], v105 offset:20480
	s_waitcnt lgkmcnt(1)
	v_fmac_f32_e32 v159, v160, v148
	v_fmac_f32_e32 v152, v160, v149
	v_fmac_f32_e32 v53, v160, v150
	v_fmac_f32_e32 v49, v160, v151
	v_fmac_f32_e32 v156, v154, v148
	v_fmac_f32_e32 v55, v154, v149
	v_fmac_f32_e32 v51, v154, v150
	v_fmac_f32_e32 v47, v154, v151
	ds_read_b128 v[148:151], v105 offset:21504
	s_waitcnt lgkmcnt(1)
	v_fmac_f32_e32 v224, v161, v144
	v_fmac_f32_e32 v223, v161, v145
	v_fmac_f32_e32 v221, v161, v146
	v_fmac_f32_e32 v217, v161, v147
	v_fmac_f32_e32 v225, v155, v144
	v_fmac_f32_e32 v222, v155, v145
	v_fmac_f32_e32 v219, v155, v146
	v_fmac_f32_e32 v215, v155, v147
	ds_read_b128 v[144:147], v105 offset:22528
	s_waitcnt lgkmcnt(1)
	v_fmac_f32_e32 v220, v161, v148
	v_fmac_f32_e32 v216, v161, v149
	v_fmac_f32_e32 v213, v161, v150
	v_fmac_f32_e32 v211, v161, v151
	v_fmac_f32_e32 v218, v155, v148
	v_fmac_f32_e32 v214, v155, v149
	v_fmac_f32_e32 v212, v155, v150
	v_fmac_f32_e32 v210, v155, v151
	ds_read_b128 v[148:151], v105 offset:23552
	s_waitcnt lgkmcnt(1)
	v_fmac_f32_e32 v209, v161, v144
	v_fmac_f32_e32 v207, v161, v145
	v_fmac_f32_e32 v205, v161, v146
	v_fmac_f32_e32 v153, v161, v147
	v_fmac_f32_e32 v208, v155, v144
	v_fmac_f32_e32 v206, v155, v145
	v_fmac_f32_e32 v158, v155, v146
	v_fmac_f32_e32 v57, v155, v147
	ds_read_b128 v[144:147], v105 offset:24576
	s_waitcnt lgkmcnt(1)
	v_fmac_f32_e32 v159, v161, v148
	v_fmac_f32_e32 v152, v161, v149
	v_fmac_f32_e32 v53, v161, v150
	v_fmac_f32_e32 v49, v161, v151
	v_fmac_f32_e32 v156, v155, v148
	v_fmac_f32_e32 v55, v155, v149
	v_fmac_f32_e32 v51, v155, v150
	v_fmac_f32_e32 v47, v155, v151
	ds_read_b128 v[148:151], v105 offset:25600
	s_waitcnt lgkmcnt(1)
	v_fmac_f32_e32 v224, v14, v144
	v_fmac_f32_e32 v223, v14, v145
	v_fmac_f32_e32 v221, v14, v146
	v_fmac_f32_e32 v217, v14, v147
	v_fmac_f32_e32 v225, v16, v144
	v_fmac_f32_e32 v222, v16, v145
	v_fmac_f32_e32 v219, v16, v146
	v_fmac_f32_e32 v215, v16, v147
	ds_read_b128 v[144:147], v105 offset:26624
	s_waitcnt lgkmcnt(1)
	v_fmac_f32_e32 v220, v14, v148
	v_fmac_f32_e32 v216, v14, v149
	v_fmac_f32_e32 v213, v14, v150
	v_fmac_f32_e32 v211, v14, v151
	v_fmac_f32_e32 v218, v16, v148
	v_fmac_f32_e32 v214, v16, v149
	v_fmac_f32_e32 v212, v16, v150
	v_fmac_f32_e32 v210, v16, v151
	ds_read_b128 v[148:151], v105 offset:27648
	s_waitcnt lgkmcnt(1)
	v_fmac_f32_e32 v209, v14, v144
	v_fmac_f32_e32 v207, v14, v145
	v_fmac_f32_e32 v205, v14, v146
	v_fmac_f32_e32 v153, v14, v147
	v_fmac_f32_e32 v208, v16, v144
	v_fmac_f32_e32 v206, v16, v145
	v_fmac_f32_e32 v158, v16, v146
	v_fmac_f32_e32 v57, v16, v147
	ds_read_b128 v[144:147], v105 offset:28672
	s_waitcnt lgkmcnt(1)
	v_fmac_f32_e32 v159, v14, v148
	v_fmac_f32_e32 v152, v14, v149
	v_fmac_f32_e32 v53, v14, v150
	v_fmac_f32_e32 v49, v14, v151
	v_fmac_f32_e32 v156, v16, v148
	v_fmac_f32_e32 v55, v16, v149
	v_fmac_f32_e32 v51, v16, v150
	v_fmac_f32_e32 v47, v16, v151
	ds_read_b128 v[148:151], v105 offset:29696
	s_waitcnt lgkmcnt(1)
	v_fmac_f32_e32 v224, v15, v144
	v_fmac_f32_e32 v223, v15, v145
	v_fmac_f32_e32 v221, v15, v146
	v_fmac_f32_e32 v217, v15, v147
	v_fmac_f32_e32 v225, v17, v144
	v_fmac_f32_e32 v222, v17, v145
	v_fmac_f32_e32 v219, v17, v146
	v_fmac_f32_e32 v215, v17, v147
	ds_read_b128 v[144:147], v105 offset:30720
	s_waitcnt lgkmcnt(1)
	v_fmac_f32_e32 v220, v15, v148
	v_fmac_f32_e32 v216, v15, v149
	v_fmac_f32_e32 v213, v15, v150
	v_fmac_f32_e32 v211, v15, v151
	v_fmac_f32_e32 v218, v17, v148
	v_fmac_f32_e32 v214, v17, v149
	v_fmac_f32_e32 v212, v17, v150
	v_fmac_f32_e32 v210, v17, v151
	ds_read_b128 v[148:151], v105 offset:31744
	s_waitcnt lgkmcnt(1)
	v_fmac_f32_e32 v57, v17, v147
	v_fmac_f32_e32 v209, v15, v144
	v_fmac_f32_e32 v207, v15, v145
	v_fmac_f32_e32 v205, v15, v146
	s_waitcnt lgkmcnt(0)
	v_fmac_f32_e32 v53, v15, v150
	v_fmac_f32_e32 v55, v17, v149
	v_fmac_f32_e32 v51, v17, v150
	v_fmac_f32_e32 v153, v15, v147
	v_fmac_f32_e32 v208, v17, v144
	v_fmac_f32_e32 v206, v17, v145
	v_fmac_f32_e32 v158, v17, v146
	v_fmac_f32_e32 v159, v15, v148
	v_fmac_f32_e32 v152, v15, v149
	v_fmac_f32_e32 v49, v15, v151
	v_fmac_f32_e32 v156, v17, v148
	v_fmac_f32_e32 v47, v17, v151
	s_waitcnt vmcnt(3)
	v_pk_add_f32 v[10:11], v[10:11], 1.0 op_sel_hi:[1,0]
	v_pk_mul_f32 v[142:143], v[102:103], v[142:143] op_sel_hi:[0,1]
	s_waitcnt vmcnt(2)
	v_pk_mul_f32 v[144:145], v[2:3], v[10:11]
	v_pk_add_f32 v[12:13], v[12:13], 1.0 op_sel_hi:[1,0]
	v_pk_fma_f32 v[146:147], v[142:143], v[144:145], v[6:7]
	v_pk_mul_f32 v[138:139], v[104:105], v[138:139] op_sel_hi:[0,1]
	v_pk_mul_f32 v[16:17], v[4:5], v[12:13]
	v_pk_mul_f32 v[14:15], v[102:103], v[140:141] op_sel_hi:[0,1]
	v_pk_mul_f32 v[136:137], v[104:105], v[136:137] op_sel_hi:[0,1]
	v_pk_fma_f32 v[144:145], v[138:139], v[144:145], v[6:7]
	v_med3_f32 v6, v146, s33, v233
	v_med3_f32 v7, v147, s33, v233
	v_mov_b32_e32 v140, 0
	v_pk_fma_f32 v[14:15], v[14:15], v[16:17], v[8:9]
	v_pk_fma_f32 v[16:17], v[136:137], v[16:17], v[8:9]
	v_cvt_pk_fp8_f32 v140, v6, v7
	v_med3_f32 v8, v144, s33, v233
	v_med3_f32 v9, v145, s33, v233
	v_mov_b32_e32 v141, 0
	v_cvt_pk_fp8_f32 v141, v8, v9
	v_med3_f32 v6, v14, s33, v233
	v_med3_f32 v7, v15, s33, v233
	v_cvt_pk_fp8_f32 v140, v6, v7 op_sel:[0,0,1]
	v_med3_f32 v6, v16, s33, v233
	v_med3_f32 v7, v17, s33, v233
	global_load_dwordx4 v[2:5], v[74:75], off
	global_load_dwordx4 v[10:13], v[76:77], off
	v_cvt_pk_fp8_f32 v141, v6, v7 op_sel:[0,0,1]
	global_load_dwordx4 v[6:9], v[32:33], off
	ds_read_b128 v[136:139], v105 offset:32768
	global_store_dword v[118:119], v140, off offset:512
	global_store_dword v[118:119], v141, off offset:2560
	ds_read_b128 v[140:143], v105 offset:33792
	s_waitcnt lgkmcnt(1)
	v_fmac_f32_e32 v224, v146, v136
	v_fmac_f32_e32 v223, v146, v137
	v_fmac_f32_e32 v221, v146, v138
	v_fmac_f32_e32 v217, v146, v139
	v_fmac_f32_e32 v225, v144, v136
	v_fmac_f32_e32 v222, v144, v137
	v_fmac_f32_e32 v219, v144, v138
	v_fmac_f32_e32 v215, v144, v139
	ds_read_b128 v[136:139], v105 offset:34816
	s_waitcnt lgkmcnt(1)
	v_fmac_f32_e32 v220, v146, v140
	v_fmac_f32_e32 v216, v146, v141
	v_fmac_f32_e32 v213, v146, v142
	v_fmac_f32_e32 v211, v146, v143
	v_fmac_f32_e32 v218, v144, v140
	v_fmac_f32_e32 v214, v144, v141
	v_fmac_f32_e32 v212, v144, v142
	v_fmac_f32_e32 v210, v144, v143
	ds_read_b128 v[140:143], v105 offset:35840
	s_waitcnt lgkmcnt(1)
	v_fmac_f32_e32 v209, v146, v136
	v_fmac_f32_e32 v207, v146, v137
	v_fmac_f32_e32 v205, v146, v138
	v_fmac_f32_e32 v153, v146, v139
	v_fmac_f32_e32 v208, v144, v136
	v_fmac_f32_e32 v206, v144, v137
	v_fmac_f32_e32 v158, v144, v138
	v_fmac_f32_e32 v57, v144, v139
	ds_read_b128 v[136:139], v105 offset:36864
	s_waitcnt lgkmcnt(1)
	v_fmac_f32_e32 v159, v146, v140
	v_fmac_f32_e32 v152, v146, v141
	v_fmac_f32_e32 v53, v146, v142
	v_fmac_f32_e32 v49, v146, v143
	v_fmac_f32_e32 v156, v144, v140
	v_fmac_f32_e32 v55, v144, v141
	v_fmac_f32_e32 v51, v144, v142
	v_fmac_f32_e32 v47, v144, v143
	ds_read_b128 v[140:143], v105 offset:37888
	s_waitcnt lgkmcnt(1)
	v_fmac_f32_e32 v224, v147, v136
	v_fmac_f32_e32 v223, v147, v137
	v_fmac_f32_e32 v221, v147, v138
	v_fmac_f32_e32 v217, v147, v139
	v_fmac_f32_e32 v225, v145, v136
	v_fmac_f32_e32 v222, v145, v137
	v_fmac_f32_e32 v219, v145, v138
	v_fmac_f32_e32 v215, v145, v139
	ds_read_b128 v[136:139], v105 offset:38912
	s_waitcnt lgkmcnt(1)
	v_fmac_f32_e32 v220, v147, v140
	v_fmac_f32_e32 v216, v147, v141
	v_fmac_f32_e32 v213, v147, v142
	v_fmac_f32_e32 v211, v147, v143
	v_fmac_f32_e32 v218, v145, v140
	v_fmac_f32_e32 v214, v145, v141
	v_fmac_f32_e32 v212, v145, v142
	v_fmac_f32_e32 v210, v145, v143
	ds_read_b128 v[140:143], v105 offset:39936
	s_waitcnt lgkmcnt(1)
	v_fmac_f32_e32 v209, v147, v136
	v_fmac_f32_e32 v207, v147, v137
	v_fmac_f32_e32 v205, v147, v138
	v_fmac_f32_e32 v153, v147, v139
	v_fmac_f32_e32 v208, v145, v136
	v_fmac_f32_e32 v206, v145, v137
	v_fmac_f32_e32 v158, v145, v138
	v_fmac_f32_e32 v57, v145, v139
	ds_read_b128 v[136:139], v105 offset:40960
	s_waitcnt lgkmcnt(1)
	v_fmac_f32_e32 v159, v147, v140
	v_fmac_f32_e32 v152, v147, v141
	v_fmac_f32_e32 v53, v147, v142
	v_fmac_f32_e32 v49, v147, v143
	v_fmac_f32_e32 v156, v145, v140
	v_fmac_f32_e32 v55, v145, v141
	v_fmac_f32_e32 v51, v145, v142
	v_fmac_f32_e32 v47, v145, v143
	ds_read_b128 v[140:143], v105 offset:41984
	s_waitcnt lgkmcnt(1)
	v_fmac_f32_e32 v224, v14, v136
	v_fmac_f32_e32 v223, v14, v137
	v_fmac_f32_e32 v221, v14, v138
	v_fmac_f32_e32 v217, v14, v139
	v_fmac_f32_e32 v225, v16, v136
	v_fmac_f32_e32 v222, v16, v137
	v_fmac_f32_e32 v219, v16, v138
	v_fmac_f32_e32 v215, v16, v139
	ds_read_b128 v[136:139], v105 offset:43008
	s_waitcnt lgkmcnt(1)
	v_fmac_f32_e32 v220, v14, v140
	v_fmac_f32_e32 v216, v14, v141
	v_fmac_f32_e32 v213, v14, v142
	v_fmac_f32_e32 v211, v14, v143
	v_fmac_f32_e32 v218, v16, v140
	v_fmac_f32_e32 v214, v16, v141
	v_fmac_f32_e32 v212, v16, v142
	v_fmac_f32_e32 v210, v16, v143
	ds_read_b128 v[140:143], v105 offset:44032
	s_waitcnt lgkmcnt(1)
	v_fmac_f32_e32 v209, v14, v136
	v_fmac_f32_e32 v207, v14, v137
	v_fmac_f32_e32 v205, v14, v138
	v_fmac_f32_e32 v153, v14, v139
	v_fmac_f32_e32 v208, v16, v136
	v_fmac_f32_e32 v206, v16, v137
	v_fmac_f32_e32 v158, v16, v138
	v_fmac_f32_e32 v57, v16, v139
	ds_read_b128 v[136:139], v105 offset:45056
	s_waitcnt lgkmcnt(1)
	v_fmac_f32_e32 v159, v14, v140
	v_fmac_f32_e32 v152, v14, v141
	v_fmac_f32_e32 v53, v14, v142
	v_fmac_f32_e32 v49, v14, v143
	v_fmac_f32_e32 v156, v16, v140
	v_fmac_f32_e32 v55, v16, v141
	v_fmac_f32_e32 v51, v16, v142
	v_fmac_f32_e32 v47, v16, v143
	ds_read_b128 v[140:143], v105 offset:46080
	s_waitcnt lgkmcnt(1)
	v_fmac_f32_e32 v224, v15, v136
	v_fmac_f32_e32 v223, v15, v137
	v_fmac_f32_e32 v221, v15, v138
	v_fmac_f32_e32 v217, v15, v139
	v_fmac_f32_e32 v225, v17, v136
	v_fmac_f32_e32 v222, v17, v137
	v_fmac_f32_e32 v219, v17, v138
	v_fmac_f32_e32 v215, v17, v139
	ds_read_b128 v[136:139], v105 offset:47104
	s_waitcnt lgkmcnt(1)
	v_fmac_f32_e32 v220, v15, v140
	v_fmac_f32_e32 v216, v15, v141
	v_fmac_f32_e32 v213, v15, v142
	v_fmac_f32_e32 v211, v15, v143
	v_fmac_f32_e32 v218, v17, v140
	v_fmac_f32_e32 v214, v17, v141
	v_fmac_f32_e32 v212, v17, v142
	v_fmac_f32_e32 v210, v17, v143
	ds_read_b128 v[140:143], v105 offset:48128
	s_waitcnt lgkmcnt(1)
	v_fmac_f32_e32 v57, v17, v139
	v_fmac_f32_e32 v209, v15, v136
	v_fmac_f32_e32 v207, v15, v137
	v_fmac_f32_e32 v205, v15, v138
	s_waitcnt lgkmcnt(0)
	v_fmac_f32_e32 v53, v15, v142
	v_fmac_f32_e32 v55, v17, v141
	v_fmac_f32_e32 v51, v17, v142
	v_fmac_f32_e32 v153, v15, v139
	v_fmac_f32_e32 v208, v17, v136
	v_fmac_f32_e32 v206, v17, v137
	v_fmac_f32_e32 v158, v17, v138
	v_fmac_f32_e32 v159, v15, v140
	v_fmac_f32_e32 v152, v15, v141
	v_fmac_f32_e32 v49, v15, v143
	v_fmac_f32_e32 v156, v17, v140
	v_fmac_f32_e32 v47, v17, v143
	s_waitcnt vmcnt(3)
	v_pk_add_f32 v[10:11], v[10:11], 1.0 op_sel_hi:[1,0]
	v_pk_mul_f32 v[130:131], v[102:103], v[130:131] op_sel_hi:[0,1]
	s_waitcnt vmcnt(2)
	v_pk_mul_f32 v[136:137], v[6:7], v[10:11]
	v_pk_add_f32 v[12:13], v[12:13], 1.0 op_sel_hi:[1,0]
	v_pk_mul_f32 v[14:15], v[102:103], v[128:129] op_sel_hi:[0,1]
	v_pk_fma_f32 v[138:139], v[130:131], v[136:137], v[2:3]
	v_pk_mul_f32 v[128:129], v[104:105], v[132:133] op_sel_hi:[0,1]
	v_pk_mul_f32 v[16:17], v[8:9], v[12:13]
	v_pk_mul_f32 v[130:131], v[104:105], v[134:135] op_sel_hi:[0,1]
	v_pk_fma_f32 v[136:137], v[128:129], v[136:137], v[2:3]
	v_med3_f32 v2, v138, s33, v233
	v_med3_f32 v3, v139, s33, v233
	v_mov_b32_e32 v132, 0
	v_pk_fma_f32 v[14:15], v[14:15], v[16:17], v[4:5]
	v_pk_fma_f32 v[16:17], v[130:131], v[16:17], v[4:5]
	v_cvt_pk_fp8_f32 v132, v2, v3
	v_med3_f32 v4, v136, s33, v233
	v_med3_f32 v5, v137, s33, v233
	v_mov_b32_e32 v133, 0
	v_cvt_pk_fp8_f32 v133, v4, v5
	v_med3_f32 v2, v14, s33, v233
	v_med3_f32 v3, v15, s33, v233
	v_cvt_pk_fp8_f32 v132, v2, v3 op_sel:[0,0,1]
	v_med3_f32 v2, v16, s33, v233
	v_med3_f32 v3, v17, s33, v233
	global_load_dwordx4 v[10:13], v[78:79], off
	global_load_dwordx4 v[6:9], v[80:81], off
	v_cvt_pk_fp8_f32 v133, v2, v3 op_sel:[0,0,1]
	global_load_dwordx4 v[2:5], v[34:35], off
	ds_read_b128 v[128:131], v105 offset:49152
	global_store_dword v[118:119], v132, off offset:768
	global_store_dword v[118:119], v133, off offset:2816
	ds_read_b128 v[132:135], v105 offset:50176
	s_waitcnt lgkmcnt(1)
	v_fmac_f32_e32 v224, v138, v128
	v_fmac_f32_e32 v223, v138, v129
	v_fmac_f32_e32 v221, v138, v130
	v_fmac_f32_e32 v217, v138, v131
	v_fmac_f32_e32 v225, v136, v128
	v_fmac_f32_e32 v222, v136, v129
	v_fmac_f32_e32 v219, v136, v130
	v_fmac_f32_e32 v215, v136, v131
	ds_read_b128 v[128:131], v105 offset:51200
	s_waitcnt lgkmcnt(1)
	v_fmac_f32_e32 v220, v138, v132
	v_fmac_f32_e32 v216, v138, v133
	v_fmac_f32_e32 v213, v138, v134
	v_fmac_f32_e32 v211, v138, v135
	v_fmac_f32_e32 v218, v136, v132
	v_fmac_f32_e32 v214, v136, v133
	v_fmac_f32_e32 v212, v136, v134
	v_fmac_f32_e32 v210, v136, v135
	ds_read_b128 v[132:135], v105 offset:52224
	s_waitcnt lgkmcnt(1)
	v_fmac_f32_e32 v209, v138, v128
	v_fmac_f32_e32 v207, v138, v129
	v_fmac_f32_e32 v205, v138, v130
	v_fmac_f32_e32 v153, v138, v131
	v_fmac_f32_e32 v208, v136, v128
	v_fmac_f32_e32 v206, v136, v129
	v_fmac_f32_e32 v158, v136, v130
	v_fmac_f32_e32 v57, v136, v131
	ds_read_b128 v[128:131], v105 offset:53248
	s_waitcnt lgkmcnt(1)
	v_fmac_f32_e32 v159, v138, v132
	v_fmac_f32_e32 v152, v138, v133
	v_fmac_f32_e32 v53, v138, v134
	v_fmac_f32_e32 v49, v138, v135
	v_fmac_f32_e32 v156, v136, v132
	v_fmac_f32_e32 v55, v136, v133
	v_fmac_f32_e32 v51, v136, v134
	v_fmac_f32_e32 v47, v136, v135
	ds_read_b128 v[132:135], v105 offset:54272
	s_waitcnt lgkmcnt(1)
	v_fmac_f32_e32 v224, v139, v128
	v_fmac_f32_e32 v223, v139, v129
	v_fmac_f32_e32 v221, v139, v130
	v_fmac_f32_e32 v217, v139, v131
	v_fmac_f32_e32 v225, v137, v128
	v_fmac_f32_e32 v222, v137, v129
	v_fmac_f32_e32 v219, v137, v130
	v_fmac_f32_e32 v215, v137, v131
	ds_read_b128 v[128:131], v105 offset:55296
	s_waitcnt lgkmcnt(1)
	v_fmac_f32_e32 v220, v139, v132
	v_fmac_f32_e32 v216, v139, v133
	v_fmac_f32_e32 v213, v139, v134
	v_fmac_f32_e32 v211, v139, v135
	v_fmac_f32_e32 v218, v137, v132
	v_fmac_f32_e32 v214, v137, v133
	v_fmac_f32_e32 v212, v137, v134
	v_fmac_f32_e32 v210, v137, v135
	ds_read_b128 v[132:135], v105 offset:56320
	s_waitcnt lgkmcnt(1)
	v_fmac_f32_e32 v209, v139, v128
	v_fmac_f32_e32 v207, v139, v129
	v_fmac_f32_e32 v205, v139, v130
	v_fmac_f32_e32 v153, v139, v131
	v_fmac_f32_e32 v208, v137, v128
	v_fmac_f32_e32 v206, v137, v129
	v_fmac_f32_e32 v158, v137, v130
	v_fmac_f32_e32 v57, v137, v131
	ds_read_b128 v[128:131], v105 offset:57344
	s_waitcnt lgkmcnt(1)
	v_fmac_f32_e32 v159, v139, v132
	v_fmac_f32_e32 v152, v139, v133
	v_fmac_f32_e32 v53, v139, v134
	v_fmac_f32_e32 v49, v139, v135
	v_fmac_f32_e32 v156, v137, v132
	v_fmac_f32_e32 v55, v137, v133
	v_fmac_f32_e32 v51, v137, v134
	v_fmac_f32_e32 v47, v137, v135
	ds_read_b128 v[132:135], v105 offset:58368
	s_waitcnt lgkmcnt(1)
	v_fmac_f32_e32 v224, v14, v128
	v_fmac_f32_e32 v223, v14, v129
	v_fmac_f32_e32 v221, v14, v130
	v_fmac_f32_e32 v217, v14, v131
	v_fmac_f32_e32 v225, v16, v128
	v_fmac_f32_e32 v222, v16, v129
	v_fmac_f32_e32 v219, v16, v130
	v_fmac_f32_e32 v215, v16, v131
	ds_read_b128 v[128:131], v105 offset:59392
	s_waitcnt lgkmcnt(1)
	v_fmac_f32_e32 v220, v14, v132
	v_fmac_f32_e32 v216, v14, v133
	v_fmac_f32_e32 v213, v14, v134
	v_fmac_f32_e32 v211, v14, v135
	v_fmac_f32_e32 v218, v16, v132
	v_fmac_f32_e32 v214, v16, v133
	v_fmac_f32_e32 v212, v16, v134
	v_fmac_f32_e32 v210, v16, v135
	ds_read_b128 v[132:135], v105 offset:60416
	s_waitcnt lgkmcnt(1)
	v_fmac_f32_e32 v209, v14, v128
	v_fmac_f32_e32 v207, v14, v129
	v_fmac_f32_e32 v205, v14, v130
	v_fmac_f32_e32 v153, v14, v131
	v_fmac_f32_e32 v208, v16, v128
	v_fmac_f32_e32 v206, v16, v129
	v_fmac_f32_e32 v158, v16, v130
	v_fmac_f32_e32 v57, v16, v131
	ds_read_b128 v[128:131], v105 offset:61440
	s_waitcnt lgkmcnt(1)
	v_fmac_f32_e32 v159, v14, v132
	v_fmac_f32_e32 v152, v14, v133
	v_fmac_f32_e32 v53, v14, v134
	v_fmac_f32_e32 v49, v14, v135
	v_fmac_f32_e32 v156, v16, v132
	v_fmac_f32_e32 v55, v16, v133
	v_fmac_f32_e32 v51, v16, v134
	v_fmac_f32_e32 v47, v16, v135
	ds_read_b128 v[132:135], v105 offset:62464
	s_waitcnt lgkmcnt(1)
	v_fmac_f32_e32 v224, v15, v128
	v_fmac_f32_e32 v223, v15, v129
	v_fmac_f32_e32 v221, v15, v130
	v_fmac_f32_e32 v217, v15, v131
	v_fmac_f32_e32 v225, v17, v128
	v_fmac_f32_e32 v222, v17, v129
	v_fmac_f32_e32 v219, v17, v130
	v_fmac_f32_e32 v215, v17, v131
	ds_read_b128 v[128:131], v105 offset:63488
	s_waitcnt lgkmcnt(1)
	v_fmac_f32_e32 v220, v15, v132
	v_fmac_f32_e32 v216, v15, v133
	v_fmac_f32_e32 v213, v15, v134
	v_fmac_f32_e32 v211, v15, v135
	v_fmac_f32_e32 v218, v17, v132
	v_fmac_f32_e32 v214, v17, v133
	v_fmac_f32_e32 v212, v17, v134
	v_fmac_f32_e32 v210, v17, v135
	ds_read_b128 v[132:135], v105 offset:64512
	s_waitcnt lgkmcnt(1)
	v_fmac_f32_e32 v57, v17, v131
	v_fmac_f32_e32 v209, v15, v128
	v_fmac_f32_e32 v207, v15, v129
	v_fmac_f32_e32 v205, v15, v130
	s_waitcnt lgkmcnt(0)
	v_fmac_f32_e32 v53, v15, v134
	v_fmac_f32_e32 v55, v17, v133
	v_fmac_f32_e32 v51, v17, v134
	v_fmac_f32_e32 v153, v15, v131
	v_fmac_f32_e32 v208, v17, v128
	v_fmac_f32_e32 v206, v17, v129
	v_fmac_f32_e32 v158, v17, v130
	v_fmac_f32_e32 v159, v15, v132
	v_fmac_f32_e32 v152, v15, v133
	v_fmac_f32_e32 v49, v15, v135
	v_fmac_f32_e32 v156, v17, v132
	v_fmac_f32_e32 v47, v17, v135
	s_waitcnt vmcnt(3)
	v_pk_add_f32 v[6:7], v[6:7], 1.0 op_sel_hi:[1,0]
	v_pk_mul_f32 v[126:127], v[102:103], v[126:127] op_sel_hi:[0,1]
	s_waitcnt vmcnt(2)
	v_pk_mul_f32 v[128:129], v[2:3], v[6:7]
	v_pk_add_f32 v[8:9], v[8:9], 1.0 op_sel_hi:[1,0]
	v_pk_fma_f32 v[130:131], v[126:127], v[128:129], v[10:11]
	v_pk_mul_f32 v[122:123], v[104:105], v[122:123] op_sel_hi:[0,1]
	v_pk_mul_f32 v[16:17], v[4:5], v[8:9]
	v_pk_mul_f32 v[14:15], v[102:103], v[124:125] op_sel_hi:[0,1]
	v_pk_mul_f32 v[120:121], v[104:105], v[120:121] op_sel_hi:[0,1]
	v_pk_fma_f32 v[128:129], v[122:123], v[128:129], v[10:11]
	v_med3_f32 v10, v130, s33, v233
	v_med3_f32 v11, v131, s33, v233
	v_mov_b32_e32 v124, 0
	v_pk_fma_f32 v[14:15], v[14:15], v[16:17], v[12:13]
	v_pk_fma_f32 v[16:17], v[120:121], v[16:17], v[12:13]
	v_cvt_pk_fp8_f32 v124, v10, v11
	v_med3_f32 v12, v128, s33, v233
	v_med3_f32 v13, v129, s33, v233
	v_mov_b32_e32 v125, 0
	v_cvt_pk_fp8_f32 v125, v12, v13
	v_med3_f32 v10, v14, s33, v233
	v_med3_f32 v11, v15, s33, v233
	v_cvt_pk_fp8_f32 v124, v10, v11 op_sel:[0,0,1]
	v_med3_f32 v10, v16, s33, v233
	v_med3_f32 v11, v17, s33, v233
	global_load_dwordx4 v[6:9], v[82:83], off
	global_load_dwordx4 v[2:5], v[84:85], off
	v_cvt_pk_fp8_f32 v125, v10, v11 op_sel:[0,0,1]
	v_add_u32_e32 v10, 0x10000, v105
	ds_read_b128 v[120:123], v10
	global_load_dwordx4 v[10:13], v[36:37], off
	s_nop 0
	global_store_dword v[118:119], v124, off offset:1024
	global_store_dword v[118:119], v125, off offset:3072
	v_add_u32_e32 v124, 0x10400, v105
	ds_read_b128 v[124:127], v124
	s_waitcnt lgkmcnt(1)
	v_fmac_f32_e32 v224, v130, v120
	v_fmac_f32_e32 v225, v128, v120
	v_add_u32_e32 v120, 0x10800, v105
	v_fmac_f32_e32 v223, v130, v121
	v_fmac_f32_e32 v221, v130, v122
	v_fmac_f32_e32 v217, v130, v123
	v_fmac_f32_e32 v222, v128, v121
	v_fmac_f32_e32 v219, v128, v122
	v_fmac_f32_e32 v215, v128, v123
	ds_read_b128 v[120:123], v120
	s_waitcnt lgkmcnt(1)
	v_fmac_f32_e32 v220, v130, v124
	v_fmac_f32_e32 v218, v128, v124
	v_add_u32_e32 v124, 0x10c00, v105
	v_fmac_f32_e32 v216, v130, v125
	v_fmac_f32_e32 v213, v130, v126
	v_fmac_f32_e32 v211, v130, v127
	v_fmac_f32_e32 v214, v128, v125
	v_fmac_f32_e32 v212, v128, v126
	v_fmac_f32_e32 v210, v128, v127
	ds_read_b128 v[124:127], v124
	s_waitcnt lgkmcnt(1)
	v_fmac_f32_e32 v209, v130, v120
	v_fmac_f32_e32 v208, v128, v120
	v_add_u32_e32 v120, 0x11000, v105
	v_fmac_f32_e32 v207, v130, v121
	v_fmac_f32_e32 v205, v130, v122
	v_fmac_f32_e32 v153, v130, v123
	v_fmac_f32_e32 v206, v128, v121
	v_fmac_f32_e32 v158, v128, v122
	v_fmac_f32_e32 v57, v128, v123
	ds_read_b128 v[120:123], v120
	s_waitcnt lgkmcnt(1)
	v_fmac_f32_e32 v159, v130, v124
	v_fmac_f32_e32 v156, v128, v124
	v_add_u32_e32 v124, 0x11400, v105
	v_fmac_f32_e32 v152, v130, v125
	v_fmac_f32_e32 v53, v130, v126
	v_fmac_f32_e32 v49, v130, v127
	v_fmac_f32_e32 v55, v128, v125
	v_fmac_f32_e32 v51, v128, v126
	v_fmac_f32_e32 v47, v128, v127
	ds_read_b128 v[124:127], v124
	s_waitcnt lgkmcnt(1)
	v_fmac_f32_e32 v224, v131, v120
	v_fmac_f32_e32 v225, v129, v120
	v_add_u32_e32 v120, 0x11800, v105
	v_fmac_f32_e32 v223, v131, v121
	v_fmac_f32_e32 v221, v131, v122
	v_fmac_f32_e32 v217, v131, v123
	v_fmac_f32_e32 v222, v129, v121
	v_fmac_f32_e32 v219, v129, v122
	v_fmac_f32_e32 v215, v129, v123
	ds_read_b128 v[120:123], v120
	s_waitcnt lgkmcnt(1)
	v_fmac_f32_e32 v220, v131, v124
	v_fmac_f32_e32 v218, v129, v124
	v_add_u32_e32 v124, 0x11c00, v105
	v_fmac_f32_e32 v216, v131, v125
	v_fmac_f32_e32 v213, v131, v126
	v_fmac_f32_e32 v211, v131, v127
	v_fmac_f32_e32 v214, v129, v125
	v_fmac_f32_e32 v212, v129, v126
	v_fmac_f32_e32 v210, v129, v127
	ds_read_b128 v[124:127], v124
	s_waitcnt lgkmcnt(1)
	v_fmac_f32_e32 v209, v131, v120
	v_fmac_f32_e32 v208, v129, v120
	v_add_u32_e32 v120, 0x12000, v105
	v_fmac_f32_e32 v207, v131, v121
	v_fmac_f32_e32 v205, v131, v122
	v_fmac_f32_e32 v153, v131, v123
	v_fmac_f32_e32 v206, v129, v121
	v_fmac_f32_e32 v158, v129, v122
	v_fmac_f32_e32 v57, v129, v123
	ds_read_b128 v[120:123], v120
	s_waitcnt lgkmcnt(1)
	v_fmac_f32_e32 v159, v131, v124
	v_fmac_f32_e32 v156, v129, v124
	v_add_u32_e32 v124, 0x12400, v105
	v_fmac_f32_e32 v152, v131, v125
	v_fmac_f32_e32 v53, v131, v126
	v_fmac_f32_e32 v49, v131, v127
	v_fmac_f32_e32 v55, v129, v125
	v_fmac_f32_e32 v51, v129, v126
	v_fmac_f32_e32 v47, v129, v127
	ds_read_b128 v[124:127], v124
	s_waitcnt lgkmcnt(1)
	v_fmac_f32_e32 v224, v14, v120
	v_fmac_f32_e32 v225, v16, v120
	v_add_u32_e32 v120, 0x12800, v105
	v_fmac_f32_e32 v223, v14, v121
	v_fmac_f32_e32 v221, v14, v122
	v_fmac_f32_e32 v217, v14, v123
	v_fmac_f32_e32 v222, v16, v121
	v_fmac_f32_e32 v219, v16, v122
	v_fmac_f32_e32 v215, v16, v123
	ds_read_b128 v[120:123], v120
	s_waitcnt lgkmcnt(1)
	v_fmac_f32_e32 v220, v14, v124
	v_fmac_f32_e32 v218, v16, v124
	v_add_u32_e32 v124, 0x12c00, v105
	v_fmac_f32_e32 v216, v14, v125
	v_fmac_f32_e32 v213, v14, v126
	v_fmac_f32_e32 v211, v14, v127
	v_fmac_f32_e32 v214, v16, v125
	v_fmac_f32_e32 v212, v16, v126
	v_fmac_f32_e32 v210, v16, v127
	ds_read_b128 v[124:127], v124
	s_waitcnt lgkmcnt(1)
	v_fmac_f32_e32 v209, v14, v120
	v_fmac_f32_e32 v207, v14, v121
	v_fmac_f32_e32 v205, v14, v122
	v_fmac_f32_e32 v153, v14, v123
	s_waitcnt lgkmcnt(0)
	v_fmac_f32_e32 v159, v14, v124
	v_fmac_f32_e32 v152, v14, v125
	v_fmac_f32_e32 v53, v14, v126
	v_fmac_f32_e32 v49, v14, v127
	v_add_u32_e32 v14, 0x13000, v105
	v_fmac_f32_e32 v208, v16, v120
	v_fmac_f32_e32 v206, v16, v121
	v_fmac_f32_e32 v158, v16, v122
	v_fmac_f32_e32 v57, v16, v123
	ds_read_b128 v[120:123], v14
	v_add_u32_e32 v14, 0x13400, v105
	v_fmac_f32_e32 v156, v16, v124
	v_fmac_f32_e32 v55, v16, v125
	v_fmac_f32_e32 v51, v16, v126
	v_fmac_f32_e32 v47, v16, v127
	ds_read_b128 v[124:127], v14
	v_add_u32_e32 v14, 0x13800, v105
	s_waitcnt lgkmcnt(1)
	v_fmac_f32_e32 v224, v15, v120
	v_fmac_f32_e32 v223, v15, v121
	v_fmac_f32_e32 v221, v15, v122
	v_fmac_f32_e32 v217, v15, v123
	v_fmac_f32_e32 v225, v17, v120
	v_fmac_f32_e32 v222, v17, v121
	v_fmac_f32_e32 v219, v17, v122
	v_fmac_f32_e32 v215, v17, v123
	ds_read_b128 v[120:123], v14
	v_add_u32_e32 v14, 0x13c00, v105
	s_waitcnt lgkmcnt(1)
	v_fmac_f32_e32 v220, v15, v124
	v_fmac_f32_e32 v216, v15, v125
	v_fmac_f32_e32 v213, v15, v126
	v_fmac_f32_e32 v211, v15, v127
	v_fmac_f32_e32 v218, v17, v124
	v_fmac_f32_e32 v214, v17, v125
	v_fmac_f32_e32 v212, v17, v126
	v_fmac_f32_e32 v210, v17, v127
	ds_read_b128 v[124:127], v14
	s_waitcnt lgkmcnt(1)
	v_fmac_f32_e32 v57, v17, v123
	v_fmac_f32_e32 v209, v15, v120
	v_fmac_f32_e32 v207, v15, v121
	v_fmac_f32_e32 v205, v15, v122
	s_waitcnt lgkmcnt(0)
	v_fmac_f32_e32 v53, v15, v126
	v_fmac_f32_e32 v55, v17, v125
	v_fmac_f32_e32 v51, v17, v126
	v_fmac_f32_e32 v153, v15, v123
	v_fmac_f32_e32 v208, v17, v120
	v_fmac_f32_e32 v206, v17, v121
	v_fmac_f32_e32 v158, v17, v122
	v_fmac_f32_e32 v159, v15, v124
	v_fmac_f32_e32 v152, v15, v125
	v_fmac_f32_e32 v49, v15, v127
	v_fmac_f32_e32 v156, v17, v124
	v_fmac_f32_e32 v47, v17, v127
	s_waitcnt vmcnt(3)
	v_pk_add_f32 v[2:3], v[2:3], 1.0 op_sel_hi:[1,0]
	v_pk_mul_f32 v[116:117], v[102:103], v[116:117] op_sel_hi:[0,1]
	s_waitcnt vmcnt(2)
	v_pk_mul_f32 v[120:121], v[10:11], v[2:3]
	v_pk_add_f32 v[4:5], v[4:5], 1.0 op_sel_hi:[1,0]
	v_pk_fma_f32 v[122:123], v[116:117], v[120:121], v[6:7]
	v_pk_mul_f32 v[112:113], v[104:105], v[112:113] op_sel_hi:[0,1]
	v_pk_mul_f32 v[16:17], v[12:13], v[4:5]
	v_pk_mul_f32 v[14:15], v[102:103], v[114:115] op_sel_hi:[0,1]
	v_pk_mul_f32 v[110:111], v[104:105], v[110:111] op_sel_hi:[0,1]
	v_pk_fma_f32 v[120:121], v[112:113], v[120:121], v[6:7]
	v_med3_f32 v6, v122, s33, v233
	v_med3_f32 v7, v123, s33, v233
	v_mov_b32_e32 v114, 0
	v_pk_fma_f32 v[14:15], v[14:15], v[16:17], v[8:9]
	v_pk_fma_f32 v[16:17], v[110:111], v[16:17], v[8:9]
	v_cvt_pk_fp8_f32 v114, v6, v7
	v_med3_f32 v8, v120, s33, v233
	v_med3_f32 v9, v121, s33, v233
	v_mov_b32_e32 v115, 0
	v_cvt_pk_fp8_f32 v115, v8, v9
	v_med3_f32 v6, v14, s33, v233
	v_med3_f32 v7, v15, s33, v233
	v_cvt_pk_fp8_f32 v114, v6, v7 op_sel:[0,0,1]
	v_med3_f32 v6, v16, s33, v233
	v_med3_f32 v7, v17, s33, v233
	v_cvt_pk_fp8_f32 v115, v6, v7 op_sel:[0,0,1]
	v_add_u32_e32 v6, 0x14000, v105
	global_load_dwordx4 v[2:5], v[86:87], off
	global_load_dwordx4 v[10:13], v[88:89], off
	ds_read_b128 v[110:113], v6
	global_load_dwordx4 v[6:9], v[38:39], off
	s_nop 0
	global_store_dword v[118:119], v114, off offset:1280
	global_store_dword v[118:119], v115, off offset:3328
	v_add_u32_e32 v114, 0x14400, v105
	ds_read_b128 v[114:117], v114
	s_waitcnt lgkmcnt(1)
	v_fmac_f32_e32 v224, v122, v110
	v_fmac_f32_e32 v225, v120, v110
	v_add_u32_e32 v110, 0x14800, v105
	v_fmac_f32_e32 v223, v122, v111
	v_fmac_f32_e32 v221, v122, v112
	v_fmac_f32_e32 v217, v122, v113
	v_fmac_f32_e32 v222, v120, v111
	v_fmac_f32_e32 v219, v120, v112
	v_fmac_f32_e32 v215, v120, v113
	ds_read_b128 v[110:113], v110
	s_waitcnt lgkmcnt(1)
	v_fmac_f32_e32 v220, v122, v114
	v_fmac_f32_e32 v218, v120, v114
	v_add_u32_e32 v114, 0x14c00, v105
	v_fmac_f32_e32 v216, v122, v115
	v_fmac_f32_e32 v213, v122, v116
	v_fmac_f32_e32 v211, v122, v117
	v_fmac_f32_e32 v214, v120, v115
	v_fmac_f32_e32 v212, v120, v116
	v_fmac_f32_e32 v210, v120, v117
	ds_read_b128 v[114:117], v114
	s_waitcnt lgkmcnt(1)
	v_fmac_f32_e32 v209, v122, v110
	v_fmac_f32_e32 v208, v120, v110
	v_add_u32_e32 v110, 0x15000, v105
	v_fmac_f32_e32 v207, v122, v111
	v_fmac_f32_e32 v205, v122, v112
	v_fmac_f32_e32 v153, v122, v113
	v_fmac_f32_e32 v206, v120, v111
	v_fmac_f32_e32 v158, v120, v112
	v_fmac_f32_e32 v57, v120, v113
	ds_read_b128 v[110:113], v110
	s_waitcnt lgkmcnt(1)
	v_fmac_f32_e32 v159, v122, v114
	v_fmac_f32_e32 v152, v122, v115
	v_fmac_f32_e32 v53, v122, v116
	v_fmac_f32_e32 v49, v122, v117
	v_fmac_f32_e32 v156, v120, v114
	v_fmac_f32_e32 v55, v120, v115
	v_fmac_f32_e32 v51, v120, v116
	v_fmac_f32_e32 v47, v120, v117
	ds_read_b128 v[114:117], v230
	s_waitcnt lgkmcnt(1)
	v_fmac_f32_e32 v224, v123, v110
	v_fmac_f32_e32 v223, v123, v111
	v_fmac_f32_e32 v221, v123, v112
	v_fmac_f32_e32 v217, v123, v113
	v_fmac_f32_e32 v225, v121, v110
	v_fmac_f32_e32 v222, v121, v111
	v_fmac_f32_e32 v219, v121, v112
	v_fmac_f32_e32 v215, v121, v113
	ds_read_b128 v[110:113], v250
	s_waitcnt lgkmcnt(1)
	v_fmac_f32_e32 v220, v123, v114
	v_fmac_f32_e32 v216, v123, v115
	v_fmac_f32_e32 v213, v123, v116
	v_fmac_f32_e32 v211, v123, v117
	v_fmac_f32_e32 v218, v121, v114
	v_fmac_f32_e32 v214, v121, v115
	v_fmac_f32_e32 v212, v121, v116
	v_fmac_f32_e32 v210, v121, v117
	ds_read_b128 v[114:117], v251
	s_waitcnt lgkmcnt(1)
	v_fmac_f32_e32 v209, v123, v110
	v_fmac_f32_e32 v207, v123, v111
	v_fmac_f32_e32 v205, v123, v112
	v_fmac_f32_e32 v153, v123, v113
	v_fmac_f32_e32 v208, v121, v110
	v_fmac_f32_e32 v206, v121, v111
	v_fmac_f32_e32 v158, v121, v112
	v_fmac_f32_e32 v57, v121, v113
	s_waitcnt lgkmcnt(0)
	v_fmac_f32_e32 v159, v123, v114
	v_fmac_f32_e32 v152, v123, v115
	v_fmac_f32_e32 v53, v123, v116
	v_fmac_f32_e32 v49, v123, v117
	v_fmac_f32_e32 v156, v121, v114
	ds_read_b128 v[110:113], v164
	v_fmac_f32_e32 v55, v121, v115
	v_fmac_f32_e32 v51, v121, v116
	v_fmac_f32_e32 v47, v121, v117
	ds_read_b128 v[114:117], v165
	s_waitcnt lgkmcnt(1)
	v_fmac_f32_e32 v224, v14, v110
	v_fmac_f32_e32 v223, v14, v111
	v_fmac_f32_e32 v221, v14, v112
	v_fmac_f32_e32 v217, v14, v113
	v_fmac_f32_e32 v225, v16, v110
	v_fmac_f32_e32 v222, v16, v111
	v_fmac_f32_e32 v219, v16, v112
	v_fmac_f32_e32 v215, v16, v113
	s_waitcnt lgkmcnt(0)
	v_fmac_f32_e32 v220, v14, v114
	v_fmac_f32_e32 v216, v14, v115
	v_fmac_f32_e32 v213, v14, v116
	v_fmac_f32_e32 v211, v14, v117
	v_fmac_f32_e32 v218, v16, v114
	ds_read_b128 v[110:113], v166
	v_fmac_f32_e32 v214, v16, v115
	v_fmac_f32_e32 v212, v16, v116
	v_fmac_f32_e32 v210, v16, v117
	ds_read_b128 v[114:117], v167
	s_waitcnt lgkmcnt(1)
	v_fmac_f32_e32 v209, v14, v110
	v_fmac_f32_e32 v207, v14, v111
	v_fmac_f32_e32 v205, v14, v112
	v_fmac_f32_e32 v153, v14, v113
	v_fmac_f32_e32 v208, v16, v110
	v_fmac_f32_e32 v206, v16, v111
	v_fmac_f32_e32 v158, v16, v112
	v_fmac_f32_e32 v57, v16, v113
	s_waitcnt lgkmcnt(0)
	v_fmac_f32_e32 v159, v14, v114
	v_fmac_f32_e32 v152, v14, v115
	v_fmac_f32_e32 v53, v14, v116
	v_fmac_f32_e32 v49, v14, v117
	v_fmac_f32_e32 v156, v16, v114
	ds_read_b128 v[110:113], v168
	v_fmac_f32_e32 v55, v16, v115
	v_fmac_f32_e32 v51, v16, v116
	v_fmac_f32_e32 v47, v16, v117
	ds_read_b128 v[114:117], v169
	s_waitcnt lgkmcnt(1)
	v_fmac_f32_e32 v224, v15, v110
	v_fmac_f32_e32 v223, v15, v111
	v_fmac_f32_e32 v221, v15, v112
	v_fmac_f32_e32 v217, v15, v113
	v_fmac_f32_e32 v225, v17, v110
	v_fmac_f32_e32 v222, v17, v111
	v_fmac_f32_e32 v219, v17, v112
	v_fmac_f32_e32 v215, v17, v113
	s_waitcnt lgkmcnt(0)
	v_fmac_f32_e32 v220, v15, v114
	v_fmac_f32_e32 v216, v15, v115
	v_fmac_f32_e32 v213, v15, v116
	v_fmac_f32_e32 v211, v15, v117
	v_fmac_f32_e32 v218, v17, v114
	ds_read_b128 v[110:113], v170
	v_fmac_f32_e32 v214, v17, v115
	v_fmac_f32_e32 v212, v17, v116
	v_fmac_f32_e32 v210, v17, v117
	ds_read_b128 v[114:117], v171
	s_waitcnt lgkmcnt(1)
	v_fmac_f32_e32 v57, v17, v113
	v_fmac_f32_e32 v209, v15, v110
	v_fmac_f32_e32 v207, v15, v111
	v_fmac_f32_e32 v205, v15, v112
	s_waitcnt lgkmcnt(0)
	v_fmac_f32_e32 v53, v15, v116
	v_fmac_f32_e32 v55, v17, v115
	v_fmac_f32_e32 v51, v17, v116
	v_fmac_f32_e32 v153, v15, v113
	v_fmac_f32_e32 v208, v17, v110
	v_fmac_f32_e32 v206, v17, v111
	v_fmac_f32_e32 v158, v17, v112
	v_fmac_f32_e32 v159, v15, v114
	v_fmac_f32_e32 v152, v15, v115
	v_fmac_f32_e32 v49, v15, v117
	v_fmac_f32_e32 v156, v17, v114
	v_fmac_f32_e32 v47, v17, v117
	s_waitcnt vmcnt(3)
	v_pk_add_f32 v[12:13], v[12:13], 1.0 op_sel_hi:[1,0]
	v_pk_add_f32 v[10:11], v[10:11], 1.0 op_sel_hi:[1,0]
	s_waitcnt vmcnt(2)
	v_pk_mul_f32 v[12:13], v[8:9], v[12:13]
	v_pk_mul_f32 v[10:11], v[6:7], v[10:11]
	global_load_dwordx4 v[6:9], v[90:91], off
	global_load_dwordx4 v[114:117], v[92:93], off
	global_load_dwordx4 v[120:123], v[40:41], off
	v_pk_mul_f32 v[14:15], v[102:103], v[108:109] op_sel_hi:[0,1]
	v_pk_mul_f32 v[16:17], v[102:103], v[106:107] op_sel_hi:[0,1]
	v_pk_fma_f32 v[106:107], v[16:17], v[12:13], v[4:5]
	v_pk_fma_f32 v[108:109], v[14:15], v[10:11], v[2:3]
	v_pk_mul_f32 v[14:15], v[104:105], v[20:21] op_sel_hi:[0,1]
	v_pk_mul_f32 v[16:17], v[104:105], v[18:19] op_sel_hi:[0,1]
	v_pk_fma_f32 v[110:111], v[16:17], v[12:13], v[4:5]
	v_pk_fma_f32 v[112:113], v[14:15], v[10:11], v[2:3]
	v_med3_f32 v2, v108, s33, v233
	v_med3_f32 v3, v109, s33, v233
	v_mov_b32_e32 v4, 0
	v_cvt_pk_fp8_f32 v4, v2, v3
	v_med3_f32 v2, v106, s33, v233
	v_med3_f32 v3, v107, s33, v233
	v_cvt_pk_fp8_f32 v4, v2, v3 op_sel:[0,0,1]
	v_med3_f32 v2, v112, s33, v233
	v_med3_f32 v3, v113, s33, v233
	global_store_dword v[118:119], v4, off offset:1536
	v_mov_b32_e32 v4, 0
	v_cvt_pk_fp8_f32 v4, v2, v3
	v_med3_f32 v2, v110, s33, v233
	v_med3_f32 v3, v111, s33, v233
	v_cvt_pk_fp8_f32 v4, v2, v3 op_sel:[0,0,1]
	global_store_dword v[118:119], v4, off offset:3584
	ds_read_b128 v[10:13], v172
	ds_read_b128 v[124:127], v173
	ds_read_b128 v[128:131], v174
	ds_read_b128 v[132:135], v175
	ds_read_b128 v[14:17], v176
	ds_read_b128 v[136:139], v177
	ds_read_b128 v[140:143], v178
	ds_read_b128 v[144:147], v179
	ds_read_b128 v[18:21], v180
	ds_read_b128 v[148:151], v181
	ds_read_b128 v[238:241], v182
	ds_read_b128 v[242:245], v183
	ds_read_b128 v[2:5], v184
	ds_read_b128 v[246:249], v185
	ds_read_b128 v[234:237], v186
	ds_read_b128 v[160:163], v187
	s_waitcnt vmcnt(3)
	v_pk_add_f32 v[116:117], v[116:117], 1.0 op_sel_hi:[1,0]
	v_pk_add_f32 v[154:155], v[114:115], 1.0 op_sel_hi:[1,0]
	s_waitcnt lgkmcnt(14)
	v_fmac_f32_e32 v215, v112, v13
	v_fmac_f32_e32 v219, v112, v12
	v_fmac_f32_e32 v222, v112, v11
	v_fmac_f32_e32 v225, v112, v10
	v_fmac_f32_e32 v217, v108, v13
	v_fmac_f32_e32 v221, v108, v12
	v_fmac_f32_e32 v223, v108, v11
	v_fmac_f32_e32 v224, v108, v10
	s_waitcnt vmcnt(2)
	v_pk_mul_f32 v[114:115], v[122:123], v[116:117]
	v_pk_mul_f32 v[116:117], v[120:121], v[154:155]
	s_waitcnt lgkmcnt(11)
	v_fmac_f32_e32 v215, v113, v17
	v_fmac_f32_e32 v219, v113, v16
	v_fmac_f32_e32 v222, v113, v15
	v_fmac_f32_e32 v225, v113, v14
	v_fmac_f32_e32 v217, v109, v17
	v_fmac_f32_e32 v221, v109, v16
	v_fmac_f32_e32 v223, v109, v15
	v_fmac_f32_e32 v224, v109, v14
	v_pk_mul_f32 v[10:11], v[102:103], v[100:101] op_sel_hi:[0,1]
	s_waitcnt lgkmcnt(7)
	v_fmac_f32_e32 v215, v110, v21
	v_fmac_f32_e32 v219, v110, v20
	v_fmac_f32_e32 v222, v110, v19
	v_fmac_f32_e32 v225, v110, v18
	v_fmac_f32_e32 v217, v106, v21
	v_fmac_f32_e32 v221, v106, v20
	v_fmac_f32_e32 v223, v106, v19
	v_fmac_f32_e32 v224, v106, v18
	v_pk_fma_f32 v[18:19], v[10:11], v[116:117], v[6:7]
	v_pk_mul_f32 v[10:11], v[104:105], v[96:97] op_sel_hi:[0,1]
	s_waitcnt lgkmcnt(3)
	v_fmac_f32_e32 v215, v111, v5
	v_fmac_f32_e32 v219, v111, v4
	v_fmac_f32_e32 v222, v111, v3
	v_fmac_f32_e32 v217, v107, v5
	v_fmac_f32_e32 v221, v107, v4
	v_fmac_f32_e32 v223, v107, v3
	v_pk_mul_f32 v[4:5], v[102:103], v[98:99] op_sel_hi:[0,1]
	v_pk_mul_f32 v[12:13], v[104:105], v[94:95] op_sel_hi:[0,1]
	v_pk_fma_f32 v[6:7], v[10:11], v[116:117], v[6:7]
	v_med3_f32 v3, v18, s33, v233
	v_med3_f32 v10, v19, s33, v233
	v_mov_b32_e32 v14, 0
	v_pk_fma_f32 v[4:5], v[4:5], v[114:115], v[8:9]
	v_pk_fma_f32 v[8:9], v[12:13], v[114:115], v[8:9]
	v_cvt_pk_fp8_f32 v14, v3, v10
	v_med3_f32 v11, v6, s33, v233
	v_med3_f32 v12, v7, s33, v233
	v_mov_b32_e32 v15, 0
	v_cvt_pk_fp8_f32 v15, v11, v12
	v_med3_f32 v3, v4, s33, v233
	v_med3_f32 v10, v5, s33, v233
	v_cvt_pk_fp8_f32 v14, v3, v10 op_sel:[0,0,1]
	v_med3_f32 v3, v8, s33, v233
	v_med3_f32 v10, v9, s33, v233
	v_cvt_pk_fp8_f32 v15, v3, v10 op_sel:[0,0,1]
	ds_read_b128 v[10:13], v188
	global_store_dword v[118:119], v14, off offset:1792
	global_store_dword v[118:119], v15, off offset:3840
	ds_read_b128 v[14:17], v189
	v_fmac_f32_e32 v210, v112, v127
	v_fmac_f32_e32 v212, v112, v126
	v_fmac_f32_e32 v214, v112, v125
	v_fmac_f32_e32 v218, v112, v124
	v_fmac_f32_e32 v211, v108, v127
	v_fmac_f32_e32 v213, v108, v126
	v_fmac_f32_e32 v216, v108, v125
	v_fmac_f32_e32 v220, v108, v124
	v_fmac_f32_e32 v210, v113, v139
	v_fmac_f32_e32 v212, v113, v138
	v_fmac_f32_e32 v214, v113, v137
	v_fmac_f32_e32 v218, v113, v136
	v_fmac_f32_e32 v211, v109, v139
	v_fmac_f32_e32 v213, v109, v138
	v_fmac_f32_e32 v216, v109, v137
	v_fmac_f32_e32 v220, v109, v136
	v_fmac_f32_e32 v210, v110, v151
	v_fmac_f32_e32 v212, v110, v150
	v_fmac_f32_e32 v214, v110, v149
	v_fmac_f32_e32 v218, v110, v148
	v_fmac_f32_e32 v211, v106, v151
	v_fmac_f32_e32 v213, v106, v150
	v_fmac_f32_e32 v216, v106, v149
	v_fmac_f32_e32 v220, v106, v148
	s_waitcnt lgkmcnt(4)
	v_fmac_f32_e32 v210, v111, v249
	v_fmac_f32_e32 v212, v111, v248
	v_fmac_f32_e32 v214, v111, v247
	v_fmac_f32_e32 v218, v111, v246
	v_fmac_f32_e32 v211, v107, v249
	v_fmac_f32_e32 v213, v107, v248
	v_fmac_f32_e32 v216, v107, v247
	v_fmac_f32_e32 v220, v107, v246
	v_fmac_f32_e32 v225, v111, v2
	v_fmac_f32_e32 v224, v107, v2
	s_waitcnt lgkmcnt(1)
	v_fmac_f32_e32 v224, v18, v10
	v_fmac_f32_e32 v223, v18, v11
	v_fmac_f32_e32 v221, v18, v12
	v_fmac_f32_e32 v217, v18, v13
	v_fmac_f32_e32 v225, v6, v10
	v_fmac_f32_e32 v222, v6, v11
	v_fmac_f32_e32 v219, v6, v12
	v_fmac_f32_e32 v215, v6, v13
	ds_read_b128 v[10:13], v190
	s_waitcnt lgkmcnt(1)
	v_fmac_f32_e32 v220, v18, v14
	v_fmac_f32_e32 v216, v18, v15
	v_fmac_f32_e32 v213, v18, v16
	v_fmac_f32_e32 v211, v18, v17
	v_fmac_f32_e32 v218, v6, v14
	v_fmac_f32_e32 v214, v6, v15
	v_fmac_f32_e32 v212, v6, v16
	v_fmac_f32_e32 v210, v6, v17
	ds_read_b128 v[14:17], v191
	v_fmac_f32_e32 v47, v112, v135
	v_fmac_f32_e32 v51, v112, v134
	v_fmac_f32_e32 v55, v112, v133
	v_fmac_f32_e32 v156, v112, v132
	v_fmac_f32_e32 v49, v108, v135
	v_fmac_f32_e32 v53, v108, v134
	v_fmac_f32_e32 v152, v108, v133
	v_fmac_f32_e32 v159, v108, v132
	v_fmac_f32_e32 v57, v112, v131
	v_fmac_f32_e32 v158, v112, v130
	v_fmac_f32_e32 v206, v112, v129
	v_fmac_f32_e32 v208, v112, v128
	v_fmac_f32_e32 v153, v108, v131
	v_fmac_f32_e32 v205, v108, v130
	v_fmac_f32_e32 v207, v108, v129
	v_fmac_f32_e32 v209, v108, v128
	v_fmac_f32_e32 v47, v113, v147
	v_fmac_f32_e32 v51, v113, v146
	v_fmac_f32_e32 v55, v113, v145
	v_fmac_f32_e32 v156, v113, v144
	v_fmac_f32_e32 v49, v109, v147
	v_fmac_f32_e32 v53, v109, v146
	v_fmac_f32_e32 v152, v109, v145
	v_fmac_f32_e32 v159, v109, v144
	v_fmac_f32_e32 v57, v113, v143
	v_fmac_f32_e32 v158, v113, v142
	v_fmac_f32_e32 v206, v113, v141
	v_fmac_f32_e32 v208, v113, v140
	v_fmac_f32_e32 v153, v109, v143
	v_fmac_f32_e32 v205, v109, v142
	v_fmac_f32_e32 v207, v109, v141
	v_fmac_f32_e32 v209, v109, v140
	v_fmac_f32_e32 v47, v110, v245
	v_fmac_f32_e32 v51, v110, v244
	v_fmac_f32_e32 v55, v110, v243
	v_fmac_f32_e32 v156, v110, v242
	v_fmac_f32_e32 v49, v106, v245
	v_fmac_f32_e32 v53, v106, v244
	v_fmac_f32_e32 v152, v106, v243
	v_fmac_f32_e32 v159, v106, v242
	v_fmac_f32_e32 v57, v110, v241
	v_fmac_f32_e32 v158, v110, v240
	v_fmac_f32_e32 v206, v110, v239
	v_fmac_f32_e32 v208, v110, v238
	v_fmac_f32_e32 v153, v106, v241
	v_fmac_f32_e32 v205, v106, v240
	v_fmac_f32_e32 v207, v106, v239
	v_fmac_f32_e32 v209, v106, v238
	v_fmac_f32_e32 v47, v111, v163
	v_fmac_f32_e32 v51, v111, v162
	v_fmac_f32_e32 v55, v111, v161
	v_fmac_f32_e32 v156, v111, v160
	v_fmac_f32_e32 v49, v107, v163
	v_fmac_f32_e32 v53, v107, v162
	v_fmac_f32_e32 v152, v107, v161
	v_fmac_f32_e32 v159, v107, v160
	v_fmac_f32_e32 v57, v111, v237
	v_fmac_f32_e32 v158, v111, v236
	v_fmac_f32_e32 v206, v111, v235
	v_fmac_f32_e32 v208, v111, v234
	v_fmac_f32_e32 v153, v107, v237
	v_fmac_f32_e32 v205, v107, v236
	v_fmac_f32_e32 v207, v107, v235
	v_fmac_f32_e32 v209, v107, v234
	s_waitcnt lgkmcnt(1)
	v_fmac_f32_e32 v209, v18, v10
	v_fmac_f32_e32 v207, v18, v11
	v_fmac_f32_e32 v205, v18, v12
	v_fmac_f32_e32 v153, v18, v13
	v_fmac_f32_e32 v208, v6, v10
	v_fmac_f32_e32 v206, v6, v11
	v_fmac_f32_e32 v158, v6, v12
	v_fmac_f32_e32 v57, v6, v13
	ds_read_b128 v[10:13], v192
	s_waitcnt lgkmcnt(1)
	v_fmac_f32_e32 v159, v18, v14
	v_fmac_f32_e32 v152, v18, v15
	v_fmac_f32_e32 v53, v18, v16
	v_fmac_f32_e32 v49, v18, v17
	v_fmac_f32_e32 v156, v6, v14
	v_fmac_f32_e32 v55, v6, v15
	v_fmac_f32_e32 v51, v6, v16
	v_fmac_f32_e32 v47, v6, v17
	ds_read_b128 v[14:17], v193
	s_waitcnt lgkmcnt(1)
	v_fmac_f32_e32 v224, v19, v10
	v_fmac_f32_e32 v223, v19, v11
	v_fmac_f32_e32 v221, v19, v12
	v_fmac_f32_e32 v217, v19, v13
	v_fmac_f32_e32 v225, v7, v10
	v_fmac_f32_e32 v222, v7, v11
	v_fmac_f32_e32 v219, v7, v12
	v_fmac_f32_e32 v215, v7, v13
	ds_read_b128 v[10:13], v194
	s_waitcnt lgkmcnt(1)
	v_fmac_f32_e32 v220, v19, v14
	v_fmac_f32_e32 v216, v19, v15
	v_fmac_f32_e32 v213, v19, v16
	v_fmac_f32_e32 v211, v19, v17
	v_fmac_f32_e32 v218, v7, v14
	v_fmac_f32_e32 v214, v7, v15
	v_fmac_f32_e32 v212, v7, v16
	v_fmac_f32_e32 v210, v7, v17
	ds_read_b128 v[14:17], v195
	s_waitcnt lgkmcnt(1)
	v_fmac_f32_e32 v209, v19, v10
	v_fmac_f32_e32 v207, v19, v11
	v_fmac_f32_e32 v205, v19, v12
	v_fmac_f32_e32 v153, v19, v13
	v_fmac_f32_e32 v208, v7, v10
	v_fmac_f32_e32 v206, v7, v11
	v_fmac_f32_e32 v158, v7, v12
	v_fmac_f32_e32 v57, v7, v13
	ds_read_b128 v[10:13], v196
	s_waitcnt lgkmcnt(1)
	v_fmac_f32_e32 v159, v19, v14
	v_fmac_f32_e32 v152, v19, v15
	v_fmac_f32_e32 v53, v19, v16
	v_fmac_f32_e32 v49, v19, v17
	v_fmac_f32_e32 v156, v7, v14
	v_fmac_f32_e32 v55, v7, v15
	v_fmac_f32_e32 v51, v7, v16
	v_fmac_f32_e32 v47, v7, v17
	ds_read_b128 v[14:17], v197
	s_waitcnt lgkmcnt(1)
	v_fmac_f32_e32 v224, v4, v10
	v_fmac_f32_e32 v223, v4, v11
	v_fmac_f32_e32 v221, v4, v12
	v_fmac_f32_e32 v217, v4, v13
	v_fmac_f32_e32 v225, v8, v10
	v_fmac_f32_e32 v222, v8, v11
	v_fmac_f32_e32 v219, v8, v12
	v_fmac_f32_e32 v215, v8, v13
	ds_read_b128 v[10:13], v198
	s_waitcnt lgkmcnt(1)
	v_fmac_f32_e32 v220, v4, v14
	v_fmac_f32_e32 v216, v4, v15
	v_fmac_f32_e32 v213, v4, v16
	v_fmac_f32_e32 v211, v4, v17
	v_fmac_f32_e32 v218, v8, v14
	v_fmac_f32_e32 v214, v8, v15
	v_fmac_f32_e32 v212, v8, v16
	v_fmac_f32_e32 v210, v8, v17
	ds_read_b128 v[14:17], v199
	s_waitcnt lgkmcnt(1)
	v_fmac_f32_e32 v209, v4, v10
	v_fmac_f32_e32 v207, v4, v11
	v_fmac_f32_e32 v205, v4, v12
	v_fmac_f32_e32 v153, v4, v13
	v_fmac_f32_e32 v208, v8, v10
	v_fmac_f32_e32 v206, v8, v11
	v_fmac_f32_e32 v158, v8, v12
	v_fmac_f32_e32 v57, v8, v13
	ds_read_b128 v[10:13], v200
	s_waitcnt lgkmcnt(1)
	v_fmac_f32_e32 v159, v4, v14
	v_fmac_f32_e32 v152, v4, v15
	v_fmac_f32_e32 v53, v4, v16
	v_fmac_f32_e32 v49, v4, v17
	v_fmac_f32_e32 v156, v8, v14
	v_fmac_f32_e32 v55, v8, v15
	v_fmac_f32_e32 v51, v8, v16
	v_fmac_f32_e32 v47, v8, v17
	ds_read_b128 v[14:17], v201
	s_waitcnt lgkmcnt(1)
	v_fmac_f32_e32 v224, v5, v10
	v_fmac_f32_e32 v223, v5, v11
	v_fmac_f32_e32 v221, v5, v12
	v_fmac_f32_e32 v217, v5, v13
	v_fmac_f32_e32 v225, v9, v10
	v_fmac_f32_e32 v222, v9, v11
	v_fmac_f32_e32 v219, v9, v12
	v_fmac_f32_e32 v215, v9, v13
	ds_read_b128 v[10:13], v202
	s_waitcnt lgkmcnt(1)
	v_fmac_f32_e32 v220, v5, v14
	v_fmac_f32_e32 v216, v5, v15
	v_fmac_f32_e32 v213, v5, v16
	v_fmac_f32_e32 v211, v5, v17
	v_fmac_f32_e32 v218, v9, v14
	v_fmac_f32_e32 v214, v9, v15
	v_fmac_f32_e32 v212, v9, v16
	v_fmac_f32_e32 v210, v9, v17
	ds_read_b128 v[14:17], v203
	s_waitcnt lgkmcnt(1)
	v_fmac_f32_e32 v57, v9, v13
	v_fmac_f32_e32 v209, v5, v10
	v_fmac_f32_e32 v207, v5, v11
	v_fmac_f32_e32 v205, v5, v12
	s_waitcnt lgkmcnt(0)
	v_fmac_f32_e32 v53, v5, v16
	v_fmac_f32_e32 v55, v9, v15
	v_fmac_f32_e32 v51, v9, v16
	v_fmac_f32_e32 v153, v5, v13
	v_fmac_f32_e32 v208, v9, v10
	v_fmac_f32_e32 v206, v9, v11
	v_fmac_f32_e32 v158, v9, v12
	v_fmac_f32_e32 v159, v5, v14
	v_fmac_f32_e32 v152, v5, v15
	v_fmac_f32_e32 v49, v5, v17
	v_fmac_f32_e32 v156, v9, v14
	v_fmac_f32_e32 v47, v9, v17
	ds_bpermute_b32 v10, v23, v221
	ds_bpermute_b32 v12, v23, v219
	ds_bpermute_b32 v14, v23, v217
	ds_bpermute_b32 v2, v23, v224
	ds_bpermute_b32 v3, v23, v225
	s_waitcnt lgkmcnt(4)
	v_add_f32_e32 v10, v221, v10
	ds_bpermute_b32 v11, v25, v10
	s_waitcnt lgkmcnt(4)
	v_add_f32_e32 v12, v219, v12
	ds_bpermute_b32 v13, v25, v12
	ds_bpermute_b32 v6, v23, v223
	ds_bpermute_b32 v8, v23, v222
	s_waitcnt lgkmcnt(3)
	v_add_f32_e32 v10, v10, v11
	ds_bpermute_b32 v11, v43, v10
	s_waitcnt lgkmcnt(3)
	v_add_f32_e32 v12, v12, v13
	ds_bpermute_b32 v13, v43, v12
	v_add_f32_e32 v2, v224, v2
	v_add_f32_e32 v3, v225, v3
	s_waitcnt lgkmcnt(1)
	v_add_f32_e32 v10, v10, v11
	ds_bpermute_b32 v11, v103, v10
	v_add_f32_e32 v6, v223, v6
	v_add_f32_e32 v8, v222, v8
	ds_bpermute_b32 v4, v25, v2
	ds_bpermute_b32 v5, v25, v3
	s_waitcnt lgkmcnt(2)
	v_add_f32_e32 v10, v10, v11
	v_mov_b32_e32 v11, v10
	s_nop 1
	v_permlane16_swap_b32_e32 v10, v11
	v_add_f32_e32 v19, v10, v11
	v_add_f32_e32 v10, v12, v13
	v_add_f32_e32 v12, v217, v14
	ds_bpermute_b32 v13, v25, v12
	ds_bpermute_b32 v11, v103, v10
	ds_bpermute_b32 v14, v23, v215
	ds_bpermute_b32 v7, v25, v6
	ds_bpermute_b32 v9, v25, v8
	s_waitcnt lgkmcnt(4)
	v_add_f32_e32 v12, v12, v13
	ds_bpermute_b32 v13, v43, v12
	s_waitcnt lgkmcnt(4)
	v_add_f32_e32 v10, v10, v11
	v_mov_b32_e32 v11, v10
	s_nop 1
	v_permlane16_swap_b32_e32 v10, v11
	v_add_f32_e32 v97, v10, v11
	s_waitcnt lgkmcnt(0)
	v_add_f32_e32 v10, v12, v13
	v_add_f32_e32 v12, v215, v14
	ds_bpermute_b32 v13, v25, v12
	ds_bpermute_b32 v11, v103, v10
	ds_bpermute_b32 v14, v23, v220
	v_add_f32_e32 v2, v2, v4
	v_add_f32_e32 v3, v3, v5
	s_waitcnt lgkmcnt(2)
	v_add_f32_e32 v12, v12, v13
	ds_bpermute_b32 v13, v43, v12
	s_waitcnt lgkmcnt(2)
	v_add_f32_e32 v10, v10, v11
	v_mov_b32_e32 v11, v10
	s_nop 1
	v_permlane16_swap_b32_e32 v10, v11
	v_add_f32_e32 v21, v10, v11
	s_waitcnt lgkmcnt(0)
	v_add_f32_e32 v10, v12, v13
	v_add_f32_e32 v12, v220, v14
	ds_bpermute_b32 v13, v25, v12
	ds_bpermute_b32 v11, v103, v10
	ds_bpermute_b32 v14, v23, v218
	v_add_f32_e32 v6, v6, v7
	v_add_f32_e32 v8, v8, v9
	s_waitcnt lgkmcnt(2)
	v_add_f32_e32 v12, v12, v13
	ds_bpermute_b32 v13, v43, v12
	s_waitcnt lgkmcnt(2)
	v_add_f32_e32 v10, v10, v11
	v_mov_b32_e32 v11, v10
	s_nop 1
	v_permlane16_swap_b32_e32 v10, v11
	v_add_f32_e32 v99, v10, v11
	s_waitcnt lgkmcnt(0)
	v_add_f32_e32 v10, v12, v13
	v_add_f32_e32 v12, v218, v14
	ds_bpermute_b32 v13, v25, v12
	ds_bpermute_b32 v11, v103, v10
	ds_bpermute_b32 v14, v23, v216
	ds_bpermute_b32 v4, v43, v2
	ds_bpermute_b32 v5, v43, v3
	s_waitcnt lgkmcnt(4)
	v_add_f32_e32 v12, v12, v13
	ds_bpermute_b32 v13, v43, v12
	s_waitcnt lgkmcnt(4)
	v_add_f32_e32 v10, v10, v11
	v_mov_b32_e32 v11, v10
	s_nop 1
	v_permlane16_swap_b32_e32 v10, v11
	v_add_f32_e32 v95, v10, v11
	s_waitcnt lgkmcnt(0)
	v_add_f32_e32 v10, v12, v13
	v_add_f32_e32 v12, v216, v14
	ds_bpermute_b32 v13, v25, v12
	ds_bpermute_b32 v11, v103, v10
	ds_bpermute_b32 v14, v23, v214
	ds_bpermute_b32 v7, v43, v6
	ds_bpermute_b32 v9, v43, v8
	s_waitcnt lgkmcnt(4)
	v_add_f32_e32 v12, v12, v13
	ds_bpermute_b32 v13, v43, v12
	s_waitcnt lgkmcnt(4)
	v_add_f32_e32 v10, v10, v11
	v_mov_b32_e32 v11, v10
	s_nop 1
	v_permlane16_swap_b32_e32 v10, v11
	v_add_f32_e32 v101, v10, v11
	s_waitcnt lgkmcnt(0)
	v_add_f32_e32 v10, v12, v13
	v_add_f32_e32 v12, v214, v14
	ds_bpermute_b32 v13, v25, v12
	ds_bpermute_b32 v11, v103, v10
	ds_bpermute_b32 v14, v23, v213
	v_add_f32_e32 v2, v2, v4
	v_add_f32_e32 v3, v3, v5
	s_waitcnt lgkmcnt(2)
	v_add_f32_e32 v12, v12, v13
	ds_bpermute_b32 v13, v43, v12
	s_waitcnt lgkmcnt(2)
	v_add_f32_e32 v10, v10, v11
	v_mov_b32_e32 v11, v10
	s_nop 1
	v_permlane16_swap_b32_e32 v10, v11
	v_add_f32_e32 v107, v10, v11
	s_waitcnt lgkmcnt(0)
	v_add_f32_e32 v10, v12, v13
	v_add_f32_e32 v12, v213, v14
	ds_bpermute_b32 v13, v25, v12
	ds_bpermute_b32 v11, v103, v10
	ds_bpermute_b32 v14, v23, v212
	v_add_f32_e32 v6, v6, v7
	v_add_f32_e32 v8, v8, v9
	s_waitcnt lgkmcnt(2)
	v_add_f32_e32 v12, v12, v13
	ds_bpermute_b32 v13, v43, v12
	s_waitcnt lgkmcnt(2)
	v_add_f32_e32 v10, v10, v11
	v_mov_b32_e32 v11, v10
	s_nop 1
	v_permlane16_swap_b32_e32 v10, v11
	v_add_f32_e32 v115, v10, v11
	s_waitcnt lgkmcnt(0)
	v_add_f32_e32 v10, v12, v13
	v_add_f32_e32 v12, v212, v14
	ds_bpermute_b32 v13, v25, v12
	ds_bpermute_b32 v11, v103, v10
	ds_bpermute_b32 v14, v23, v211
	ds_bpermute_b32 v4, v103, v2
	ds_bpermute_b32 v5, v103, v3
	s_waitcnt lgkmcnt(4)
	v_add_f32_e32 v12, v12, v13
	ds_bpermute_b32 v13, v43, v12
	s_waitcnt lgkmcnt(4)
	v_add_f32_e32 v10, v10, v11
	v_mov_b32_e32 v11, v10
	s_nop 1
	v_permlane16_swap_b32_e32 v10, v11
	v_add_f32_e32 v104, v10, v11
	s_waitcnt lgkmcnt(0)
	v_add_f32_e32 v10, v12, v13
	v_add_f32_e32 v12, v211, v14
	ds_bpermute_b32 v13, v25, v12
	ds_bpermute_b32 v11, v103, v10
	ds_bpermute_b32 v14, v23, v210
	ds_bpermute_b32 v7, v103, v6
	ds_bpermute_b32 v9, v103, v8
	s_waitcnt lgkmcnt(4)
	v_add_f32_e32 v12, v12, v13
	ds_bpermute_b32 v13, v43, v12
	s_waitcnt lgkmcnt(4)
	v_add_f32_e32 v10, v10, v11
	v_mov_b32_e32 v11, v10
	s_nop 1
	v_permlane16_swap_b32_e32 v10, v11
	v_add_f32_e32 v113, v10, v11
	s_waitcnt lgkmcnt(0)
	v_add_f32_e32 v10, v12, v13
	v_add_f32_e32 v12, v210, v14
	ds_bpermute_b32 v13, v25, v12
	ds_bpermute_b32 v11, v103, v10
	ds_bpermute_b32 v14, v23, v209
	v_add_f32_e32 v2, v2, v4
	v_add_f32_e32 v4, v3, v5
	s_waitcnt lgkmcnt(2)
	v_add_f32_e32 v12, v12, v13
	ds_bpermute_b32 v13, v43, v12
	s_waitcnt lgkmcnt(2)
	v_add_f32_e32 v10, v10, v11
	v_mov_b32_e32 v11, v10
	s_nop 1
	v_permlane16_swap_b32_e32 v10, v11
	v_add_f32_e32 v109, v10, v11
	s_waitcnt lgkmcnt(0)
	v_add_f32_e32 v10, v12, v13
	v_add_f32_e32 v12, v209, v14
	ds_bpermute_b32 v13, v25, v12
	ds_bpermute_b32 v11, v103, v10
	ds_bpermute_b32 v14, v23, v208
	v_add_f32_e32 v6, v6, v7
	v_add_f32_e32 v8, v8, v9
	s_waitcnt lgkmcnt(2)
	v_add_f32_e32 v12, v12, v13
	ds_bpermute_b32 v13, v43, v12
	s_waitcnt lgkmcnt(2)
	v_add_f32_e32 v10, v10, v11
	v_mov_b32_e32 v11, v10
	s_nop 1
	v_permlane16_swap_b32_e32 v10, v11
	v_add_f32_e32 v117, v10, v11
	s_waitcnt lgkmcnt(0)
	v_add_f32_e32 v10, v12, v13
	v_add_f32_e32 v12, v208, v14
	ds_bpermute_b32 v13, v25, v12
	ds_bpermute_b32 v11, v103, v10
	ds_bpermute_b32 v14, v23, v207
	v_mov_b32_e32 v3, v2
	v_mov_b32_e32 v5, v4
	s_waitcnt lgkmcnt(2)
	v_add_f32_e32 v12, v12, v13
	ds_bpermute_b32 v13, v43, v12
	s_waitcnt lgkmcnt(2)
	v_add_f32_e32 v10, v10, v11
	v_mov_b32_e32 v11, v10
	s_nop 1
	v_permlane16_swap_b32_e32 v10, v11
	v_add_f32_e32 v111, v10, v11
	s_waitcnt lgkmcnt(0)
	v_add_f32_e32 v10, v12, v13
	v_add_f32_e32 v12, v207, v14
	ds_bpermute_b32 v13, v25, v12
	ds_bpermute_b32 v11, v103, v10
	ds_bpermute_b32 v14, v23, v206
	v_mov_b32_e32 v7, v6
	v_mov_b32_e32 v9, v8
	s_waitcnt lgkmcnt(2)
	v_add_f32_e32 v12, v12, v13
	ds_bpermute_b32 v13, v43, v12
	s_waitcnt lgkmcnt(2)
	v_add_f32_e32 v10, v10, v11
	v_mov_b32_e32 v11, v10
	s_nop 1
	v_permlane16_swap_b32_e32 v10, v11
	v_add_f32_e32 v119, v10, v11
	s_waitcnt lgkmcnt(0)
	v_add_f32_e32 v10, v12, v13
	v_add_f32_e32 v12, v206, v14
	ds_bpermute_b32 v13, v25, v12
	ds_bpermute_b32 v11, v103, v10
	ds_bpermute_b32 v14, v23, v205
	v_permlane16_swap_b32_e32 v2, v3
	s_waitcnt lgkmcnt(2)
	v_add_f32_e32 v12, v12, v13
	ds_bpermute_b32 v13, v43, v12
	s_waitcnt lgkmcnt(2)
	v_add_f32_e32 v10, v10, v11
	v_mov_b32_e32 v11, v10
	s_nop 1
	v_permlane16_swap_b32_e32 v10, v11
	v_add_f32_e32 v123, v10, v11
	s_waitcnt lgkmcnt(0)
	v_add_f32_e32 v10, v12, v13
	v_add_f32_e32 v12, v205, v14
	ds_bpermute_b32 v13, v25, v12
	ds_bpermute_b32 v11, v103, v10
	ds_bpermute_b32 v14, v23, v158
	v_permlane16_swap_b32_e32 v4, v5
	s_waitcnt lgkmcnt(2)
	v_add_f32_e32 v12, v12, v13
	ds_bpermute_b32 v13, v43, v12
	s_waitcnt lgkmcnt(2)
	v_add_f32_e32 v10, v10, v11
	v_mov_b32_e32 v11, v10
	s_nop 1
	v_permlane16_swap_b32_e32 v10, v11
	v_add_f32_e32 v130, v10, v11
	s_waitcnt lgkmcnt(0)
	v_add_f32_e32 v10, v12, v13
	v_add_f32_e32 v12, v158, v14
	ds_bpermute_b32 v13, v25, v12
	ds_bpermute_b32 v11, v103, v10
	ds_bpermute_b32 v14, v23, v153
	v_permlane16_swap_b32_e32 v6, v7
	s_waitcnt lgkmcnt(2)
	v_add_f32_e32 v12, v12, v13
	ds_bpermute_b32 v13, v43, v12
	s_waitcnt lgkmcnt(2)
	v_add_f32_e32 v10, v10, v11
	v_mov_b32_e32 v11, v10
	s_nop 1
	v_permlane16_swap_b32_e32 v10, v11
	v_add_f32_e32 v121, v10, v11
	s_waitcnt lgkmcnt(0)
	v_add_f32_e32 v10, v12, v13
	v_add_f32_e32 v12, v153, v14
	ds_bpermute_b32 v13, v25, v12
	ds_bpermute_b32 v11, v103, v10
	ds_bpermute_b32 v14, v23, v57
	v_permlane16_swap_b32_e32 v8, v9
	s_waitcnt lgkmcnt(2)
	v_add_f32_e32 v12, v12, v13
	ds_bpermute_b32 v13, v43, v12
	s_waitcnt lgkmcnt(2)
	v_add_f32_e32 v10, v10, v11
	v_mov_b32_e32 v11, v10
	s_nop 1
	v_permlane16_swap_b32_e32 v10, v11
	v_add_f32_e32 v128, v10, v11
	s_waitcnt lgkmcnt(0)
	v_add_f32_e32 v10, v12, v13
	v_add_f32_e32 v12, v57, v14
	ds_bpermute_b32 v13, v25, v12
	ds_bpermute_b32 v11, v103, v10
	ds_bpermute_b32 v14, v23, v159
	v_add_f32_e32 v2, v2, v3
	v_add_f32_e32 v4, v4, v5
	s_waitcnt lgkmcnt(2)
	v_add_f32_e32 v12, v12, v13
	ds_bpermute_b32 v13, v43, v12
	s_waitcnt lgkmcnt(2)
	v_add_f32_e32 v10, v10, v11
	v_mov_b32_e32 v11, v10
	s_nop 1
	v_permlane16_swap_b32_e32 v10, v11
	v_add_f32_e32 v57, v10, v11
	s_waitcnt lgkmcnt(0)
	v_add_f32_e32 v10, v12, v13
	v_add_f32_e32 v12, v159, v14
	ds_bpermute_b32 v13, v25, v12
	ds_bpermute_b32 v11, v103, v10
	ds_bpermute_b32 v14, v23, v156
	v_add_f32_e32 v6, v6, v7
	v_add_f32_e32 v8, v8, v9
	s_waitcnt lgkmcnt(2)
	v_add_f32_e32 v12, v12, v13
	ds_bpermute_b32 v13, v43, v12
	s_waitcnt lgkmcnt(2)
	v_add_f32_e32 v10, v10, v11
	v_mov_b32_e32 v11, v10
	s_nop 1
	v_permlane16_swap_b32_e32 v10, v11
	v_add_f32_e32 v132, v10, v11
	s_waitcnt lgkmcnt(0)
	v_add_f32_e32 v10, v12, v13
	v_add_f32_e32 v12, v156, v14
	ds_bpermute_b32 v13, v25, v12
	ds_bpermute_b32 v11, v103, v10
	ds_bpermute_b32 v14, v23, v152
	v_mov_b32_e32 v3, v2
	v_mov_b32_e32 v5, v4
	s_waitcnt lgkmcnt(2)
	v_add_f32_e32 v12, v12, v13
	ds_bpermute_b32 v13, v43, v12
	s_waitcnt lgkmcnt(2)
	v_add_f32_e32 v10, v10, v11
	v_mov_b32_e32 v11, v10
	s_nop 1
	v_permlane16_swap_b32_e32 v10, v11
	v_add_f32_e32 v126, v10, v11
	s_waitcnt lgkmcnt(0)
	v_add_f32_e32 v10, v12, v13
	v_add_f32_e32 v12, v152, v14
	ds_bpermute_b32 v13, v25, v12
	ds_bpermute_b32 v11, v103, v10
	ds_bpermute_b32 v14, v23, v55
	v_mov_b32_e32 v7, v6
	v_mov_b32_e32 v9, v8
	s_waitcnt lgkmcnt(2)
	v_add_f32_e32 v12, v12, v13
	ds_bpermute_b32 v13, v43, v12
	s_waitcnt lgkmcnt(2)
	v_add_f32_e32 v10, v10, v11
	v_mov_b32_e32 v11, v10
	s_nop 1
	v_permlane16_swap_b32_e32 v10, v11
	v_add_f32_e32 v134, v10, v11
	s_waitcnt lgkmcnt(0)
	v_add_f32_e32 v10, v12, v13
	v_add_f32_e32 v12, v55, v14
	ds_bpermute_b32 v13, v25, v12
	ds_bpermute_b32 v11, v103, v10
	ds_bpermute_b32 v14, v23, v53
	v_mov_b32_e32 v20, v19
	v_mov_b32_e32 v98, v97
	s_waitcnt lgkmcnt(2)
	v_add_f32_e32 v12, v12, v13
	ds_bpermute_b32 v13, v43, v12
	s_waitcnt lgkmcnt(2)
	v_add_f32_e32 v10, v10, v11
	v_mov_b32_e32 v11, v10
	s_nop 1
	v_permlane16_swap_b32_e32 v10, v11
	v_add_f32_e32 v55, v10, v11
	s_waitcnt lgkmcnt(0)
	v_add_f32_e32 v10, v12, v13
	v_add_f32_e32 v12, v53, v14
	ds_bpermute_b32 v13, v25, v12
	ds_bpermute_b32 v11, v103, v10
	ds_bpermute_b32 v14, v23, v51
	v_mov_b32_e32 v94, v21
	v_mov_b32_e32 v100, v99
	s_waitcnt lgkmcnt(2)
	v_add_f32_e32 v12, v12, v13
	ds_bpermute_b32 v13, v43, v12
	s_waitcnt lgkmcnt(2)
	v_add_f32_e32 v10, v10, v11
	v_mov_b32_e32 v11, v10
	s_nop 1
	v_permlane16_swap_b32_e32 v10, v11
	v_add_f32_e32 v143, v10, v11
	s_waitcnt lgkmcnt(0)
	v_add_f32_e32 v10, v12, v13
	v_add_f32_e32 v12, v51, v14
	ds_bpermute_b32 v11, v103, v10
	ds_bpermute_b32 v13, v25, v12
	ds_bpermute_b32 v14, v23, v47
	v_mov_b32_e32 v96, v95
	v_mov_b32_e32 v102, v101
	s_waitcnt lgkmcnt(2)
	v_add_f32_e32 v10, v10, v11
	s_waitcnt lgkmcnt(1)
	v_add_f32_e32 v11, v12, v13
	ds_bpermute_b32 v12, v43, v11
	v_mov_b32_e32 v13, v10
	s_nop 1
	v_permlane16_swap_b32_e32 v10, v13
	v_add_f32_e32 v51, v10, v13
	s_waitcnt lgkmcnt(0)
	v_add_f32_e32 v10, v11, v12
	ds_bpermute_b32 v11, v103, v10
	ds_bpermute_b32 v12, v23, v49
	v_mov_b32_e32 v108, v107
	v_mov_b32_e32 v116, v115
	v_mov_b32_e32 v106, v104
	s_waitcnt lgkmcnt(1)
	v_add_f32_e32 v10, v10, v11
	s_waitcnt lgkmcnt(0)
	v_add_f32_e32 v11, v49, v12
	v_mov_b32_e32 v13, v10
	ds_bpermute_b32 v12, v25, v11
	s_nop 0
	v_permlane16_swap_b32_e32 v10, v13
	v_add_f32_e32 v141, v10, v13
	v_add_f32_e32 v10, v47, v14
	ds_bpermute_b32 v13, v25, v10
	s_waitcnt lgkmcnt(1)
	v_add_f32_e32 v11, v11, v12
	ds_bpermute_b32 v12, v43, v11
	v_mov_b32_e32 v114, v113
	v_mov_b32_e32 v110, v109
	s_waitcnt lgkmcnt(1)
	v_add_f32_e32 v10, v10, v13
	ds_bpermute_b32 v13, v43, v10
	s_waitcnt lgkmcnt(1)
	v_add_f32_e32 v11, v11, v12
	ds_bpermute_b32 v12, v103, v11
	v_mov_b32_e32 v118, v117
	v_mov_b32_e32 v112, v111
	s_waitcnt lgkmcnt(1)
	v_add_f32_e32 v10, v10, v13
	ds_bpermute_b32 v13, v103, v10
	s_waitcnt lgkmcnt(1)
	v_add_f32_e32 v11, v11, v12
	v_mov_b32_e32 v12, v11
	s_nop 1
	v_permlane16_swap_b32_e32 v11, v12
	s_waitcnt lgkmcnt(0)
	v_add_f32_e32 v10, v10, v13
	v_add_f32_e32 v136, v11, v12
	v_mov_b32_e32 v11, v10
	s_nop 1
	v_permlane16_swap_b32_e32 v10, v11
	v_add_f32_e32 v139, v10, v11
	v_mov_b32_e32 v120, v119
	v_mov_b32_e32 v124, v123
	v_mov_b32_e32 v131, v130
	v_mov_b32_e32 v122, v121
	v_mov_b32_e32 v129, v128
	v_mov_b32_e32 v125, v57
	v_mov_b32_e32 v133, v132
	v_mov_b32_e32 v127, v126
	v_mov_b32_e32 v135, v134
	v_mov_b32_e32 v137, v55
	v_mov_b32_e32 v144, v143
	v_mov_b32_e32 v53, v51
	v_mov_b32_e32 v142, v141
	v_mov_b32_e32 v138, v136
	v_mov_b32_e32 v140, v139
	v_permlane32_swap_b32_e32 v2, v3
	v_permlane32_swap_b32_e32 v4, v5
	v_permlane32_swap_b32_e32 v6, v7
	v_permlane32_swap_b32_e32 v8, v9
	v_permlane32_swap_b32_e32 v19, v20
	v_permlane32_swap_b32_e32 v97, v98
	v_permlane32_swap_b32_e32 v21, v94
	v_permlane32_swap_b32_e32 v99, v100
	v_permlane32_swap_b32_e32 v95, v96
	v_permlane32_swap_b32_e32 v101, v102
	v_permlane32_swap_b32_e32 v107, v108
	v_permlane32_swap_b32_e32 v115, v116
	v_permlane32_swap_b32_e32 v104, v106
	v_permlane32_swap_b32_e32 v113, v114
	v_permlane32_swap_b32_e32 v109, v110
	v_permlane32_swap_b32_e32 v117, v118
	v_permlane32_swap_b32_e32 v111, v112
	v_permlane32_swap_b32_e32 v119, v120
	v_permlane32_swap_b32_e32 v123, v124
	v_permlane32_swap_b32_e32 v130, v131
	v_permlane32_swap_b32_e32 v121, v122
	v_permlane32_swap_b32_e32 v128, v129
	v_permlane32_swap_b32_e32 v57, v125
	v_permlane32_swap_b32_e32 v132, v133
	v_permlane32_swap_b32_e32 v126, v127
	v_permlane32_swap_b32_e32 v134, v135
	v_permlane32_swap_b32_e32 v55, v137
	v_permlane32_swap_b32_e32 v143, v144
	v_permlane32_swap_b32_e32 v51, v53
	v_permlane32_swap_b32_e32 v141, v142
	v_permlane32_swap_b32_e32 v136, v138
	v_permlane32_swap_b32_e32 v139, v140
	s_and_saveexec_b64 s[4:5], s[42:43]
	s_cbranch_execz .LBB0_1299
	v_add_f32_e32 v4, v4, v5
	v_add_f32_e32 v2, v2, v3
	v_cndmask_b32_e64 v2, v2, v4, s[40:41]
	v_mul_f32_e32 v2, 0xbfb8aa3b, v2
	s_load_dwordx2 s[6:7], s[56:57], 0xd0
	v_exp_f32_e32 v2, v2
	v_add_f32_e32 v8, v8, v9
	v_add_f32_e32 v6, v6, v7
	v_cndmask_b32_e64 v49, v6, v8, s[40:41]
	v_add_f32_e32 v2, 1.0, v2
	v_rcp_f32_e32 v18, v2
	s_waitcnt lgkmcnt(0)
	global_load_dwordx4 v[2:5], v1, s[6:7] offset:48
	global_load_dwordx4 v[6:9], v1, s[6:7] offset:32
	global_load_dwordx4 v[10:13], v1, s[6:7] offset:16
	global_load_dwordx4 v[14:17], v1, s[6:7]
	s_mov_b32 s6, 0xf149f2ca
	s_waitcnt vmcnt(0)
	v_add_f32_e32 v47, v18, v14
	v_mul_f32_e32 v14, 0xbfb8aa3b, v49
	v_exp_f32_e32 v14, v14
	v_cmp_nlt_f32_e32 vcc, s6, v47
	v_add_f32_e32 v14, 1.0, v14
	v_rcp_f32_e32 v14, v14
	s_nop 0
	v_add_f32_e32 v49, v14, v15
	v_mov_b32_e32 v15, 0xf149f2ca
	v_cndmask_b32_e32 v145, v47, v15, vcc
	v_cmp_gt_f32_e64 s[44:45], v49, v145
	v_cmp_ngt_f32_e64 s[46:47], v49, v145
	v_mov_b32_e32 v148, v49
	v_mov_b32_e32 v147, v145
	s_and_saveexec_b64 s[6:7], s[46:47]
	s_cbranch_execz .LBB0_1305
	v_mov_b32_e32 v147, 0xf149f2ca
	v_cmp_gt_f32_e64 s[46:47], v49, v147
	s_and_saveexec_b64 s[8:9], s[46:47]
	v_mov_b32_e32 v147, v49
	s_or_b64 exec, exec, s[8:9]
	v_mov_b32_e32 v148, v145

.LBB0_1613:
	s_add_u32 s2, s0, s17
	s_addc_u32 s3, s1, s18
	global_load_dwordx4 v[106:109], v65, s[2:3] nt
	v_add_co_u32_e32 v84, vcc, s13, v80
	v_lshl_add_u64 v[82:83], s[0:1], 0, v[78:79]
	s_nop 0
	v_addc_co_u32_e32 v85, vcc, -1, v81, vcc
	v_add_co_u32_e32 v82, vcc, 0x11100000, v82
	s_add_i32 s15, s15, s66
	s_nop 0
	v_addc_co_u32_e32 v83, vcc, 0, v83, vcc
	global_load_dwordx2 v[110:111], v[82:83], off nt
	global_load_dwordx2 v[112:113], v[82:83], off offset:512 nt
	global_load_dwordx2 v[114:115], v[82:83], off offset:1024 nt
	global_load_dwordx2 v[116:117], v[82:83], off offset:1536 nt
	global_load_dwordx2 v[118:119], v[82:83], off offset:2048 nt
	global_load_dwordx2 v[120:121], v[82:83], off offset:2560 nt
	global_load_dwordx2 v[122:123], v[82:83], off offset:3072 nt
	global_load_dwordx2 v[124:125], v[82:83], off offset:3584 nt
	v_lshl_add_u64 v[78:79], v[78:79], 0, s[94:95]
	s_waitcnt vmcnt(8)
	v_readfirstlane_b32 s2, v106
	v_readfirstlane_b32 s3, v107
	s_lshr_b32 s4, s2, 18
	s_lshl_b32 s2, s2, 11
	s_lshr_b32 s11, s3, 18
	s_and_b32 s19, s4, 0x3ffc
	s_and_b32 s4, s2, 0x7ffff800
	s_and_b32 s2, s11, 0x3ffc
	s_add_i32 s11, s81, s19
	s_add_i32 s2, s81, s2
	v_mov_b32_e32 v105, s11
	v_mov_b32_e32 v139, s2
	ds_read_b32 v138, v105
	ds_read_b32 v140, v139
	s_lshl_b32 s3, s3, 11
	v_pk_mul_f32 v[82:83], v[108:109], s[8:9] op_sel_hi:[1,0]
	s_waitcnt vmcnt(7)
	v_lshlrev_b32_e32 v106, 16, v110
	s_waitcnt lgkmcnt(1)
	v_ashrrev_i32_e32 v139, 31, v138
	s_waitcnt lgkmcnt(0)
	v_ashrrev_i32_e32 v141, 31, v140
	v_lshlrev_b64 v[138:139], 19, v[138:139]
	v_lshlrev_b64 v[140:141], 19, v[140:141]
	v_lshl_add_u64 v[138:139], s[6:7], 0, v[138:139]
	v_lshl_add_u64 v[140:141], s[6:7], 0, v[140:141]
	v_lshl_add_u64 v[138:139], v[138:139], 0, s[4:5]
	s_and_b32 s4, s3, 0x7ffff800
	v_lshl_add_u64 v[140:141], v[140:141], 0, s[4:5]
	v_readfirstlane_b32 s2, v138
	v_readfirstlane_b32 s3, v139
	s_nop 4
	global_load_dword v105, v93, s[2:3] nt
	global_load_dword v139, v93, s[2:3] offset:256 nt
	global_load_dword v143, v93, s[2:3] offset:512 nt
	global_load_dword v145, v93, s[2:3] offset:768 nt
	global_load_dword v147, v93, s[2:3] offset:1024 nt
	global_load_dword v149, v93, s[2:3] offset:1280 nt
	global_load_dword v151, v93, s[2:3] offset:1536 nt
	global_load_dword v153, v93, s[2:3] offset:1792 nt
	v_readfirstlane_b32 s2, v140
	v_readfirstlane_b32 s3, v141
	s_nop 4
	global_load_dword v155, v93, s[2:3] nt
	global_load_dword v157, v93, s[2:3] offset:256 nt
	global_load_dword v159, v93, s[2:3] offset:512 nt
	global_load_dword v167, v93, s[2:3] offset:768 nt
	global_load_dword v175, v93, s[2:3] offset:1024 nt
	global_load_dword v183, v93, s[2:3] offset:1280 nt
	global_load_dword v191, v93, s[2:3] offset:1536 nt
	global_load_dword v199, v93, s[2:3] offset:1792 nt
	v_and_b32_e32 v107, 0xffff0000, v110
	v_lshlrev_b32_e32 v108, 16, v111
	v_and_b32_e32 v109, 0xffff0000, v111
	s_waitcnt vmcnt(22)
	v_lshlrev_b32_e32 v110, 16, v112
	v_and_b32_e32 v111, 0xffff0000, v112
	v_lshlrev_b32_e32 v112, 16, v113
	v_and_b32_e32 v113, 0xffff0000, v113
	s_waitcnt vmcnt(21)
	v_lshlrev_b32_e32 v126, 16, v114
	v_and_b32_e32 v127, 0xffff0000, v114
	v_lshlrev_b32_e32 v114, 16, v115
	v_and_b32_e32 v115, 0xffff0000, v115
	s_waitcnt vmcnt(16)
	v_lshlrev_b32_e32 v136, 16, v124
	v_and_b32_e32 v137, 0xffff0000, v124
	v_lshlrev_b32_e32 v124, 16, v125
	v_and_b32_e32 v125, 0xffff0000, v125
	v_lshlrev_b32_e32 v128, 16, v116
	v_and_b32_e32 v129, 0xffff0000, v116
	v_lshlrev_b32_e32 v116, 16, v117
	v_and_b32_e32 v117, 0xffff0000, v117
	v_lshlrev_b32_e32 v130, 16, v118
	v_and_b32_e32 v131, 0xffff0000, v118
	v_lshlrev_b32_e32 v118, 16, v119
	v_and_b32_e32 v119, 0xffff0000, v119
	v_lshlrev_b32_e32 v132, 16, v120
	v_and_b32_e32 v133, 0xffff0000, v120
	v_lshlrev_b32_e32 v120, 16, v121
	v_and_b32_e32 v121, 0xffff0000, v121
	v_lshlrev_b32_e32 v134, 16, v122
	v_and_b32_e32 v135, 0xffff0000, v122
	v_lshlrev_b32_e32 v122, 16, v123
	v_and_b32_e32 v123, 0xffff0000, v123
	s_add_u32 s17, s17, s68
	s_addc_u32 s18, s18, s69
	s_cmp_ge_i32 s15, s16
	s_waitcnt vmcnt(15)
	v_cvt_f32_fp8_sdwa v140, v105 src0_sel:BYTE_1
	v_cvt_f32_fp8_sdwa v144, v105 src0_sel:BYTE_3
	s_waitcnt vmcnt(14)
	v_cvt_f32_fp8_sdwa v148, v139 src0_sel:BYTE_1
	v_cvt_f32_fp8_sdwa v152, v139 src0_sel:BYTE_3
	s_waitcnt vmcnt(12)
	v_cvt_f32_fp8_e32 v162, v145
	v_cvt_f32_fp8_sdwa v164, v145 src0_sel:BYTE_1
	v_cvt_f32_fp8_sdwa v166, v145 src0_sel:BYTE_2
	v_cvt_f32_fp8_sdwa v168, v145 src0_sel:BYTE_3
	s_waitcnt vmcnt(10)
	v_cvt_f32_fp8_e32 v178, v149
	v_cvt_f32_fp8_sdwa v180, v149 src0_sel:BYTE_1
	v_cvt_f32_fp8_sdwa v182, v149 src0_sel:BYTE_2
	v_cvt_f32_fp8_sdwa v184, v149 src0_sel:BYTE_3
	s_waitcnt vmcnt(8)
	v_cvt_f32_fp8_e32 v194, v153
	v_cvt_f32_fp8_sdwa v196, v153 src0_sel:BYTE_1
	v_cvt_f32_fp8_sdwa v198, v153 src0_sel:BYTE_2
	v_cvt_f32_fp8_sdwa v200, v153 src0_sel:BYTE_3
	s_waitcnt vmcnt(7)
	v_cvt_f32_fp8_e32 v141, v155
	v_cvt_f32_fp8_sdwa v145, v155 src0_sel:BYTE_2
	s_waitcnt vmcnt(6)
	v_cvt_f32_fp8_e32 v149, v157
	v_cvt_f32_fp8_sdwa v153, v157 src0_sel:BYTE_2
	v_cvt_f32_fp8_e32 v138, v105
	v_cvt_f32_fp8_sdwa v142, v105 src0_sel:BYTE_2
	v_cvt_f32_fp8_e32 v146, v139
	v_cvt_f32_fp8_sdwa v150, v139 src0_sel:BYTE_2
	v_cvt_f32_fp8_e32 v154, v143
	v_cvt_f32_fp8_sdwa v156, v143 src0_sel:BYTE_1
	v_cvt_f32_fp8_sdwa v158, v143 src0_sel:BYTE_2
	v_cvt_f32_fp8_sdwa v160, v143 src0_sel:BYTE_3
	v_cvt_f32_fp8_e32 v170, v147
	v_cvt_f32_fp8_sdwa v172, v147 src0_sel:BYTE_1
	v_cvt_f32_fp8_sdwa v174, v147 src0_sel:BYTE_2
	v_cvt_f32_fp8_sdwa v176, v147 src0_sel:BYTE_3
	v_cvt_f32_fp8_e32 v186, v151
	v_cvt_f32_fp8_sdwa v188, v151 src0_sel:BYTE_1
	v_cvt_f32_fp8_sdwa v190, v151 src0_sel:BYTE_2
	v_cvt_f32_fp8_sdwa v192, v151 src0_sel:BYTE_3
	v_cvt_f32_fp8_sdwa v139, v155 src0_sel:BYTE_1
	v_cvt_f32_fp8_sdwa v143, v155 src0_sel:BYTE_3
	v_cvt_f32_fp8_sdwa v147, v157 src0_sel:BYTE_1
	v_cvt_f32_fp8_sdwa v151, v157 src0_sel:BYTE_3
	s_waitcnt vmcnt(5)
	v_cvt_f32_fp8_e32 v157, v159
	v_cvt_f32_fp8_sdwa v161, v159 src0_sel:BYTE_2
	s_waitcnt vmcnt(4)
	v_cvt_f32_fp8_e32 v165, v167
	v_cvt_f32_fp8_sdwa v169, v167 src0_sel:BYTE_2
	s_waitcnt vmcnt(3)
	v_cvt_f32_fp8_e32 v173, v175
	v_cvt_f32_fp8_sdwa v177, v175 src0_sel:BYTE_2
	s_waitcnt vmcnt(2)
	v_cvt_f32_fp8_e32 v181, v183
	v_cvt_f32_fp8_sdwa v185, v183 src0_sel:BYTE_2
	s_waitcnt vmcnt(1)
	v_cvt_f32_fp8_e32 v189, v191
	v_cvt_f32_fp8_sdwa v193, v191 src0_sel:BYTE_2
	s_waitcnt vmcnt(0)
	v_cvt_f32_fp8_e32 v197, v199
	v_cvt_f32_fp8_sdwa v201, v199 src0_sel:BYTE_2
	v_cvt_f32_fp8_sdwa v155, v159 src0_sel:BYTE_1
	v_cvt_f32_fp8_sdwa v159, v159 src0_sel:BYTE_3
	v_cvt_f32_fp8_sdwa v163, v167 src0_sel:BYTE_1
	v_cvt_f32_fp8_sdwa v167, v167 src0_sel:BYTE_3
	v_cvt_f32_fp8_sdwa v171, v175 src0_sel:BYTE_1
	v_cvt_f32_fp8_sdwa v175, v175 src0_sel:BYTE_3
	v_cvt_f32_fp8_sdwa v179, v183 src0_sel:BYTE_1
	v_cvt_f32_fp8_sdwa v183, v183 src0_sel:BYTE_3
	v_cvt_f32_fp8_sdwa v187, v191 src0_sel:BYTE_1
	v_cvt_f32_fp8_sdwa v191, v191 src0_sel:BYTE_3
	v_cvt_f32_fp8_sdwa v195, v199 src0_sel:BYTE_1
	v_cvt_f32_fp8_sdwa v199, v199 src0_sel:BYTE_3
	v_pk_mul_f32 v[140:141], v[82:83], v[140:141]
	v_pk_mul_f32 v[144:145], v[82:83], v[144:145]
	v_pk_mul_f32 v[148:149], v[82:83], v[148:149]
	v_pk_mul_f32 v[152:153], v[82:83], v[152:153]
	v_pk_mul_f32 v[156:157], v[82:83], v[156:157]
	v_pk_mul_f32 v[160:161], v[82:83], v[160:161]
	v_pk_mul_f32 v[164:165], v[82:83], v[164:165]
	v_pk_mul_f32 v[168:169], v[82:83], v[168:169]
	v_pk_mul_f32 v[172:173], v[82:83], v[172:173]
	v_pk_mul_f32 v[176:177], v[82:83], v[176:177]
	v_pk_mul_f32 v[180:181], v[82:83], v[180:181]
	v_pk_mul_f32 v[184:185], v[82:83], v[184:185]
	v_pk_mul_f32 v[188:189], v[82:83], v[188:189]
	v_pk_mul_f32 v[192:193], v[82:83], v[192:193]
	v_pk_mul_f32 v[196:197], v[82:83], v[196:197]
	v_pk_mul_f32 v[200:201], v[82:83], v[200:201]
	v_pk_fma_f32 v[138:139], v[82:83], v[138:139], v[140:141] op_sel:[0,0,1] op_sel_hi:[1,1,0]
	v_pk_fma_f32 v[140:141], v[82:83], v[142:143], v[144:145] op_sel:[0,0,1] op_sel_hi:[1,1,0]
	v_pk_fma_f32 v[142:143], v[82:83], v[146:147], v[148:149] op_sel:[0,0,1] op_sel_hi:[1,1,0]
	v_pk_fma_f32 v[144:145], v[82:83], v[150:151], v[152:153] op_sel:[0,0,1] op_sel_hi:[1,1,0]
	v_pk_fma_f32 v[146:147], v[82:83], v[154:155], v[156:157] op_sel:[0,0,1] op_sel_hi:[1,1,0]
	v_pk_fma_f32 v[148:149], v[82:83], v[158:159], v[160:161] op_sel:[0,0,1] op_sel_hi:[1,1,0]
	v_pk_fma_f32 v[150:151], v[82:83], v[162:163], v[164:165] op_sel:[0,0,1] op_sel_hi:[1,1,0]
	v_pk_fma_f32 v[152:153], v[82:83], v[166:167], v[168:169] op_sel:[0,0,1] op_sel_hi:[1,1,0]
	v_pk_fma_f32 v[154:155], v[82:83], v[170:171], v[172:173] op_sel:[0,0,1] op_sel_hi:[1,1,0]
	v_pk_fma_f32 v[156:157], v[82:83], v[174:175], v[176:177] op_sel:[0,0,1] op_sel_hi:[1,1,0]
	v_pk_fma_f32 v[158:159], v[82:83], v[178:179], v[180:181] op_sel:[0,0,1] op_sel_hi:[1,1,0]
	v_pk_fma_f32 v[160:161], v[82:83], v[182:183], v[184:185] op_sel:[0,0,1] op_sel_hi:[1,1,0]
	v_pk_fma_f32 v[162:163], v[82:83], v[186:187], v[188:189] op_sel:[0,0,1] op_sel_hi:[1,1,0]
	v_pk_fma_f32 v[164:165], v[82:83], v[190:191], v[192:193] op_sel:[0,0,1] op_sel_hi:[1,1,0]
	v_pk_fma_f32 v[166:167], v[82:83], v[194:195], v[196:197] op_sel:[0,0,1] op_sel_hi:[1,1,0]
	v_pk_fma_f32 v[82:83], v[82:83], v[198:199], v[200:201] op_sel:[0,0,1] op_sel_hi:[1,1,0]
	v_pk_fma_f32 v[108:109], v[10:11], v[140:141], v[108:109]
	v_pk_fma_f32 v[106:107], v[8:9], v[138:139], v[106:107]
	v_pk_fma_f32 v[112:113], v[14:15], v[144:145], v[112:113]
	v_pk_fma_f32 v[110:111], v[12:13], v[142:143], v[110:111]
	v_pk_fma_f32 v[114:115], v[26:27], v[148:149], v[114:115]
	v_pk_fma_f32 v[126:127], v[24:25], v[146:147], v[126:127]
	v_pk_fma_f32 v[82:83], v[62:63], v[82:83], v[124:125]
	v_pk_fma_f32 v[124:125], v[60:61], v[166:167], v[136:137]
	v_mul_f32_e32 v105, v107, v107
	v_mul_f32_e32 v136, v109, v109
	v_mul_f32_e32 v137, v111, v111
	v_mul_f32_e32 v138, v113, v113
	v_pk_fma_f32 v[116:117], v[30:31], v[152:153], v[116:117]
	v_pk_fma_f32 v[128:129], v[28:29], v[150:151], v[128:129]
	v_mul_f32_e32 v139, v127, v127
	v_mul_f32_e32 v140, v115, v115
	v_fmac_f32_e32 v105, v106, v106
	v_fmac_f32_e32 v136, v108, v108
	v_fmac_f32_e32 v137, v110, v110
	v_fmac_f32_e32 v138, v112, v112
	v_pk_fma_f32 v[118:119], v[42:43], v[156:157], v[118:119]
	v_pk_fma_f32 v[130:131], v[40:41], v[154:155], v[130:131]
	v_mul_f32_e32 v141, v129, v129
	v_mul_f32_e32 v142, v117, v117
	v_fmac_f32_e32 v139, v126, v126
	v_fmac_f32_e32 v140, v114, v114
	v_add_f32_e32 v105, v105, v136
	v_add_f32_e32 v136, v137, v138
	v_pk_fma_f32 v[120:121], v[46:47], v[160:161], v[120:121]
	v_pk_fma_f32 v[132:133], v[44:45], v[158:159], v[132:133]
	v_mul_f32_e32 v143, v131, v131
	v_mul_f32_e32 v144, v119, v119
	v_fmac_f32_e32 v141, v128, v128
	v_fmac_f32_e32 v142, v116, v116
	v_add_f32_e32 v137, v139, v140
	v_add_f32_e32 v105, v105, v136
	v_pk_fma_f32 v[122:123], v[58:59], v[164:165], v[122:123]
	v_pk_fma_f32 v[134:135], v[56:57], v[162:163], v[134:135]
	v_mul_f32_e32 v145, v133, v133
	v_mul_f32_e32 v146, v121, v121
	v_fmac_f32_e32 v143, v130, v130
	v_fmac_f32_e32 v144, v118, v118
	v_add_f32_e32 v138, v141, v142
	v_add_f32_e32 v105, v105, v137
	v_mul_f32_e32 v147, v135, v135
	v_mul_f32_e32 v148, v123, v123
	v_fmac_f32_e32 v145, v132, v132
	v_fmac_f32_e32 v146, v120, v120
	v_add_f32_e32 v139, v143, v144
	v_add_f32_e32 v105, v105, v138
	v_mul_f32_e32 v149, v125, v125
	v_mul_f32_e32 v150, v83, v83
	v_fmac_f32_e32 v147, v134, v134
	v_fmac_f32_e32 v148, v122, v122
	v_add_f32_e32 v140, v145, v146
	v_add_f32_e32 v105, v105, v139
	v_fmac_f32_e32 v149, v124, v124
	v_fmac_f32_e32 v150, v82, v82
	v_add_f32_e32 v141, v147, v148
	v_add_f32_e32 v105, v105, v140
	v_add_f32_e32 v142, v149, v150
	v_add_f32_e32 v105, v105, v141
	v_add_f32_e32 v105, v105, v142
	ds_bpermute_b32 v136, v101, v105
	s_waitcnt lgkmcnt(0)
	v_add_f32_e32 v105, v105, v136
	ds_bpermute_b32 v136, v102, v105
	s_waitcnt lgkmcnt(0)
	v_add_f32_e32 v105, v105, v136
	ds_bpermute_b32 v136, v103, v105
	s_waitcnt lgkmcnt(0)
	v_add_f32_e32 v105, v105, v136
	ds_bpermute_b32 v136, v104, v105
	s_waitcnt lgkmcnt(0)
	v_add_f32_e32 v105, v105, v136
	v_mov_b32_e32 v136, v105
	s_nop 1
	v_permlane16_swap_b32_e32 v105, v136
	v_add_f32_e32 v105, v105, v136
	v_mov_b32_e32 v136, v105
	s_nop 1
	v_permlane32_swap_b32_e32 v105, v136
	v_add_f32_e32 v105, v105, v136
	v_fmamk_f32 v105, v105, 0x3a000000, v94
	v_mul_f32_e32 v136, 0x4f800000, v105
	v_cmp_gt_f32_e32 vcc, s12, v105
	s_nop 1
	v_cndmask_b32_e32 v105, v105, v136, vcc
	v_sqrt_f32_e32 v136, v105
	s_nop 0
	v_add_u32_e32 v137, -1, v136
	v_add_u32_e32 v138, 1, v136
	v_fma_f32 v139, -v137, v136, v105
	v_fma_f32 v140, -v138, v136, v105
	v_cmp_ge_f32_e64 s[2:3], 0, v139
	s_nop 1
	v_cndmask_b32_e64 v136, v136, v137, s[2:3]
	v_cmp_lt_f32_e64 s[2:3], 0, v140
	s_nop 1
	v_cndmask_b32_e64 v136, v136, v138, s[2:3]
	v_mul_f32_e32 v137, 0x37800000, v136
	v_cndmask_b32_e32 v136, v136, v137, vcc
	v_cmp_class_f32_e32 vcc, v105, v95
	s_nop 1
	v_cndmask_b32_e32 v105, v136, v105, vcc
	v_div_scale_f32 v136, s[2:3], v105, v105, 1.0
	v_rcp_f32_e32 v138, v136
	v_div_scale_f32 v137, vcc, 1.0, v105, 1.0
	v_fma_f32 v139, -v136, v138, 1.0
	v_fmac_f32_e32 v138, v139, v138
	v_mul_f32_e32 v139, v137, v138
	v_fma_f32 v140, -v136, v139, v137
	v_fmac_f32_e32 v139, v140, v138
	v_fma_f32 v136, -v136, v139, v137
	v_div_fmas_f32 v136, v136, v138, v139
	v_div_fixup_f32 v136, v136, v105, 1.0
	v_pk_mul_f32 v[106:107], v[106:107], v[136:137] op_sel_hi:[1,0]
	v_pk_mul_f32 v[108:109], v[108:109], v[136:137] op_sel_hi:[1,0]
	v_pk_mul_f32 v[110:111], v[110:111], v[136:137] op_sel_hi:[1,0]
	v_pk_mul_f32 v[112:113], v[112:113], v[136:137] op_sel_hi:[1,0]
	v_pk_mul_f32 v[126:127], v[126:127], v[136:137] op_sel_hi:[1,0]
	v_pk_mul_f32 v[114:115], v[114:115], v[136:137] op_sel_hi:[1,0]
	v_pk_mul_f32 v[128:129], v[128:129], v[136:137] op_sel_hi:[1,0]
	v_pk_mul_f32 v[138:139], v[116:117], v[136:137] op_sel_hi:[1,0]
	v_pk_mul_f32 v[130:131], v[130:131], v[136:137] op_sel_hi:[1,0]
	v_pk_mul_f32 v[140:141], v[118:119], v[136:137] op_sel_hi:[1,0]
	v_pk_mul_f32 v[132:133], v[132:133], v[136:137] op_sel_hi:[1,0]
	v_pk_mul_f32 v[142:143], v[120:121], v[136:137] op_sel_hi:[1,0]
	v_pk_mul_f32 v[134:135], v[134:135], v[136:137] op_sel_hi:[1,0]
	v_pk_mul_f32 v[144:145], v[122:123], v[136:137] op_sel_hi:[1,0]
	v_pk_mul_f32 v[146:147], v[124:125], v[136:137] op_sel_hi:[1,0]
	v_pk_mul_f32 v[82:83], v[82:83], v[136:137] op_sel_hi:[1,0]
	v_pk_mul_f32 v[108:109], v[2:3], v[108:109]
	v_pk_mul_f32 v[106:107], v[0:1], v[106:107]
	v_pk_mul_f32 v[112:113], v[6:7], v[112:113]
	v_pk_mul_f32 v[110:111], v[4:5], v[110:111]
	v_pk_mul_f32 v[116:117], v[18:19], v[114:115]
	v_pk_mul_f32 v[114:115], v[16:17], v[126:127]
	v_pk_mul_f32 v[120:121], v[22:23], v[138:139]
	v_pk_mul_f32 v[118:119], v[20:21], v[128:129]
	v_pk_mul_f32 v[124:125], v[34:35], v[140:141]
	v_pk_mul_f32 v[122:123], v[32:33], v[130:131]
	v_pk_mul_f32 v[128:129], v[38:39], v[142:143]
	v_pk_mul_f32 v[126:127], v[36:37], v[132:133]
	v_pk_mul_f32 v[132:133], v[50:51], v[144:145]
	v_pk_mul_f32 v[130:131], v[48:49], v[134:135]
	v_pk_mul_f32 v[136:137], v[54:55], v[82:83]
	v_pk_mul_f32 v[134:135], v[52:53], v[146:147]
	global_store_dwordx4 v[84:85], v[106:109], off offset:-3072 sc1
	global_store_dwordx4 v[84:85], v[110:113], off offset:-2048 sc1
	global_store_dwordx4 v[84:85], v[114:117], off offset:-1024 sc1
	global_store_dwordx4 v[80:81], v[118:121], off offset:-4096 sc1
	global_store_dwordx4 v[80:81], v[122:125], off offset:-3072 sc1
	global_store_dwordx4 v[80:81], v[126:129], off offset:-2048 sc1
	global_store_dwordx4 v[80:81], v[130:133], off offset:-1024 sc1
	global_store_dwordx4 v[80:81], v[134:137], off sc1
	v_lshl_add_u64 v[80:81], v[80:81], 0, s[24:25]
	s_cbranch_scc0 .LBB0_1613
	s_branch .LBB0_1610
